# v58 + counted waits: 66 single-counter s_waitcnt already implied by an earlier wait removed kernel-wide (vmcnt 7/6/5/4 ladders behind vmcnt(4) in the K/V write blocks, lgkmcnt(0) twins, P0 ladder)
# speedup vs baseline: 1.0058x; 1.0014x over previous
.LBB0_168:
	s_and_b32 s2, s37, 0x7ffff800
	s_add_i32 s2, s2, s33
	s_ashr_i32 s10, s2, 31
	s_lshr_b32 s10, s10, 28
	s_add_i32 s10, s2, s10
	s_ashr_i32 s11, s10, 4
	s_mul_hi_i32 s12, s11, 0x2aaaaaab
	s_lshr_b32 s13, s12, 31
	s_lshr_b32 s12, s12, 3
	s_and_b32 s10, s10, -16
	s_add_i32 s12, s12, s13
	s_sub_i32 s10, s2, s10
	s_mul_i32 s12, s12, 48
	s_mul_hi_i32 s2, s2, 0x2aaaaaab
	s_sub_i32 s40, s11, s12
	s_lshr_b32 s11, s2, 31
	s_ashr_i32 s2, s2, 7
	s_add_i32 s12, s2, s11
	s_and_b32 s11, s39, 6
	s_ashr_i32 s13, s12, 31
	s_lshl_b32 s41, s10, 7
	s_lshl_b32 s2, s11, 4
	s_lshl_b64 s[14:15], s[12:13], 11
	s_ashr_i32 s42, s41, 31
	s_add_u32 s14, s14, s41
	s_addc_u32 s15, s15, s42
	s_or_b32 s2, s2, s14
	s_or_b32 s2, s2, 16
	s_mul_i32 s15, s15, 0xc000
	s_mul_hi_u32 s14, s2, 0xc000
	s_add_i32 s14, s14, s15
	s_mul_i32 s2, s2, 0xc000
	s_add_u32 s2, s8, s2
	s_addc_u32 s42, s9, s14
	s_lshl_b32 s14, s40, 8
	s_ashr_i32 s15, s14, 31
	s_lshl_b64 s[40:41], s[14:15], 2
	s_add_u32 s40, s2, s40
	s_addc_u32 s41, s42, s41
	v_lshl_add_u64 v[32:33], s[40:41], 0, v[178:179]
	v_add_co_u32_e32 v34, vcc, s17, v32
	s_and_b32 s2, s38, 0x60
	s_nop 0
	v_addc_co_u32_e32 v35, vcc, 0, v33, vcc
	v_add_co_u32_e32 v36, vcc, s36, v32
	s_lshl_b32 s2, s2, 2
	s_nop 0
	v_addc_co_u32_e32 v37, vcc, 0, v33, vcc
	v_add_co_u32_e32 v38, vcc, s35, v32
	s_add_i32 s39, s39, 2
	s_nop 0
	v_addc_co_u32_e32 v39, vcc, 0, v33, vcc
	v_add_co_u32_e32 v40, vcc, s34, v32
	s_nop 1
	v_addc_co_u32_e32 v41, vcc, 0, v33, vcc
	v_add_co_u32_e32 v42, vcc, s31, v32
	s_nop 1
	v_addc_co_u32_e32 v43, vcc, 0, v33, vcc
	v_add_co_u32_e32 v44, vcc, s30, v32
	s_nop 1
	v_addc_co_u32_e32 v45, vcc, 0, v33, vcc
	v_add_co_u32_e32 v46, vcc, s29, v32
	s_nop 1
	v_addc_co_u32_e32 v47, vcc, 0, v33, vcc
	v_add_co_u32_e32 v64, vcc, s28, v32
	s_nop 1
	v_addc_co_u32_e32 v65, vcc, 0, v33, vcc
	v_add_co_u32_e32 v66, vcc, s27, v32
	s_nop 1
	v_addc_co_u32_e32 v67, vcc, 0, v33, vcc
	v_add_co_u32_e32 v76, vcc, s26, v32
	s_nop 1
	v_addc_co_u32_e32 v77, vcc, 0, v33, vcc
	v_add_co_u32_e32 v124, vcc, s25, v32
	s_nop 1
	v_addc_co_u32_e32 v125, vcc, 0, v33, vcc
	v_add_co_u32_e32 v126, vcc, s24, v32
	s_nop 1
	v_addc_co_u32_e32 v127, vcc, 0, v33, vcc
	v_add_co_u32_e32 v164, vcc, s23, v32
	s_nop 1
	v_addc_co_u32_e32 v165, vcc, 0, v33, vcc
	v_add_co_u32_e32 v166, vcc, s22, v32
	s_nop 1
	v_addc_co_u32_e32 v167, vcc, 0, v33, vcc
	v_add_co_u32_e32 v32, vcc, s21, v32
	s_nop 1
	v_addc_co_u32_e32 v33, vcc, 0, v33, vcc
	global_load_dwordx4 v[120:123], v[34:35], off nt
	global_load_dwordx4 v[116:119], v[36:37], off nt
	global_load_dwordx4 v[112:115], v[38:39], off nt
	global_load_dwordx4 v[108:111], v[40:41], off nt
	global_load_dwordx4 v[104:107], v[42:43], off nt
	global_load_dwordx4 v[100:103], v[44:45], off nt
	global_load_dwordx4 v[96:99], v[46:47], off nt
	global_load_dwordx4 v[92:95], v[64:65], off nt
	global_load_dwordx4 v[80:83], v[66:67], off nt
	s_nop 0
	global_load_dwordx4 v[76:79], v[76:77], off nt
	s_nop 0
	global_load_dwordx4 v[64:67], v[124:125], off nt
	global_load_dwordx4 v[44:47], v[126:127], off nt
	global_load_dwordx4 v[40:43], v[164:165], off nt
	global_load_dwordx4 v[36:39], v[166:167], off nt
	s_nop 0
	global_load_dwordx4 v[32:35], v[32:33], off nt
	s_nop 0
	global_load_dwordx4 v[124:127], v178, s[40:41] nt
	s_lshl_b32 s40, s10, 9
	s_add_i32 s40, s40, 0
	s_add_i32 s2, s40, s2
	v_mov_b32_e32 v188, s2
	ds_read_b128 v[168:171], v188
	ds_read_b128 v[164:167], v188 offset:16
	ds_read_b128 v[172:175], v188 offset:8192
	s_add_i32 s41, s2, 0x10000
	s_waitcnt vmcnt(16) lgkmcnt(2)
	v_pk_fma_f32 v[182:183], v[74:75], v[168:169], v[162:163] op_sel_hi:[1,0,1]
	v_pk_fma_f32 v[184:185], v[72:73], v[168:169], v[160:161] op_sel_hi:[1,0,1]
	ds_read_b128 v[160:163], v188 offset:8208
	ds_read_b128 v[190:193], v188 offset:16384
	s_waitcnt lgkmcnt(2)
	v_pk_fma_f32 v[218:219], v[74:75], v[172:173], v[158:159] op_sel_hi:[1,0,1]
	v_pk_fma_f32 v[220:221], v[72:73], v[172:173], v[156:157] op_sel_hi:[1,0,1]
	ds_read_b128 v[156:159], v188 offset:16400
	ds_read_b128 v[194:197], v188 offset:24576
	s_waitcnt lgkmcnt(2)
	v_pk_fma_f32 v[222:223], v[74:75], v[190:191], v[154:155] op_sel_hi:[1,0,1]
	v_pk_fma_f32 v[224:225], v[72:73], v[190:191], v[152:153] op_sel_hi:[1,0,1]
	ds_read_b128 v[152:155], v188 offset:24592
	ds_read_b128 v[198:201], v188 offset:32768
	s_waitcnt lgkmcnt(2)
	v_pk_fma_f32 v[226:227], v[74:75], v[194:195], v[150:151] op_sel_hi:[1,0,1]
	v_pk_fma_f32 v[228:229], v[72:73], v[194:195], v[148:149] op_sel_hi:[1,0,1]
	ds_read_b128 v[148:151], v188 offset:32784
	ds_read_b128 v[202:205], v188 offset:40960
	s_waitcnt lgkmcnt(2)
	v_pk_fma_f32 v[230:231], v[74:75], v[198:199], v[146:147] op_sel_hi:[1,0,1]
	v_pk_fma_f32 v[232:233], v[72:73], v[198:199], v[144:145] op_sel_hi:[1,0,1]
	ds_read_b128 v[144:147], v188 offset:40976
	ds_read_b128 v[206:209], v188 offset:49152
	s_waitcnt lgkmcnt(2)
	v_pk_fma_f32 v[234:235], v[74:75], v[202:203], v[142:143] op_sel_hi:[1,0,1]
	v_pk_fma_f32 v[236:237], v[72:73], v[202:203], v[140:141] op_sel_hi:[1,0,1]
	ds_read_b128 v[140:143], v188 offset:57344
	ds_read_b128 v[210:213], v188 offset:49168
	s_waitcnt lgkmcnt(2)
	v_pk_fma_f32 v[240:241], v[72:73], v[206:207], v[136:137] op_sel_hi:[1,0,1]
	v_pk_fma_f32 v[238:239], v[74:75], v[206:207], v[138:139] op_sel_hi:[1,0,1]
	s_waitcnt lgkmcnt(1)
	v_pk_fma_f32 v[242:243], v[74:75], v[140:141], v[134:135] op_sel_hi:[1,0,1]
	v_mov_b32_e32 v134, s41
	ds_read_b128 v[214:217], v134
	v_pk_fma_f32 v[244:245], v[72:73], v[140:141], v[132:133] op_sel_hi:[1,0,1]
	s_add_i32 s41, s2, 0x10010
	v_mov_b32_e32 v132, s41
	ds_read_b128 v[136:139], v188 offset:57360
	ds_read_b128 v[132:135], v132
	s_waitcnt lgkmcnt(2)
	v_pk_fma_f32 v[72:73], v[72:73], v[214:215], v[128:129] op_sel_hi:[1,0,1]
	v_pk_fma_f32 v[74:75], v[74:75], v[214:215], v[130:131] op_sel_hi:[1,0,1]
	v_pk_fma_f32 v[128:129], v[84:85], v[168:169], v[184:185] op_sel:[0,1,0]
	v_pk_fma_f32 v[130:131], v[86:87], v[168:169], v[182:183] op_sel:[0,1,0]
	v_pk_fma_f32 v[168:169], v[84:85], v[172:173], v[220:221] op_sel:[0,1,0]
	v_pk_fma_f32 v[172:173], v[86:87], v[172:173], v[218:219] op_sel:[0,1,0]
	v_pk_fma_f32 v[182:183], v[84:85], v[190:191], v[224:225] op_sel:[0,1,0]
	v_pk_fma_f32 v[184:185], v[86:87], v[190:191], v[222:223] op_sel:[0,1,0]
	v_pk_fma_f32 v[190:191], v[84:85], v[194:195], v[228:229] op_sel:[0,1,0]
	v_pk_fma_f32 v[194:195], v[86:87], v[194:195], v[226:227] op_sel:[0,1,0]
	v_pk_fma_f32 v[218:219], v[84:85], v[198:199], v[232:233] op_sel:[0,1,0]
	v_pk_fma_f32 v[198:199], v[86:87], v[198:199], v[230:231] op_sel:[0,1,0]
	v_pk_fma_f32 v[220:221], v[84:85], v[202:203], v[236:237] op_sel:[0,1,0]
	v_pk_fma_f32 v[202:203], v[86:87], v[202:203], v[234:235] op_sel:[0,1,0]
	v_pk_fma_f32 v[222:223], v[84:85], v[206:207], v[240:241] op_sel:[0,1,0]
	v_pk_fma_f32 v[224:225], v[84:85], v[140:141], v[244:245] op_sel:[0,1,0]
	v_pk_fma_f32 v[72:73], v[84:85], v[214:215], v[72:73] op_sel:[0,1,0]
	v_pk_fma_f32 v[206:207], v[86:87], v[206:207], v[238:239] op_sel:[0,1,0]
	v_pk_fma_f32 v[140:141], v[86:87], v[140:141], v[242:243] op_sel:[0,1,0]
	v_pk_fma_f32 v[74:75], v[86:87], v[214:215], v[74:75] op_sel:[0,1,0]
	v_pk_fma_f32 v[84:85], v[90:91], v[170:171], v[130:131] op_sel_hi:[1,0,1]
	v_pk_fma_f32 v[86:87], v[88:89], v[170:171], v[128:129] op_sel_hi:[1,0,1]
	v_pk_fma_f32 v[128:129], v[90:91], v[174:175], v[172:173] op_sel_hi:[1,0,1]
	v_pk_fma_f32 v[130:131], v[88:89], v[174:175], v[168:169] op_sel_hi:[1,0,1]
	v_pk_fma_f32 v[168:169], v[90:91], v[192:193], v[184:185] op_sel_hi:[1,0,1]
	v_pk_fma_f32 v[172:173], v[88:89], v[192:193], v[182:183] op_sel_hi:[1,0,1]
	v_pk_fma_f32 v[182:183], v[90:91], v[196:197], v[194:195] op_sel_hi:[1,0,1]
	v_pk_fma_f32 v[184:185], v[88:89], v[196:197], v[190:191] op_sel_hi:[1,0,1]
	v_pk_fma_f32 v[190:191], v[90:91], v[200:201], v[198:199] op_sel_hi:[1,0,1]
	v_pk_fma_f32 v[194:195], v[88:89], v[200:201], v[218:219] op_sel_hi:[1,0,1]
	v_pk_fma_f32 v[198:199], v[90:91], v[204:205], v[202:203] op_sel_hi:[1,0,1]
	v_pk_fma_f32 v[202:203], v[88:89], v[204:205], v[220:221] op_sel_hi:[1,0,1]
	v_pk_fma_f32 v[214:215], v[88:89], v[208:209], v[222:223] op_sel_hi:[1,0,1]
	v_pk_fma_f32 v[218:219], v[88:89], v[142:143], v[224:225] op_sel_hi:[1,0,1]
	v_pk_fma_f32 v[72:73], v[88:89], v[216:217], v[72:73] op_sel_hi:[1,0,1]
	v_mov_b32_e32 v88, v171
	v_pk_fma_f32 v[86:87], v[68:69], v[88:89], v[86:87] op_sel_hi:[1,0,1]
	v_pk_fma_f32 v[84:85], v[70:71], v[88:89], v[84:85] op_sel_hi:[1,0,1]
	v_mov_b32_e32 v88, v175
	v_pk_fma_f32 v[206:207], v[90:91], v[208:209], v[206:207] op_sel_hi:[1,0,1]
	v_pk_fma_f32 v[140:141], v[90:91], v[142:143], v[140:141] op_sel_hi:[1,0,1]
	v_pk_fma_f32 v[74:75], v[90:91], v[216:217], v[74:75] op_sel_hi:[1,0,1]
	v_pk_fma_f32 v[90:91], v[68:69], v[88:89], v[130:131] op_sel_hi:[1,0,1]
	v_pk_fma_f32 v[88:89], v[70:71], v[88:89], v[128:129] op_sel_hi:[1,0,1]
	v_mov_b32_e32 v128, v193
	v_mov_b32_e32 v142, v197
	v_pk_fma_f32 v[130:131], v[68:69], v[128:129], v[172:173] op_sel_hi:[1,0,1]
	v_pk_fma_f32 v[128:129], v[70:71], v[128:129], v[168:169] op_sel_hi:[1,0,1]
	v_pk_fma_f32 v[168:169], v[68:69], v[142:143], v[184:185] op_sel_hi:[1,0,1]
	v_pk_fma_f32 v[170:171], v[70:71], v[142:143], v[182:183] op_sel_hi:[1,0,1]
	v_mov_b32_e32 v142, v201
	v_pk_fma_f32 v[172:173], v[68:69], v[142:143], v[194:195] op_sel_hi:[1,0,1]
	v_pk_fma_f32 v[174:175], v[70:71], v[142:143], v[190:191] op_sel_hi:[1,0,1]
	v_mov_b32_e32 v142, v205
	v_pk_fma_f32 v[182:183], v[68:69], v[142:143], v[202:203] op_sel_hi:[1,0,1]
	v_pk_fma_f32 v[184:185], v[70:71], v[142:143], v[198:199] op_sel_hi:[1,0,1]
	v_mov_b32_e32 v142, v209
	v_pk_fma_f32 v[190:191], v[68:69], v[142:143], v[214:215] op_sel_hi:[1,0,1]
	v_pk_fma_f32 v[192:193], v[70:71], v[142:143], v[206:207] op_sel_hi:[1,0,1]
	v_mov_b32_e32 v142, v143
	v_pk_fma_f32 v[194:195], v[68:69], v[142:143], v[218:219] op_sel_hi:[1,0,1]
	v_pk_fma_f32 v[140:141], v[70:71], v[142:143], v[140:141] op_sel_hi:[1,0,1]
	v_mov_b32_e32 v142, v217
	v_pk_fma_f32 v[68:69], v[68:69], v[142:143], v[72:73] op_sel_hi:[1,0,1]
	v_pk_fma_f32 v[70:71], v[70:71], v[142:143], v[74:75] op_sel_hi:[1,0,1]
	v_pk_fma_f32 v[72:73], v[62:63], v[164:165], v[84:85] op_sel_hi:[1,0,1]
	v_pk_fma_f32 v[74:75], v[60:61], v[164:165], v[86:87] op_sel_hi:[1,0,1]
	v_pk_fma_f32 v[84:85], v[62:63], v[160:161], v[88:89] op_sel_hi:[1,0,1]
	v_pk_fma_f32 v[86:87], v[60:61], v[160:161], v[90:91] op_sel_hi:[1,0,1]
	v_pk_fma_f32 v[88:89], v[62:63], v[156:157], v[128:129] op_sel_hi:[1,0,1]
	v_pk_fma_f32 v[90:91], v[60:61], v[156:157], v[130:131] op_sel_hi:[1,0,1]
	v_pk_fma_f32 v[128:129], v[62:63], v[152:153], v[170:171] op_sel_hi:[1,0,1]
	v_pk_fma_f32 v[130:131], v[60:61], v[152:153], v[168:169] op_sel_hi:[1,0,1]
	v_pk_fma_f32 v[142:143], v[62:63], v[148:149], v[174:175] op_sel_hi:[1,0,1]
	v_pk_fma_f32 v[168:169], v[60:61], v[148:149], v[172:173] op_sel_hi:[1,0,1]
	v_pk_fma_f32 v[170:171], v[62:63], v[144:145], v[184:185] op_sel_hi:[1,0,1]
	v_pk_fma_f32 v[172:173], v[60:61], v[144:145], v[182:183] op_sel_hi:[1,0,1]
	v_pk_fma_f32 v[182:183], v[60:61], v[210:211], v[190:191] op_sel_hi:[1,0,1]
	s_waitcnt lgkmcnt(1)
	v_pk_fma_f32 v[184:185], v[60:61], v[136:137], v[194:195] op_sel_hi:[1,0,1]
	s_waitcnt lgkmcnt(0)
	v_pk_fma_f32 v[60:61], v[60:61], v[132:133], v[68:69] op_sel_hi:[1,0,1]
	v_pk_fma_f32 v[174:175], v[62:63], v[210:211], v[192:193] op_sel_hi:[1,0,1]
	v_pk_fma_f32 v[140:141], v[62:63], v[136:137], v[140:141] op_sel_hi:[1,0,1]
	v_pk_fma_f32 v[62:63], v[62:63], v[132:133], v[70:71] op_sel_hi:[1,0,1]
	v_pk_fma_f32 v[68:69], v[56:57], v[164:165], v[74:75] op_sel:[0,1,0]
	v_pk_fma_f32 v[70:71], v[58:59], v[164:165], v[72:73] op_sel:[0,1,0]
	v_pk_fma_f32 v[72:73], v[56:57], v[160:161], v[86:87] op_sel:[0,1,0]
	v_pk_fma_f32 v[74:75], v[58:59], v[160:161], v[84:85] op_sel:[0,1,0]
	v_pk_fma_f32 v[84:85], v[56:57], v[156:157], v[90:91] op_sel:[0,1,0]
	v_pk_fma_f32 v[86:87], v[58:59], v[156:157], v[88:89] op_sel:[0,1,0]
	v_pk_fma_f32 v[88:89], v[56:57], v[152:153], v[130:131] op_sel:[0,1,0]
	v_pk_fma_f32 v[90:91], v[58:59], v[152:153], v[128:129] op_sel:[0,1,0]
	v_pk_fma_f32 v[128:129], v[56:57], v[148:149], v[168:169] op_sel:[0,1,0]
	v_pk_fma_f32 v[130:131], v[58:59], v[148:149], v[142:143] op_sel:[0,1,0]
	v_pk_fma_f32 v[142:143], v[56:57], v[144:145], v[172:173] op_sel:[0,1,0]
	v_pk_fma_f32 v[148:149], v[56:57], v[210:211], v[182:183] op_sel:[0,1,0]
	v_pk_fma_f32 v[156:157], v[56:57], v[136:137], v[184:185] op_sel:[0,1,0]
	v_pk_fma_f32 v[56:57], v[56:57], v[132:133], v[60:61] op_sel:[0,1,0]
	v_pk_fma_f32 v[144:145], v[58:59], v[144:145], v[170:171] op_sel:[0,1,0]
	v_pk_fma_f32 v[152:153], v[58:59], v[210:211], v[174:175] op_sel:[0,1,0]
	v_pk_fma_f32 v[136:137], v[58:59], v[136:137], v[140:141] op_sel:[0,1,0]
	v_pk_fma_f32 v[58:59], v[58:59], v[132:133], v[62:63] op_sel:[0,1,0]
	v_pk_fma_f32 v[60:61], v[54:55], v[166:167], v[70:71] op_sel_hi:[1,0,1]
	v_pk_fma_f32 v[62:63], v[52:53], v[166:167], v[68:69] op_sel_hi:[1,0,1]
	v_pk_fma_f32 v[68:69], v[54:55], v[162:163], v[74:75] op_sel_hi:[1,0,1]
	v_pk_fma_f32 v[70:71], v[52:53], v[162:163], v[72:73] op_sel_hi:[1,0,1]
	v_pk_fma_f32 v[72:73], v[54:55], v[158:159], v[86:87] op_sel_hi:[1,0,1]
	v_pk_fma_f32 v[74:75], v[52:53], v[158:159], v[84:85] op_sel_hi:[1,0,1]
	v_pk_fma_f32 v[84:85], v[54:55], v[154:155], v[90:91] op_sel_hi:[1,0,1]
	v_pk_fma_f32 v[86:87], v[52:53], v[154:155], v[88:89] op_sel_hi:[1,0,1]
	v_pk_fma_f32 v[88:89], v[54:55], v[150:151], v[130:131] op_sel_hi:[1,0,1]
	v_pk_fma_f32 v[90:91], v[52:53], v[150:151], v[128:129] op_sel_hi:[1,0,1]
	v_pk_fma_f32 v[130:131], v[52:53], v[146:147], v[142:143] op_sel_hi:[1,0,1]
	v_pk_fma_f32 v[140:141], v[52:53], v[212:213], v[148:149] op_sel_hi:[1,0,1]
	v_pk_fma_f32 v[142:143], v[52:53], v[138:139], v[156:157] op_sel_hi:[1,0,1]
	v_pk_fma_f32 v[56:57], v[52:53], v[134:135], v[56:57] op_sel_hi:[1,0,1]
	v_mov_b32_e32 v52, v167
	v_pk_fma_f32 v[128:129], v[54:55], v[146:147], v[144:145] op_sel_hi:[1,0,1]
	v_pk_fma_f32 v[144:145], v[48:49], v[52:53], v[62:63] op_sel_hi:[1,0,1]
	v_pk_fma_f32 v[148:149], v[50:51], v[52:53], v[60:61] op_sel_hi:[1,0,1]
	v_mov_b32_e32 v52, v163
	v_pk_fma_f32 v[132:133], v[54:55], v[212:213], v[152:153] op_sel_hi:[1,0,1]
	v_pk_fma_f32 v[152:153], v[48:49], v[52:53], v[70:71] op_sel_hi:[1,0,1]
	v_pk_fma_f32 v[156:157], v[50:51], v[52:53], v[68:69] op_sel_hi:[1,0,1]
	v_mov_b32_e32 v52, v159
	v_pk_fma_f32 v[158:159], v[48:49], v[52:53], v[74:75] op_sel_hi:[1,0,1]
	v_pk_fma_f32 v[160:161], v[50:51], v[52:53], v[72:73] op_sel_hi:[1,0,1]
	v_mov_b32_e32 v52, v155
	v_pk_fma_f32 v[154:155], v[48:49], v[52:53], v[86:87] op_sel_hi:[1,0,1]
	v_pk_fma_f32 v[162:163], v[50:51], v[52:53], v[84:85] op_sel_hi:[1,0,1]
	v_mov_b32_e32 v52, v151
	v_pk_fma_f32 v[150:151], v[48:49], v[52:53], v[90:91] op_sel_hi:[1,0,1]
	v_pk_fma_f32 v[164:165], v[50:51], v[52:53], v[88:89] op_sel_hi:[1,0,1]
	v_mov_b32_e32 v52, v147
	v_pk_fma_f32 v[166:167], v[48:49], v[52:53], v[130:131] op_sel_hi:[1,0,1]
	v_pk_fma_f32 v[168:169], v[50:51], v[52:53], v[128:129] op_sel_hi:[1,0,1]
	v_mov_b32_e32 v52, v213
	v_pk_fma_f32 v[136:137], v[54:55], v[138:139], v[136:137] op_sel_hi:[1,0,1]
	v_pk_fma_f32 v[58:59], v[54:55], v[134:135], v[58:59] op_sel_hi:[1,0,1]
	v_pk_fma_f32 v[170:171], v[48:49], v[52:53], v[140:141] op_sel_hi:[1,0,1]
	v_pk_fma_f32 v[172:173], v[50:51], v[52:53], v[132:133] op_sel_hi:[1,0,1]
	v_mov_b32_e32 v52, v139
	v_mov_b32_e32 v68, v135
	v_pk_fma_f32 v[60:61], v[48:49], v[52:53], v[142:143] op_sel_hi:[1,0,1]
	v_pk_fma_f32 v[70:71], v[50:51], v[52:53], v[136:137] op_sel_hi:[1,0,1]
	ds_read_b128 v[52:55], v188 offset:32
	v_pk_fma_f32 v[62:63], v[48:49], v[68:69], v[56:57] op_sel_hi:[1,0,1]
	v_pk_fma_f32 v[68:69], v[50:51], v[68:69], v[58:59] op_sel_hi:[1,0,1]
	ds_read_b128 v[48:51], v188 offset:48
	ds_read_b128 v[56:59], v188 offset:8224
	ds_read_b128 v[72:75], v188 offset:8240
	ds_read_b128 v[84:87], v188 offset:16416
	ds_read_b128 v[88:91], v188 offset:16432
	ds_read_b128 v[128:131], v188 offset:24608
	ds_read_b128 v[132:135], v188 offset:24624
	ds_read_b128 v[136:139], v188 offset:32800
	s_add_i32 s41, s2, 0x10020
	s_waitcnt lgkmcnt(8)
	v_pk_fma_f32 v[174:175], v[30:31], v[52:53], v[148:149] op_sel_hi:[1,0,1]
	s_waitcnt lgkmcnt(4)
	v_pk_fma_f32 v[202:203], v[30:31], v[84:85], v[160:161] op_sel_hi:[1,0,1]
	v_mov_b32_e32 v160, s41
	v_pk_fma_f32 v[196:197], v[28:29], v[52:53], v[144:145] op_sel_hi:[1,0,1]
	v_pk_fma_f32 v[198:199], v[30:31], v[56:57], v[156:157] op_sel_hi:[1,0,1]
	v_pk_fma_f32 v[200:201], v[28:29], v[56:57], v[152:153] op_sel_hi:[1,0,1]
	v_pk_fma_f32 v[204:205], v[28:29], v[84:85], v[158:159] op_sel_hi:[1,0,1]
	s_waitcnt lgkmcnt(2)
	v_pk_fma_f32 v[206:207], v[30:31], v[128:129], v[162:163] op_sel_hi:[1,0,1]
	v_pk_fma_f32 v[208:209], v[28:29], v[128:129], v[154:155] op_sel_hi:[1,0,1]
	ds_read_b128 v[140:143], v188 offset:32816
	ds_read_b128 v[144:147], v188 offset:40992
	s_waitcnt lgkmcnt(2)
	v_pk_fma_f32 v[210:211], v[28:29], v[136:137], v[150:151] op_sel_hi:[1,0,1]
	ds_read_b128 v[148:151], v188 offset:41008
	ds_read_b128 v[152:155], v188 offset:49184
	ds_read_b128 v[156:159], v188 offset:57376
	ds_read_b128 v[182:185], v188 offset:49200
	ds_read_b128 v[188:191], v188 offset:57392
	ds_read_b128 v[160:163], v160
	v_pk_fma_f32 v[164:165], v[30:31], v[136:137], v[164:165] op_sel_hi:[1,0,1]
	s_waitcnt lgkmcnt(6)
	v_pk_fma_f32 v[166:167], v[28:29], v[144:145], v[166:167] op_sel_hi:[1,0,1]
	s_waitcnt lgkmcnt(4)
	v_pk_fma_f32 v[170:171], v[28:29], v[152:153], v[170:171] op_sel_hi:[1,0,1]
	s_waitcnt lgkmcnt(3)
	v_pk_fma_f32 v[60:61], v[28:29], v[156:157], v[60:61] op_sel_hi:[1,0,1]
	s_waitcnt lgkmcnt(0)
	v_pk_fma_f32 v[28:29], v[28:29], v[160:161], v[62:63] op_sel_hi:[1,0,1]
	v_pk_fma_f32 v[168:169], v[30:31], v[144:145], v[168:169] op_sel_hi:[1,0,1]
	v_pk_fma_f32 v[172:173], v[30:31], v[152:153], v[172:173] op_sel_hi:[1,0,1]
	v_pk_fma_f32 v[70:71], v[30:31], v[156:157], v[70:71] op_sel_hi:[1,0,1]
	v_pk_fma_f32 v[30:31], v[30:31], v[160:161], v[68:69] op_sel_hi:[1,0,1]
	v_pk_fma_f32 v[62:63], v[24:25], v[52:53], v[196:197] op_sel:[0,1,0]
	v_pk_fma_f32 v[52:53], v[26:27], v[52:53], v[174:175] op_sel:[0,1,0]
	v_pk_fma_f32 v[68:69], v[24:25], v[56:57], v[200:201] op_sel:[0,1,0]
	v_pk_fma_f32 v[56:57], v[26:27], v[56:57], v[198:199] op_sel:[0,1,0]
	v_pk_fma_f32 v[174:175], v[24:25], v[84:85], v[204:205] op_sel:[0,1,0]
	v_pk_fma_f32 v[84:85], v[26:27], v[84:85], v[202:203] op_sel:[0,1,0]
	v_pk_fma_f32 v[196:197], v[24:25], v[128:129], v[208:209] op_sel:[0,1,0]
	v_pk_fma_f32 v[128:129], v[26:27], v[128:129], v[206:207] op_sel:[0,1,0]
	v_pk_fma_f32 v[198:199], v[24:25], v[136:137], v[210:211] op_sel:[0,1,0]
	v_pk_fma_f32 v[136:137], v[26:27], v[136:137], v[164:165] op_sel:[0,1,0]
	v_pk_fma_f32 v[164:165], v[24:25], v[144:145], v[166:167] op_sel:[0,1,0]
	v_pk_fma_f32 v[166:167], v[24:25], v[152:153], v[170:171] op_sel:[0,1,0]
	v_pk_fma_f32 v[60:61], v[24:25], v[156:157], v[60:61] op_sel:[0,1,0]
	v_pk_fma_f32 v[24:25], v[24:25], v[160:161], v[28:29] op_sel:[0,1,0]
	v_pk_fma_f32 v[144:145], v[26:27], v[144:145], v[168:169] op_sel:[0,1,0]
	v_pk_fma_f32 v[152:153], v[26:27], v[152:153], v[172:173] op_sel:[0,1,0]
	v_pk_fma_f32 v[70:71], v[26:27], v[156:157], v[70:71] op_sel:[0,1,0]
	v_pk_fma_f32 v[26:27], v[26:27], v[160:161], v[30:31] op_sel:[0,1,0]
	v_pk_fma_f32 v[28:29], v[22:23], v[54:55], v[52:53] op_sel_hi:[1,0,1]
	v_pk_fma_f32 v[30:31], v[20:21], v[54:55], v[62:63] op_sel_hi:[1,0,1]
	v_pk_fma_f32 v[52:53], v[22:23], v[58:59], v[56:57] op_sel_hi:[1,0,1]
	v_pk_fma_f32 v[56:57], v[20:21], v[58:59], v[68:69] op_sel_hi:[1,0,1]
	v_pk_fma_f32 v[62:63], v[22:23], v[86:87], v[84:85] op_sel_hi:[1,0,1]
	v_pk_fma_f32 v[68:69], v[20:21], v[86:87], v[174:175] op_sel_hi:[1,0,1]
	v_pk_fma_f32 v[84:85], v[22:23], v[130:131], v[128:129] op_sel_hi:[1,0,1]
	v_pk_fma_f32 v[128:129], v[20:21], v[130:131], v[196:197] op_sel_hi:[1,0,1]
	v_pk_fma_f32 v[156:157], v[20:21], v[138:139], v[198:199] op_sel_hi:[1,0,1]
	v_pk_fma_f32 v[160:161], v[20:21], v[146:147], v[164:165] op_sel_hi:[1,0,1]
	v_pk_fma_f32 v[164:165], v[20:21], v[154:155], v[166:167] op_sel_hi:[1,0,1]
	v_pk_fma_f32 v[60:61], v[20:21], v[158:159], v[60:61] op_sel_hi:[1,0,1]
	v_pk_fma_f32 v[20:21], v[20:21], v[162:163], v[24:25] op_sel_hi:[1,0,1]
	v_mov_b32_e32 v24, v55
	v_pk_fma_f32 v[136:137], v[22:23], v[138:139], v[136:137] op_sel_hi:[1,0,1]
	v_pk_fma_f32 v[144:145], v[22:23], v[146:147], v[144:145] op_sel_hi:[1,0,1]
	v_pk_fma_f32 v[152:153], v[22:23], v[154:155], v[152:153] op_sel_hi:[1,0,1]
	v_pk_fma_f32 v[70:71], v[22:23], v[158:159], v[70:71] op_sel_hi:[1,0,1]
	v_pk_fma_f32 v[22:23], v[22:23], v[162:163], v[26:27] op_sel_hi:[1,0,1]
	v_pk_fma_f32 v[26:27], v[16:17], v[24:25], v[30:31] op_sel_hi:[1,0,1]
	v_pk_fma_f32 v[24:25], v[18:19], v[24:25], v[28:29] op_sel_hi:[1,0,1]
	v_mov_b32_e32 v28, v59
	v_pk_fma_f32 v[30:31], v[16:17], v[28:29], v[56:57] op_sel_hi:[1,0,1]
	v_pk_fma_f32 v[28:29], v[18:19], v[28:29], v[52:53] op_sel_hi:[1,0,1]
	v_mov_b32_e32 v52, v87
	s_add_i32 s2, s2, 0x10030
	v_pk_fma_f32 v[54:55], v[16:17], v[52:53], v[68:69] op_sel_hi:[1,0,1]
	v_pk_fma_f32 v[52:53], v[18:19], v[52:53], v[62:63] op_sel_hi:[1,0,1]
	v_mov_b32_e32 v62, v139
	v_mov_b32_e32 v192, s2
	v_mov_b32_e32 v56, v131
	v_pk_fma_f32 v[68:69], v[16:17], v[62:63], v[156:157] op_sel_hi:[1,0,1]
	v_pk_fma_f32 v[62:63], v[18:19], v[62:63], v[136:137] op_sel_hi:[1,0,1]
	v_mov_b32_e32 v136, v159
	s_min_i32 s2, s39, s20
	v_pk_fma_f32 v[58:59], v[16:17], v[56:57], v[128:129] op_sel_hi:[1,0,1]
	v_pk_fma_f32 v[56:57], v[18:19], v[56:57], v[84:85] op_sel_hi:[1,0,1]
	v_mov_b32_e32 v84, v147
	v_mov_b32_e32 v128, v155
	v_pk_fma_f32 v[60:61], v[16:17], v[136:137], v[60:61] op_sel_hi:[1,0,1]
	v_pk_fma_f32 v[70:71], v[18:19], v[136:137], v[70:71] op_sel_hi:[1,0,1]
	v_mov_b32_e32 v136, v163
	s_lshl_b32 s41, s2, 8
	v_pk_fma_f32 v[86:87], v[16:17], v[84:85], v[160:161] op_sel_hi:[1,0,1]
	v_pk_fma_f32 v[84:85], v[18:19], v[84:85], v[144:145] op_sel_hi:[1,0,1]
	v_pk_fma_f32 v[130:131], v[16:17], v[128:129], v[164:165] op_sel_hi:[1,0,1]
	v_pk_fma_f32 v[128:129], v[18:19], v[128:129], v[152:153] op_sel_hi:[1,0,1]
	v_pk_fma_f32 v[18:19], v[18:19], v[136:137], v[22:23] op_sel_hi:[1,0,1]
	v_pk_fma_f32 v[22:23], v[12:13], v[48:49], v[26:27] op_sel_hi:[1,0,1]
	s_and_b32 s41, s41, 0xfffff800
	v_pk_fma_f32 v[16:17], v[16:17], v[136:137], v[20:21] op_sel_hi:[1,0,1]
	v_pk_fma_f32 v[20:21], v[14:15], v[48:49], v[24:25] op_sel_hi:[1,0,1]
	v_pk_fma_f32 v[22:23], v[8:9], v[48:49], v[22:23] op_sel:[0,1,0]
	s_add_i32 s41, s41, s33
	v_pk_fma_f32 v[20:21], v[10:11], v[48:49], v[20:21] op_sel:[0,1,0]
	v_pk_fma_f32 v[22:23], v[4:5], v[50:51], v[22:23] op_sel_hi:[1,0,1]
	v_mov_b32_e32 v24, v51
	s_ashr_i32 s42, s41, 31
	v_pk_fma_f32 v[20:21], v[6:7], v[50:51], v[20:21] op_sel_hi:[1,0,1]
	v_pk_fma_f32 v[196:197], v[0:1], v[24:25], v[22:23] op_sel_hi:[1,0,1]
	v_pk_fma_f32 v[22:23], v[12:13], v[72:73], v[30:31] op_sel_hi:[1,0,1]
	s_lshr_b32 s42, s42, 28
	v_pk_fma_f32 v[198:199], v[2:3], v[24:25], v[20:21] op_sel_hi:[1,0,1]
	v_pk_fma_f32 v[20:21], v[14:15], v[72:73], v[28:29] op_sel_hi:[1,0,1]
	v_pk_fma_f32 v[22:23], v[8:9], v[72:73], v[22:23] op_sel:[0,1,0]
	s_add_i32 s42, s41, s42
	v_pk_fma_f32 v[20:21], v[10:11], v[72:73], v[20:21] op_sel:[0,1,0]
	v_pk_fma_f32 v[22:23], v[4:5], v[74:75], v[22:23] op_sel_hi:[1,0,1]
	v_mov_b32_e32 v24, v75
	s_ashr_i32 s43, s42, 4
	s_and_b32 s42, s42, 0x1fffff0
	v_pk_fma_f32 v[20:21], v[6:7], v[74:75], v[20:21] op_sel_hi:[1,0,1]
	v_pk_fma_f32 v[172:173], v[0:1], v[24:25], v[22:23] op_sel_hi:[1,0,1]
	v_pk_fma_f32 v[22:23], v[12:13], v[88:89], v[54:55] op_sel_hi:[1,0,1]
	s_sub_i32 s44, s41, s42
	s_mul_hi_i32 s42, s43, 0x2aaaaaab
	v_pk_fma_f32 v[174:175], v[2:3], v[24:25], v[20:21] op_sel_hi:[1,0,1]
	v_pk_fma_f32 v[20:21], v[14:15], v[88:89], v[52:53] op_sel_hi:[1,0,1]
	v_pk_fma_f32 v[22:23], v[8:9], v[88:89], v[22:23] op_sel:[0,1,0]
	s_lshr_b32 s45, s42, 31
	s_lshr_b32 s42, s42, 3
	v_pk_fma_f32 v[20:21], v[10:11], v[88:89], v[20:21] op_sel:[0,1,0]
	v_pk_fma_f32 v[22:23], v[4:5], v[90:91], v[22:23] op_sel_hi:[1,0,1]
	v_mov_b32_e32 v24, v91
	s_add_i32 s42, s42, s45
	v_pk_fma_f32 v[20:21], v[6:7], v[90:91], v[20:21] op_sel_hi:[1,0,1]
	v_pk_fma_f32 v[168:169], v[0:1], v[24:25], v[22:23] op_sel_hi:[1,0,1]
	v_pk_fma_f32 v[22:23], v[12:13], v[132:133], v[58:59] op_sel_hi:[1,0,1]
	s_mul_i32 s42, s42, 48
	s_mul_hi_i32 s41, s41, 0x2aaaaaab
	v_pk_fma_f32 v[170:171], v[2:3], v[24:25], v[20:21] op_sel_hi:[1,0,1]
	v_pk_fma_f32 v[20:21], v[14:15], v[132:133], v[56:57] op_sel_hi:[1,0,1]
	v_pk_fma_f32 v[22:23], v[8:9], v[132:133], v[22:23] op_sel:[0,1,0]
	s_sub_i32 s45, s43, s42
	s_lshr_b32 s42, s41, 31
	s_ashr_i32 s41, s41, 7
	v_pk_fma_f32 v[20:21], v[10:11], v[132:133], v[20:21] op_sel:[0,1,0]
	v_pk_fma_f32 v[22:23], v[4:5], v[134:135], v[22:23] op_sel_hi:[1,0,1]
	v_mov_b32_e32 v24, v135
	s_add_i32 s42, s41, s42
	v_pk_fma_f32 v[20:21], v[6:7], v[134:135], v[20:21] op_sel_hi:[1,0,1]
	v_pk_fma_f32 v[164:165], v[0:1], v[24:25], v[22:23] op_sel_hi:[1,0,1]
	v_pk_fma_f32 v[22:23], v[12:13], v[140:141], v[68:69] op_sel_hi:[1,0,1]
	s_lshl_b32 s2, s2, 4
	s_ashr_i32 s43, s42, 31
	s_lshl_b32 s41, s44, 7
	v_pk_fma_f32 v[166:167], v[2:3], v[24:25], v[20:21] op_sel_hi:[1,0,1]
	v_pk_fma_f32 v[20:21], v[14:15], v[140:141], v[62:63] op_sel_hi:[1,0,1]
	v_pk_fma_f32 v[22:23], v[8:9], v[140:141], v[22:23] op_sel:[0,1,0]
	s_and_b32 s2, s2, 0x60
	s_lshl_b64 s[42:43], s[42:43], 11
	s_ashr_i32 s44, s41, 31
	v_pk_fma_f32 v[20:21], v[10:11], v[140:141], v[20:21] op_sel:[0,1,0]
	v_pk_fma_f32 v[22:23], v[4:5], v[142:143], v[22:23] op_sel_hi:[1,0,1]
	v_mov_b32_e32 v24, v143
	s_add_u32 s41, s42, s41
	v_pk_fma_f32 v[20:21], v[6:7], v[142:143], v[20:21] op_sel_hi:[1,0,1]
	v_pk_fma_f32 v[160:161], v[0:1], v[24:25], v[22:23] op_sel_hi:[1,0,1]
	v_pk_fma_f32 v[22:23], v[12:13], v[148:149], v[86:87] op_sel_hi:[1,0,1]
	s_addc_u32 s42, s43, s44
	s_or_b32 s2, s41, s2
	ds_read_b128 v[192:195], v192
	v_pk_fma_f32 v[162:163], v[2:3], v[24:25], v[20:21] op_sel_hi:[1,0,1]
	v_pk_fma_f32 v[20:21], v[14:15], v[148:149], v[84:85] op_sel_hi:[1,0,1]
	v_pk_fma_f32 v[22:23], v[8:9], v[148:149], v[22:23] op_sel:[0,1,0]
	s_mul_i32 s42, s42, 0xc000
	s_mul_hi_u32 s41, s2, 0xc000
	v_pk_fma_f32 v[20:21], v[10:11], v[148:149], v[20:21] op_sel:[0,1,0]
	v_pk_fma_f32 v[22:23], v[4:5], v[150:151], v[22:23] op_sel_hi:[1,0,1]
	v_mov_b32_e32 v24, v151
	s_add_i32 s41, s41, s42
	s_mul_i32 s2, s2, 0xc000
	v_pk_fma_f32 v[20:21], v[6:7], v[150:151], v[20:21] op_sel_hi:[1,0,1]
	v_pk_fma_f32 v[156:157], v[0:1], v[24:25], v[22:23] op_sel_hi:[1,0,1]
	v_pk_fma_f32 v[22:23], v[12:13], v[182:183], v[130:131] op_sel_hi:[1,0,1]
	s_add_u32 s2, s8, s2
	v_pk_fma_f32 v[158:159], v[2:3], v[24:25], v[20:21] op_sel_hi:[1,0,1]
	v_pk_fma_f32 v[20:21], v[14:15], v[182:183], v[128:129] op_sel_hi:[1,0,1]
	v_pk_fma_f32 v[22:23], v[8:9], v[182:183], v[22:23] op_sel:[0,1,0]
	s_addc_u32 s41, s9, s41
	s_lshl_b32 s42, s45, 8
	v_pk_fma_f32 v[20:21], v[10:11], v[182:183], v[20:21] op_sel:[0,1,0]
	v_pk_fma_f32 v[22:23], v[4:5], v[184:185], v[22:23] op_sel_hi:[1,0,1]
	v_mov_b32_e32 v24, v185
	s_ashr_i32 s43, s42, 31
	v_pk_fma_f32 v[20:21], v[6:7], v[184:185], v[20:21] op_sel_hi:[1,0,1]
	v_pk_fma_f32 v[152:153], v[0:1], v[24:25], v[22:23] op_sel_hi:[1,0,1]
	v_pk_fma_f32 v[22:23], v[12:13], v[188:189], v[60:61] op_sel_hi:[1,0,1]
	s_waitcnt lgkmcnt(0)
	v_pk_fma_f32 v[12:13], v[12:13], v[192:193], v[16:17] op_sel_hi:[1,0,1]
	s_lshl_b64 s[42:43], s[42:43], 2
	v_pk_fma_f32 v[154:155], v[2:3], v[24:25], v[20:21] op_sel_hi:[1,0,1]
	v_pk_fma_f32 v[20:21], v[14:15], v[188:189], v[70:71] op_sel_hi:[1,0,1]
	v_pk_fma_f32 v[22:23], v[8:9], v[188:189], v[22:23] op_sel:[0,1,0]
	v_pk_fma_f32 v[14:15], v[14:15], v[192:193], v[18:19] op_sel_hi:[1,0,1]
	v_pk_fma_f32 v[8:9], v[8:9], v[192:193], v[12:13] op_sel:[0,1,0]
	s_add_u32 s42, s2, s42
	v_pk_fma_f32 v[20:21], v[10:11], v[188:189], v[20:21] op_sel:[0,1,0]
	v_pk_fma_f32 v[22:23], v[4:5], v[190:191], v[22:23] op_sel_hi:[1,0,1]
	v_mov_b32_e32 v24, v191
	v_pk_fma_f32 v[10:11], v[10:11], v[192:193], v[14:15] op_sel:[0,1,0]
	v_pk_fma_f32 v[4:5], v[4:5], v[194:195], v[8:9] op_sel_hi:[1,0,1]
	v_mov_b32_e32 v8, v195
	s_addc_u32 s43, s41, s43
	v_pk_fma_f32 v[20:21], v[6:7], v[190:191], v[20:21] op_sel_hi:[1,0,1]
	v_pk_fma_f32 v[144:145], v[0:1], v[24:25], v[22:23] op_sel_hi:[1,0,1]
	v_pk_fma_f32 v[6:7], v[6:7], v[194:195], v[10:11] op_sel_hi:[1,0,1]
	v_pk_fma_f32 v[146:147], v[0:1], v[8:9], v[4:5] op_sel_hi:[1,0,1]
	v_lshl_add_u64 v[0:1], s[42:43], 0, v[178:179]
	v_pk_fma_f32 v[150:151], v[2:3], v[24:25], v[20:21] op_sel_hi:[1,0,1]
	v_pk_fma_f32 v[148:149], v[2:3], v[8:9], v[6:7] op_sel_hi:[1,0,1]
	v_add_co_u32_e32 v2, vcc, s17, v0
	s_lshl_b32 s2, s11, 6
	s_nop 0
	v_addc_co_u32_e32 v3, vcc, 0, v1, vcc
	v_add_co_u32_e32 v4, vcc, s36, v0
	s_add_i32 s2, s40, s2
	s_nop 0
	v_addc_co_u32_e32 v5, vcc, 0, v1, vcc
	v_add_co_u32_e32 v6, vcc, s35, v0
	v_mov_b32_e32 v182, s2
	s_nop 0
	v_addc_co_u32_e32 v7, vcc, 0, v1, vcc
	v_add_co_u32_e32 v8, vcc, s34, v0
	s_add_i32 s40, s2, 0x10040
	s_nop 0
	v_addc_co_u32_e32 v9, vcc, 0, v1, vcc
	v_add_co_u32_e32 v10, vcc, s31, v0
	v_mov_b32_e32 v183, s40
	s_nop 0
	v_addc_co_u32_e32 v11, vcc, 0, v1, vcc
	v_add_co_u32_e32 v12, vcc, s30, v0
	s_add_i32 s40, s2, 0x10050
	s_nop 0
	v_addc_co_u32_e32 v13, vcc, 0, v1, vcc
	v_add_co_u32_e32 v14, vcc, s29, v0
	s_nop 1
	v_addc_co_u32_e32 v15, vcc, 0, v1, vcc
	v_add_co_u32_e32 v16, vcc, s28, v0
	s_nop 1
	v_addc_co_u32_e32 v17, vcc, 0, v1, vcc
	v_add_co_u32_e32 v18, vcc, s27, v0
	s_nop 1
	v_addc_co_u32_e32 v19, vcc, 0, v1, vcc
	v_add_co_u32_e32 v20, vcc, s26, v0
	s_nop 1
	v_addc_co_u32_e32 v21, vcc, 0, v1, vcc
	v_add_co_u32_e32 v72, vcc, s25, v0
	s_nop 1
	v_addc_co_u32_e32 v73, vcc, 0, v1, vcc
	v_add_co_u32_e32 v74, vcc, s24, v0
	s_nop 1
	v_addc_co_u32_e32 v75, vcc, 0, v1, vcc
	v_add_co_u32_e32 v128, vcc, s23, v0
	s_nop 1
	v_addc_co_u32_e32 v129, vcc, 0, v1, vcc
	v_add_co_u32_e32 v130, vcc, s22, v0
	s_nop 1
	v_addc_co_u32_e32 v131, vcc, 0, v1, vcc
	v_add_co_u32_e32 v0, vcc, s21, v0
	s_nop 1
	v_addc_co_u32_e32 v1, vcc, 0, v1, vcc
	global_load_dwordx4 v[84:87], v[2:3], off nt
	global_load_dwordx4 v[88:91], v[4:5], off nt
	global_load_dwordx4 v[68:71], v[6:7], off nt
	global_load_dwordx4 v[60:63], v[8:9], off nt
	global_load_dwordx4 v[56:59], v[10:11], off nt
	global_load_dwordx4 v[52:55], v[12:13], off nt
	global_load_dwordx4 v[48:51], v[14:15], off nt
	global_load_dwordx4 v[28:31], v[16:17], off nt
	global_load_dwordx4 v[24:27], v[18:19], off nt
	s_nop 0
	global_load_dwordx4 v[20:23], v[20:21], off nt
	s_nop 0
	global_load_dwordx4 v[16:19], v[72:73], off nt
	global_load_dwordx4 v[12:15], v[74:75], off nt
	global_load_dwordx4 v[8:11], v[128:129], off nt
	global_load_dwordx4 v[4:7], v[130:131], off nt
	s_nop 0
	global_load_dwordx4 v[0:3], v[0:1], off nt
	s_nop 0
	global_load_dwordx4 v[72:75], v178, s[42:43] nt
	ds_read_b128 v[132:135], v182 offset:64
	ds_read_b128 v[128:131], v182 offset:80
	ds_read_b128 v[136:139], v182 offset:8256
	ds_read_b128 v[140:143], v182 offset:8272
	ds_read_b128 v[188:191], v182 offset:16448
	s_waitcnt vmcnt(16) lgkmcnt(4)
	v_pk_fma_f32 v[184:185], v[126:127], v[132:133], v[198:199] op_sel_hi:[1,0,1]
	v_pk_fma_f32 v[220:221], v[124:125], v[132:133], v[196:197] op_sel_hi:[1,0,1]
	s_waitcnt lgkmcnt(2)
	v_pk_fma_f32 v[222:223], v[126:127], v[136:137], v[174:175] op_sel_hi:[1,0,1]
	v_pk_fma_f32 v[224:225], v[124:125], v[136:137], v[172:173] op_sel_hi:[1,0,1]
	ds_read_b128 v[172:175], v182 offset:16464
	ds_read_b128 v[192:195], v182 offset:24640
	s_waitcnt lgkmcnt(2)
	v_pk_fma_f32 v[226:227], v[126:127], v[188:189], v[170:171] op_sel_hi:[1,0,1]
	v_pk_fma_f32 v[228:229], v[124:125], v[188:189], v[168:169] op_sel_hi:[1,0,1]
	ds_read_b128 v[168:171], v182 offset:24656
	ds_read_b128 v[196:199], v182 offset:32832
	s_waitcnt lgkmcnt(2)
	v_pk_fma_f32 v[230:231], v[126:127], v[192:193], v[166:167] op_sel_hi:[1,0,1]
	v_pk_fma_f32 v[232:233], v[124:125], v[192:193], v[164:165] op_sel_hi:[1,0,1]
	ds_read_b128 v[164:167], v182 offset:32848
	ds_read_b128 v[200:203], v182 offset:41024
	s_waitcnt lgkmcnt(2)
	v_pk_fma_f32 v[234:235], v[126:127], v[196:197], v[162:163] op_sel_hi:[1,0,1]
	v_pk_fma_f32 v[236:237], v[124:125], v[196:197], v[160:161] op_sel_hi:[1,0,1]
	ds_read_b128 v[160:163], v182 offset:41040
	ds_read_b128 v[204:207], v182 offset:49216
	s_waitcnt lgkmcnt(2)
	v_pk_fma_f32 v[238:239], v[126:127], v[200:201], v[158:159] op_sel_hi:[1,0,1]
	v_pk_fma_f32 v[240:241], v[124:125], v[200:201], v[156:157] op_sel_hi:[1,0,1]
	ds_read_b128 v[156:159], v182 offset:57408
	ds_read_b128 v[208:211], v182 offset:49232
	s_waitcnt lgkmcnt(2)
	v_pk_fma_f32 v[242:243], v[126:127], v[204:205], v[154:155] op_sel_hi:[1,0,1]
	v_pk_fma_f32 v[244:245], v[124:125], v[204:205], v[152:153] op_sel_hi:[1,0,1]
	ds_read_b128 v[152:155], v182 offset:57424
	ds_read_b128 v[212:215], v183
	s_waitcnt lgkmcnt(3)
	v_pk_fma_f32 v[144:145], v[124:125], v[156:157], v[144:145] op_sel_hi:[1,0,1]
	v_pk_fma_f32 v[150:151], v[126:127], v[156:157], v[150:151] op_sel_hi:[1,0,1]
	v_pk_fma_f32 v[144:145], v[120:121], v[156:157], v[144:145] op_sel:[0,1,0]
	v_pk_fma_f32 v[150:151], v[122:123], v[156:157], v[150:151] op_sel:[0,1,0]
	s_waitcnt lgkmcnt(0)
	v_pk_fma_f32 v[124:125], v[124:125], v[212:213], v[146:147] op_sel_hi:[1,0,1]
	v_pk_fma_f32 v[126:127], v[126:127], v[212:213], v[148:149] op_sel_hi:[1,0,1]
	v_pk_fma_f32 v[146:147], v[122:123], v[132:133], v[184:185] op_sel:[0,1,0]
	v_pk_fma_f32 v[132:133], v[120:121], v[132:133], v[220:221] op_sel:[0,1,0]
	v_pk_fma_f32 v[148:149], v[122:123], v[136:137], v[222:223] op_sel:[0,1,0]
	v_pk_fma_f32 v[136:137], v[120:121], v[136:137], v[224:225] op_sel:[0,1,0]
	v_pk_fma_f32 v[184:185], v[122:123], v[188:189], v[226:227] op_sel:[0,1,0]
	v_pk_fma_f32 v[188:189], v[120:121], v[188:189], v[228:229] op_sel:[0,1,0]
	v_pk_fma_f32 v[220:221], v[122:123], v[192:193], v[230:231] op_sel:[0,1,0]
	v_pk_fma_f32 v[192:193], v[120:121], v[192:193], v[232:233] op_sel:[0,1,0]
	v_pk_fma_f32 v[222:223], v[122:123], v[196:197], v[234:235] op_sel:[0,1,0]
	v_pk_fma_f32 v[196:197], v[120:121], v[196:197], v[236:237] op_sel:[0,1,0]
	v_pk_fma_f32 v[224:225], v[122:123], v[200:201], v[238:239] op_sel:[0,1,0]
	v_pk_fma_f32 v[200:201], v[120:121], v[200:201], v[240:241] op_sel:[0,1,0]
	v_pk_fma_f32 v[226:227], v[122:123], v[204:205], v[242:243] op_sel:[0,1,0]
	v_pk_fma_f32 v[204:205], v[120:121], v[204:205], v[244:245] op_sel:[0,1,0]
	v_pk_fma_f32 v[120:121], v[120:121], v[212:213], v[124:125] op_sel:[0,1,0]
	v_pk_fma_f32 v[122:123], v[122:123], v[212:213], v[126:127] op_sel:[0,1,0]
	v_pk_fma_f32 v[124:125], v[118:119], v[134:135], v[146:147] op_sel_hi:[1,0,1]
	v_pk_fma_f32 v[126:127], v[116:117], v[134:135], v[132:133] op_sel_hi:[1,0,1]
	v_pk_fma_f32 v[132:133], v[118:119], v[138:139], v[148:149] op_sel_hi:[1,0,1]
	v_pk_fma_f32 v[136:137], v[116:117], v[138:139], v[136:137] op_sel_hi:[1,0,1]
	v_pk_fma_f32 v[146:147], v[118:119], v[190:191], v[184:185] op_sel_hi:[1,0,1]
	v_pk_fma_f32 v[148:149], v[116:117], v[190:191], v[188:189] op_sel_hi:[1,0,1]
	v_pk_fma_f32 v[184:185], v[116:117], v[194:195], v[192:193] op_sel_hi:[1,0,1]
	v_pk_fma_f32 v[192:193], v[116:117], v[198:199], v[196:197] op_sel_hi:[1,0,1]
	v_pk_fma_f32 v[200:201], v[116:117], v[202:203], v[200:201] op_sel_hi:[1,0,1]
	v_pk_fma_f32 v[204:205], v[116:117], v[206:207], v[204:205] op_sel_hi:[1,0,1]
	v_pk_fma_f32 v[144:145], v[116:117], v[158:159], v[144:145] op_sel_hi:[1,0,1]
	v_pk_fma_f32 v[116:117], v[116:117], v[214:215], v[120:121] op_sel_hi:[1,0,1]
	v_mov_b32_e32 v120, v135
	v_mov_b32_e32 v183, s40
	v_pk_fma_f32 v[156:157], v[118:119], v[194:195], v[220:221] op_sel_hi:[1,0,1]
	v_pk_fma_f32 v[188:189], v[118:119], v[198:199], v[222:223] op_sel_hi:[1,0,1]
	v_pk_fma_f32 v[196:197], v[118:119], v[202:203], v[224:225] op_sel_hi:[1,0,1]
	v_pk_fma_f32 v[212:213], v[118:119], v[206:207], v[226:227] op_sel_hi:[1,0,1]
	v_pk_fma_f32 v[150:151], v[118:119], v[158:159], v[150:151] op_sel_hi:[1,0,1]
	v_pk_fma_f32 v[118:119], v[118:119], v[214:215], v[122:123] op_sel_hi:[1,0,1]
	v_pk_fma_f32 v[122:123], v[114:115], v[120:121], v[124:125] op_sel_hi:[1,0,1]
	v_mov_b32_e32 v124, v139
	ds_read_b128 v[216:219], v183
	v_pk_fma_f32 v[120:121], v[112:113], v[120:121], v[126:127] op_sel_hi:[1,0,1]
	v_pk_fma_f32 v[126:127], v[114:115], v[124:125], v[132:133] op_sel_hi:[1,0,1]
	v_mov_b32_e32 v132, v191
	v_pk_fma_f32 v[134:135], v[114:115], v[132:133], v[146:147] op_sel_hi:[1,0,1]
	v_mov_b32_e32 v146, v199
	v_mov_b32_e32 v158, v207
	v_pk_fma_f32 v[124:125], v[112:113], v[124:125], v[136:137] op_sel_hi:[1,0,1]
	v_pk_fma_f32 v[132:133], v[112:113], v[132:133], v[148:149] op_sel_hi:[1,0,1]
	v_mov_b32_e32 v136, v195
	v_pk_fma_f32 v[148:149], v[114:115], v[146:147], v[188:189] op_sel_hi:[1,0,1]
	v_pk_fma_f32 v[188:189], v[114:115], v[158:159], v[212:213] op_sel_hi:[1,0,1]
	v_pk_fma_f32 v[190:191], v[112:113], v[158:159], v[204:205] op_sel_hi:[1,0,1]
	v_mov_b32_e32 v158, v159
	v_pk_fma_f32 v[138:139], v[114:115], v[136:137], v[156:157] op_sel_hi:[1,0,1]
	v_mov_b32_e32 v156, v203
	v_pk_fma_f32 v[150:151], v[114:115], v[158:159], v[150:151] op_sel_hi:[1,0,1]
	v_pk_fma_f32 v[144:145], v[112:113], v[158:159], v[144:145] op_sel_hi:[1,0,1]
	v_mov_b32_e32 v158, v215
	v_pk_fma_f32 v[136:137], v[112:113], v[136:137], v[184:185] op_sel_hi:[1,0,1]
	v_pk_fma_f32 v[146:147], v[112:113], v[146:147], v[192:193] op_sel_hi:[1,0,1]
	v_pk_fma_f32 v[184:185], v[114:115], v[156:157], v[196:197] op_sel_hi:[1,0,1]
	v_pk_fma_f32 v[156:157], v[112:113], v[156:157], v[200:201] op_sel_hi:[1,0,1]
	v_pk_fma_f32 v[112:113], v[112:113], v[158:159], v[116:117] op_sel_hi:[1,0,1]
	v_pk_fma_f32 v[114:115], v[114:115], v[158:159], v[118:119] op_sel_hi:[1,0,1]
	v_pk_fma_f32 v[116:117], v[110:111], v[128:129], v[122:123] op_sel_hi:[1,0,1]
	v_pk_fma_f32 v[118:119], v[108:109], v[128:129], v[120:121] op_sel_hi:[1,0,1]
	v_pk_fma_f32 v[120:121], v[110:111], v[140:141], v[126:127] op_sel_hi:[1,0,1]
	v_pk_fma_f32 v[122:123], v[108:109], v[140:141], v[124:125] op_sel_hi:[1,0,1]
	v_pk_fma_f32 v[124:125], v[110:111], v[172:173], v[134:135] op_sel_hi:[1,0,1]
	v_pk_fma_f32 v[126:127], v[108:109], v[172:173], v[132:133] op_sel_hi:[1,0,1]
	v_pk_fma_f32 v[132:133], v[110:111], v[168:169], v[138:139] op_sel_hi:[1,0,1]
	v_pk_fma_f32 v[134:135], v[108:109], v[168:169], v[136:137] op_sel_hi:[1,0,1]
	v_pk_fma_f32 v[136:137], v[110:111], v[164:165], v[148:149] op_sel_hi:[1,0,1]
	v_pk_fma_f32 v[138:139], v[108:109], v[164:165], v[146:147] op_sel_hi:[1,0,1]
	v_pk_fma_f32 v[148:149], v[108:109], v[160:161], v[156:157] op_sel_hi:[1,0,1]
	v_pk_fma_f32 v[158:159], v[108:109], v[208:209], v[190:191] op_sel_hi:[1,0,1]
	v_pk_fma_f32 v[144:145], v[108:109], v[152:153], v[144:145] op_sel_hi:[1,0,1]
	s_waitcnt lgkmcnt(0)
	v_pk_fma_f32 v[108:109], v[108:109], v[216:217], v[112:113] op_sel_hi:[1,0,1]
	v_pk_fma_f32 v[146:147], v[110:111], v[160:161], v[184:185] op_sel_hi:[1,0,1]
	v_pk_fma_f32 v[156:157], v[110:111], v[208:209], v[188:189] op_sel_hi:[1,0,1]
	v_pk_fma_f32 v[150:151], v[110:111], v[152:153], v[150:151] op_sel_hi:[1,0,1]
	v_pk_fma_f32 v[110:111], v[110:111], v[216:217], v[114:115] op_sel_hi:[1,0,1]
	v_pk_fma_f32 v[112:113], v[106:107], v[128:129], v[116:117] op_sel:[0,1,0]
	v_pk_fma_f32 v[114:115], v[104:105], v[128:129], v[118:119] op_sel:[0,1,0]
	v_pk_fma_f32 v[116:117], v[106:107], v[140:141], v[120:121] op_sel:[0,1,0]
	v_pk_fma_f32 v[118:119], v[104:105], v[140:141], v[122:123] op_sel:[0,1,0]
	v_pk_fma_f32 v[120:121], v[106:107], v[172:173], v[124:125] op_sel:[0,1,0]
	v_pk_fma_f32 v[122:123], v[104:105], v[172:173], v[126:127] op_sel:[0,1,0]
	v_pk_fma_f32 v[124:125], v[106:107], v[168:169], v[132:133] op_sel:[0,1,0]
	v_pk_fma_f32 v[126:127], v[104:105], v[168:169], v[134:135] op_sel:[0,1,0]
	v_pk_fma_f32 v[128:129], v[106:107], v[164:165], v[136:137] op_sel:[0,1,0]
	v_pk_fma_f32 v[132:133], v[104:105], v[164:165], v[138:139] op_sel:[0,1,0]
	v_pk_fma_f32 v[136:137], v[104:105], v[160:161], v[148:149] op_sel:[0,1,0]
	v_pk_fma_f32 v[140:141], v[104:105], v[208:209], v[158:159] op_sel:[0,1,0]
	v_pk_fma_f32 v[144:145], v[104:105], v[152:153], v[144:145] op_sel:[0,1,0]
	v_pk_fma_f32 v[104:105], v[104:105], v[216:217], v[108:109] op_sel:[0,1,0]
	v_pk_fma_f32 v[134:135], v[106:107], v[160:161], v[146:147] op_sel:[0,1,0]
	v_pk_fma_f32 v[138:139], v[106:107], v[208:209], v[156:157] op_sel:[0,1,0]
	v_pk_fma_f32 v[146:147], v[106:107], v[152:153], v[150:151] op_sel:[0,1,0]
	v_pk_fma_f32 v[106:107], v[106:107], v[216:217], v[110:111] op_sel:[0,1,0]
	v_pk_fma_f32 v[108:109], v[102:103], v[130:131], v[112:113] op_sel_hi:[1,0,1]
	v_pk_fma_f32 v[110:111], v[100:101], v[130:131], v[114:115] op_sel_hi:[1,0,1]
	v_pk_fma_f32 v[114:115], v[100:101], v[142:143], v[118:119] op_sel_hi:[1,0,1]
	v_pk_fma_f32 v[118:119], v[100:101], v[174:175], v[122:123] op_sel_hi:[1,0,1]
	v_pk_fma_f32 v[122:123], v[100:101], v[170:171], v[126:127] op_sel_hi:[1,0,1]
	v_pk_fma_f32 v[126:127], v[100:101], v[166:167], v[132:133] op_sel_hi:[1,0,1]
	v_pk_fma_f32 v[132:133], v[100:101], v[162:163], v[136:137] op_sel_hi:[1,0,1]
	v_pk_fma_f32 v[136:137], v[100:101], v[210:211], v[140:141] op_sel_hi:[1,0,1]
	v_pk_fma_f32 v[140:141], v[100:101], v[154:155], v[144:145] op_sel_hi:[1,0,1]
	v_pk_fma_f32 v[104:105], v[100:101], v[218:219], v[104:105] op_sel_hi:[1,0,1]
	v_mov_b32_e32 v100, v131
	v_pk_fma_f32 v[112:113], v[102:103], v[142:143], v[116:117] op_sel_hi:[1,0,1]
	v_pk_fma_f32 v[130:131], v[98:99], v[100:101], v[108:109] op_sel_hi:[1,0,1]
	v_pk_fma_f32 v[144:145], v[96:97], v[100:101], v[110:111] op_sel_hi:[1,0,1]
	v_mov_b32_e32 v100, v143
	v_pk_fma_f32 v[116:117], v[102:103], v[174:175], v[120:121] op_sel_hi:[1,0,1]
	v_pk_fma_f32 v[120:121], v[102:103], v[170:171], v[124:125] op_sel_hi:[1,0,1]
	v_pk_fma_f32 v[124:125], v[102:103], v[166:167], v[128:129] op_sel_hi:[1,0,1]
	v_pk_fma_f32 v[128:129], v[102:103], v[162:163], v[134:135] op_sel_hi:[1,0,1]
	v_pk_fma_f32 v[134:135], v[102:103], v[210:211], v[138:139] op_sel_hi:[1,0,1]
	v_pk_fma_f32 v[138:139], v[102:103], v[154:155], v[146:147] op_sel_hi:[1,0,1]
	v_pk_fma_f32 v[142:143], v[98:99], v[100:101], v[112:113] op_sel_hi:[1,0,1]
	v_pk_fma_f32 v[146:147], v[96:97], v[100:101], v[114:115] op_sel_hi:[1,0,1]
	v_mov_b32_e32 v100, v175
	v_pk_fma_f32 v[148:149], v[98:99], v[100:101], v[116:117] op_sel_hi:[1,0,1]
	v_pk_fma_f32 v[150:151], v[96:97], v[100:101], v[118:119] op_sel_hi:[1,0,1]
	v_mov_b32_e32 v100, v171
	v_pk_fma_f32 v[152:153], v[98:99], v[100:101], v[120:121] op_sel_hi:[1,0,1]
	v_pk_fma_f32 v[156:157], v[96:97], v[100:101], v[122:123] op_sel_hi:[1,0,1]
	v_mov_b32_e32 v100, v167
	v_pk_fma_f32 v[158:159], v[98:99], v[100:101], v[124:125] op_sel_hi:[1,0,1]
	v_pk_fma_f32 v[160:161], v[96:97], v[100:101], v[126:127] op_sel_hi:[1,0,1]
	v_mov_b32_e32 v100, v163
	v_pk_fma_f32 v[162:163], v[98:99], v[100:101], v[128:129] op_sel_hi:[1,0,1]
	v_pk_fma_f32 v[172:173], v[96:97], v[100:101], v[132:133] op_sel_hi:[1,0,1]
	v_mov_b32_e32 v100, v211
	v_pk_fma_f32 v[120:121], v[98:99], v[100:101], v[134:135] op_sel_hi:[1,0,1]
	v_pk_fma_f32 v[122:123], v[96:97], v[100:101], v[136:137] op_sel_hi:[1,0,1]
	v_mov_b32_e32 v100, v155
	v_pk_fma_f32 v[106:107], v[102:103], v[218:219], v[106:107] op_sel_hi:[1,0,1]
	v_pk_fma_f32 v[114:115], v[98:99], v[100:101], v[138:139] op_sel_hi:[1,0,1]
	v_pk_fma_f32 v[108:109], v[96:97], v[100:101], v[140:141] op_sel_hi:[1,0,1]
	ds_read_b128 v[100:103], v182 offset:96
	v_mov_b32_e32 v112, v219
	v_pk_fma_f32 v[110:111], v[98:99], v[112:113], v[106:107] op_sel_hi:[1,0,1]
	v_pk_fma_f32 v[112:113], v[96:97], v[112:113], v[104:105] op_sel_hi:[1,0,1]
	ds_read_b128 v[96:99], v182 offset:112
	ds_read_b128 v[104:107], v182 offset:8288
	s_waitcnt lgkmcnt(2)
	v_pk_fma_f32 v[116:117], v[94:95], v[100:101], v[130:131] op_sel_hi:[1,0,1]
	ds_read_b128 v[124:127], v182 offset:8304
	ds_read_b128 v[128:131], v182 offset:16480
	ds_read_b128 v[132:135], v182 offset:16496
	ds_read_b128 v[136:139], v182 offset:24672
	v_pk_fma_f32 v[118:119], v[92:93], v[100:101], v[144:145] op_sel_hi:[1,0,1]
	s_waitcnt lgkmcnt(4)
	v_pk_fma_f32 v[188:189], v[94:95], v[104:105], v[142:143] op_sel_hi:[1,0,1]
	v_pk_fma_f32 v[190:191], v[92:93], v[104:105], v[146:147] op_sel_hi:[1,0,1]
	ds_read_b128 v[140:143], v182 offset:24688
	ds_read_b128 v[144:147], v182 offset:32864
	s_waitcnt lgkmcnt(4)
	v_pk_fma_f32 v[192:193], v[94:95], v[128:129], v[148:149] op_sel_hi:[1,0,1]
	v_pk_fma_f32 v[194:195], v[92:93], v[128:129], v[150:151] op_sel_hi:[1,0,1]
	s_waitcnt lgkmcnt(2)
	v_pk_fma_f32 v[196:197], v[94:95], v[136:137], v[152:153] op_sel_hi:[1,0,1]
	ds_read_b128 v[164:167], v182 offset:32880
	ds_read_b128 v[148:151], v182 offset:41056
	ds_read_b128 v[168:171], v182 offset:41072
	ds_read_b128 v[152:155], v182 offset:49248
	s_add_i32 s40, s2, 0x10060
	s_waitcnt lgkmcnt(4)
	v_pk_fma_f32 v[202:203], v[92:93], v[144:145], v[160:161] op_sel_hi:[1,0,1]
	v_mov_b32_e32 v160, s40
	v_pk_fma_f32 v[198:199], v[92:93], v[136:137], v[156:157] op_sel_hi:[1,0,1]
	v_pk_fma_f32 v[200:201], v[94:95], v[144:145], v[158:159] op_sel_hi:[1,0,1]
	s_waitcnt lgkmcnt(2)
	v_pk_fma_f32 v[204:205], v[94:95], v[148:149], v[162:163] op_sel_hi:[1,0,1]
	v_pk_fma_f32 v[206:207], v[92:93], v[148:149], v[172:173] op_sel_hi:[1,0,1]
	ds_read_b128 v[156:159], v182 offset:57440
	ds_read_b128 v[172:175], v182 offset:49264
	s_waitcnt lgkmcnt(2)
	v_pk_fma_f32 v[208:209], v[94:95], v[152:153], v[120:121] op_sel_hi:[1,0,1]
	v_pk_fma_f32 v[210:211], v[92:93], v[152:153], v[122:123] op_sel_hi:[1,0,1]
	ds_read_b128 v[120:123], v182 offset:57456
	ds_read_b128 v[160:163], v160
	s_waitcnt lgkmcnt(3)
	v_pk_fma_f32 v[108:109], v[92:93], v[156:157], v[108:109] op_sel_hi:[1,0,1]
	v_pk_fma_f32 v[114:115], v[94:95], v[156:157], v[114:115] op_sel_hi:[1,0,1]
	v_pk_fma_f32 v[108:109], v[80:81], v[156:157], v[108:109] op_sel:[0,1,0]
	v_pk_fma_f32 v[114:115], v[82:83], v[156:157], v[114:115] op_sel:[0,1,0]
	s_waitcnt lgkmcnt(0)
	v_pk_fma_f32 v[92:93], v[92:93], v[160:161], v[112:113] op_sel_hi:[1,0,1]
	v_pk_fma_f32 v[94:95], v[94:95], v[160:161], v[110:111] op_sel_hi:[1,0,1]
	v_pk_fma_f32 v[110:111], v[82:83], v[100:101], v[116:117] op_sel:[0,1,0]
	v_pk_fma_f32 v[100:101], v[80:81], v[100:101], v[118:119] op_sel:[0,1,0]
	v_pk_fma_f32 v[112:113], v[82:83], v[104:105], v[188:189] op_sel:[0,1,0]
	v_pk_fma_f32 v[104:105], v[80:81], v[104:105], v[190:191] op_sel:[0,1,0]
	v_pk_fma_f32 v[116:117], v[82:83], v[128:129], v[192:193] op_sel:[0,1,0]
	v_pk_fma_f32 v[118:119], v[80:81], v[128:129], v[194:195] op_sel:[0,1,0]
	v_pk_fma_f32 v[128:129], v[82:83], v[136:137], v[196:197] op_sel:[0,1,0]
	v_pk_fma_f32 v[136:137], v[80:81], v[136:137], v[198:199] op_sel:[0,1,0]
	v_pk_fma_f32 v[188:189], v[82:83], v[144:145], v[200:201] op_sel:[0,1,0]
	v_pk_fma_f32 v[144:145], v[80:81], v[144:145], v[202:203] op_sel:[0,1,0]
	v_pk_fma_f32 v[190:191], v[82:83], v[148:149], v[204:205] op_sel:[0,1,0]
	v_pk_fma_f32 v[148:149], v[80:81], v[148:149], v[206:207] op_sel:[0,1,0]
	v_pk_fma_f32 v[192:193], v[82:83], v[152:153], v[208:209] op_sel:[0,1,0]
	v_pk_fma_f32 v[152:153], v[80:81], v[152:153], v[210:211] op_sel:[0,1,0]
	v_pk_fma_f32 v[80:81], v[80:81], v[160:161], v[92:93] op_sel:[0,1,0]
	v_pk_fma_f32 v[82:83], v[82:83], v[160:161], v[94:95] op_sel:[0,1,0]
	v_pk_fma_f32 v[92:93], v[78:79], v[102:103], v[110:111] op_sel_hi:[1,0,1]
	v_pk_fma_f32 v[94:95], v[76:77], v[102:103], v[100:101] op_sel_hi:[1,0,1]
	v_pk_fma_f32 v[100:101], v[78:79], v[106:107], v[112:113] op_sel_hi:[1,0,1]
	v_pk_fma_f32 v[104:105], v[76:77], v[106:107], v[104:105] op_sel_hi:[1,0,1]
	v_pk_fma_f32 v[112:113], v[76:77], v[130:131], v[118:119] op_sel_hi:[1,0,1]
	v_pk_fma_f32 v[118:119], v[76:77], v[138:139], v[136:137] op_sel_hi:[1,0,1]
	v_pk_fma_f32 v[136:137], v[76:77], v[146:147], v[144:145] op_sel_hi:[1,0,1]
	v_pk_fma_f32 v[148:149], v[76:77], v[150:151], v[148:149] op_sel_hi:[1,0,1]
	v_pk_fma_f32 v[152:153], v[76:77], v[154:155], v[152:153] op_sel_hi:[1,0,1]
	v_pk_fma_f32 v[108:109], v[76:77], v[158:159], v[108:109] op_sel_hi:[1,0,1]
	v_pk_fma_f32 v[76:77], v[76:77], v[162:163], v[80:81] op_sel_hi:[1,0,1]
	v_mov_b32_e32 v80, v103
	v_pk_fma_f32 v[110:111], v[78:79], v[130:131], v[116:117] op_sel_hi:[1,0,1]
	v_pk_fma_f32 v[116:117], v[78:79], v[138:139], v[128:129] op_sel_hi:[1,0,1]
	v_pk_fma_f32 v[128:129], v[78:79], v[146:147], v[188:189] op_sel_hi:[1,0,1]
	v_pk_fma_f32 v[144:145], v[78:79], v[150:151], v[190:191] op_sel_hi:[1,0,1]
	v_pk_fma_f32 v[156:157], v[78:79], v[154:155], v[192:193] op_sel_hi:[1,0,1]
	v_pk_fma_f32 v[114:115], v[78:79], v[158:159], v[114:115] op_sel_hi:[1,0,1]
	v_pk_fma_f32 v[78:79], v[78:79], v[162:163], v[82:83] op_sel_hi:[1,0,1]
	v_pk_fma_f32 v[82:83], v[66:67], v[80:81], v[92:93] op_sel_hi:[1,0,1]
	v_mov_b32_e32 v92, v107
	v_pk_fma_f32 v[80:81], v[64:65], v[80:81], v[94:95] op_sel_hi:[1,0,1]
	v_pk_fma_f32 v[94:95], v[66:67], v[92:93], v[100:101] op_sel_hi:[1,0,1]
	v_mov_b32_e32 v100, v131
	v_pk_fma_f32 v[102:103], v[66:67], v[100:101], v[110:111] op_sel_hi:[1,0,1]
	v_mov_b32_e32 v110, v147
	v_pk_fma_f32 v[92:93], v[64:65], v[92:93], v[104:105] op_sel_hi:[1,0,1]
	v_pk_fma_f32 v[100:101], v[64:65], v[100:101], v[112:113] op_sel_hi:[1,0,1]
	v_mov_b32_e32 v104, v139
	v_pk_fma_f32 v[112:113], v[66:67], v[110:111], v[128:129] op_sel_hi:[1,0,1]
	v_pk_fma_f32 v[110:111], v[64:65], v[110:111], v[136:137] op_sel_hi:[1,0,1]
	v_mov_b32_e32 v136, v159
	v_pk_fma_f32 v[106:107], v[66:67], v[104:105], v[116:117] op_sel_hi:[1,0,1]
	v_mov_b32_e32 v116, v151
	v_mov_b32_e32 v128, v155
	v_pk_fma_f32 v[114:115], v[66:67], v[136:137], v[114:115] op_sel_hi:[1,0,1]
	v_pk_fma_f32 v[108:109], v[64:65], v[136:137], v[108:109] op_sel_hi:[1,0,1]
	v_mov_b32_e32 v136, v163
	v_pk_fma_f32 v[104:105], v[64:65], v[104:105], v[118:119] op_sel_hi:[1,0,1]
	v_pk_fma_f32 v[118:119], v[66:67], v[116:117], v[144:145] op_sel_hi:[1,0,1]
	v_pk_fma_f32 v[116:117], v[64:65], v[116:117], v[148:149] op_sel_hi:[1,0,1]
	v_pk_fma_f32 v[130:131], v[66:67], v[128:129], v[156:157] op_sel_hi:[1,0,1]
	v_pk_fma_f32 v[128:129], v[64:65], v[128:129], v[152:153] op_sel_hi:[1,0,1]
	v_pk_fma_f32 v[66:67], v[66:67], v[136:137], v[78:79] op_sel_hi:[1,0,1]
	v_pk_fma_f32 v[64:65], v[64:65], v[136:137], v[76:77] op_sel_hi:[1,0,1]
	v_pk_fma_f32 v[76:77], v[46:47], v[96:97], v[82:83] op_sel_hi:[1,0,1]
	v_pk_fma_f32 v[78:79], v[44:45], v[96:97], v[80:81] op_sel_hi:[1,0,1]
	v_pk_fma_f32 v[76:77], v[42:43], v[96:97], v[76:77] op_sel:[0,1,0]
	v_pk_fma_f32 v[78:79], v[40:41], v[96:97], v[78:79] op_sel:[0,1,0]
	v_pk_fma_f32 v[76:77], v[38:39], v[98:99], v[76:77] op_sel_hi:[1,0,1]
	v_pk_fma_f32 v[78:79], v[36:37], v[98:99], v[78:79] op_sel_hi:[1,0,1]
	v_mov_b32_e32 v80, v99
	v_pk_fma_f32 v[162:163], v[34:35], v[80:81], v[76:77] op_sel_hi:[1,0,1]
	v_pk_fma_f32 v[160:161], v[32:33], v[80:81], v[78:79] op_sel_hi:[1,0,1]
	v_pk_fma_f32 v[76:77], v[46:47], v[124:125], v[94:95] op_sel_hi:[1,0,1]
	v_pk_fma_f32 v[78:79], v[44:45], v[124:125], v[92:93] op_sel_hi:[1,0,1]
	v_pk_fma_f32 v[76:77], v[42:43], v[124:125], v[76:77] op_sel:[0,1,0]
	v_pk_fma_f32 v[78:79], v[40:41], v[124:125], v[78:79] op_sel:[0,1,0]
	v_pk_fma_f32 v[76:77], v[38:39], v[126:127], v[76:77] op_sel_hi:[1,0,1]
	v_pk_fma_f32 v[78:79], v[36:37], v[126:127], v[78:79] op_sel_hi:[1,0,1]
	v_mov_b32_e32 v80, v127
	v_pk_fma_f32 v[158:159], v[34:35], v[80:81], v[76:77] op_sel_hi:[1,0,1]
	v_pk_fma_f32 v[156:157], v[32:33], v[80:81], v[78:79] op_sel_hi:[1,0,1]
	v_pk_fma_f32 v[76:77], v[46:47], v[132:133], v[102:103] op_sel_hi:[1,0,1]
	v_pk_fma_f32 v[78:79], v[44:45], v[132:133], v[100:101] op_sel_hi:[1,0,1]
	v_pk_fma_f32 v[76:77], v[42:43], v[132:133], v[76:77] op_sel:[0,1,0]
	v_pk_fma_f32 v[78:79], v[40:41], v[132:133], v[78:79] op_sel:[0,1,0]
	v_pk_fma_f32 v[76:77], v[38:39], v[134:135], v[76:77] op_sel_hi:[1,0,1]
	v_pk_fma_f32 v[78:79], v[36:37], v[134:135], v[78:79] op_sel_hi:[1,0,1]
	v_mov_b32_e32 v80, v135
	v_pk_fma_f32 v[154:155], v[34:35], v[80:81], v[76:77] op_sel_hi:[1,0,1]
	v_pk_fma_f32 v[152:153], v[32:33], v[80:81], v[78:79] op_sel_hi:[1,0,1]
	v_pk_fma_f32 v[76:77], v[46:47], v[140:141], v[106:107] op_sel_hi:[1,0,1]
	v_pk_fma_f32 v[78:79], v[44:45], v[140:141], v[104:105] op_sel_hi:[1,0,1]
	v_pk_fma_f32 v[76:77], v[42:43], v[140:141], v[76:77] op_sel:[0,1,0]
	v_pk_fma_f32 v[78:79], v[40:41], v[140:141], v[78:79] op_sel:[0,1,0]
	v_pk_fma_f32 v[76:77], v[38:39], v[142:143], v[76:77] op_sel_hi:[1,0,1]
	v_pk_fma_f32 v[78:79], v[36:37], v[142:143], v[78:79] op_sel_hi:[1,0,1]
	v_mov_b32_e32 v80, v143
	v_pk_fma_f32 v[150:151], v[34:35], v[80:81], v[76:77] op_sel_hi:[1,0,1]
	v_pk_fma_f32 v[148:149], v[32:33], v[80:81], v[78:79] op_sel_hi:[1,0,1]
	v_pk_fma_f32 v[76:77], v[46:47], v[164:165], v[112:113] op_sel_hi:[1,0,1]
	v_pk_fma_f32 v[78:79], v[44:45], v[164:165], v[110:111] op_sel_hi:[1,0,1]
	v_pk_fma_f32 v[76:77], v[42:43], v[164:165], v[76:77] op_sel:[0,1,0]
	v_pk_fma_f32 v[78:79], v[40:41], v[164:165], v[78:79] op_sel:[0,1,0]
	s_add_i32 s2, s2, 0x10070
	v_pk_fma_f32 v[76:77], v[38:39], v[166:167], v[76:77] op_sel_hi:[1,0,1]
	v_pk_fma_f32 v[78:79], v[36:37], v[166:167], v[78:79] op_sel_hi:[1,0,1]
	v_mov_b32_e32 v80, v167
	v_mov_b32_e32 v182, s2
	v_pk_fma_f32 v[146:147], v[34:35], v[80:81], v[76:77] op_sel_hi:[1,0,1]
	v_pk_fma_f32 v[144:145], v[32:33], v[80:81], v[78:79] op_sel_hi:[1,0,1]
	v_pk_fma_f32 v[76:77], v[46:47], v[168:169], v[118:119] op_sel_hi:[1,0,1]
	v_pk_fma_f32 v[78:79], v[44:45], v[168:169], v[116:117] op_sel_hi:[1,0,1]
	ds_read_b128 v[182:185], v182
	v_pk_fma_f32 v[76:77], v[42:43], v[168:169], v[76:77] op_sel:[0,1,0]
	v_pk_fma_f32 v[78:79], v[40:41], v[168:169], v[78:79] op_sel:[0,1,0]
	v_pk_fma_f32 v[76:77], v[38:39], v[170:171], v[76:77] op_sel_hi:[1,0,1]
	v_pk_fma_f32 v[78:79], v[36:37], v[170:171], v[78:79] op_sel_hi:[1,0,1]
	v_mov_b32_e32 v80, v171
	v_pk_fma_f32 v[142:143], v[34:35], v[80:81], v[76:77] op_sel_hi:[1,0,1]
	v_pk_fma_f32 v[140:141], v[32:33], v[80:81], v[78:79] op_sel_hi:[1,0,1]
	v_pk_fma_f32 v[76:77], v[46:47], v[172:173], v[130:131] op_sel_hi:[1,0,1]
	v_pk_fma_f32 v[78:79], v[44:45], v[172:173], v[128:129] op_sel_hi:[1,0,1]
	v_pk_fma_f32 v[76:77], v[42:43], v[172:173], v[76:77] op_sel:[0,1,0]
	v_pk_fma_f32 v[78:79], v[40:41], v[172:173], v[78:79] op_sel:[0,1,0]
	v_pk_fma_f32 v[76:77], v[38:39], v[174:175], v[76:77] op_sel_hi:[1,0,1]
	v_pk_fma_f32 v[78:79], v[36:37], v[174:175], v[78:79] op_sel_hi:[1,0,1]
	v_mov_b32_e32 v80, v175
	v_pk_fma_f32 v[138:139], v[34:35], v[80:81], v[76:77] op_sel_hi:[1,0,1]
	v_pk_fma_f32 v[136:137], v[32:33], v[80:81], v[78:79] op_sel_hi:[1,0,1]
	v_pk_fma_f32 v[76:77], v[46:47], v[120:121], v[114:115] op_sel_hi:[1,0,1]
	v_pk_fma_f32 v[78:79], v[44:45], v[120:121], v[108:109] op_sel_hi:[1,0,1]
	s_waitcnt lgkmcnt(0)
	v_pk_fma_f32 v[46:47], v[46:47], v[182:183], v[66:67] op_sel_hi:[1,0,1]
	v_pk_fma_f32 v[44:45], v[44:45], v[182:183], v[64:65] op_sel_hi:[1,0,1]
	v_pk_fma_f32 v[76:77], v[42:43], v[120:121], v[76:77] op_sel:[0,1,0]
	v_pk_fma_f32 v[78:79], v[40:41], v[120:121], v[78:79] op_sel:[0,1,0]
	v_pk_fma_f32 v[42:43], v[42:43], v[182:183], v[46:47] op_sel:[0,1,0]
	v_pk_fma_f32 v[40:41], v[40:41], v[182:183], v[44:45] op_sel:[0,1,0]
	v_pk_fma_f32 v[76:77], v[38:39], v[122:123], v[76:77] op_sel_hi:[1,0,1]
	v_pk_fma_f32 v[78:79], v[36:37], v[122:123], v[78:79] op_sel_hi:[1,0,1]
	v_mov_b32_e32 v80, v123
	v_pk_fma_f32 v[38:39], v[38:39], v[184:185], v[42:43] op_sel_hi:[1,0,1]
	v_pk_fma_f32 v[36:37], v[36:37], v[184:185], v[40:41] op_sel_hi:[1,0,1]
	v_mov_b32_e32 v40, v185
	v_pk_fma_f32 v[134:135], v[34:35], v[80:81], v[76:77] op_sel_hi:[1,0,1]
	v_pk_fma_f32 v[132:133], v[32:33], v[80:81], v[78:79] op_sel_hi:[1,0,1]
	v_pk_fma_f32 v[130:131], v[34:35], v[40:41], v[38:39] op_sel_hi:[1,0,1]
	s_cmp_lg_u32 s11, 6
	v_pk_fma_f32 v[128:129], v[32:33], v[40:41], v[36:37] op_sel_hi:[1,0,1]
	s_cbranch_scc1 .LBB0_167
	s_ashr_i32 s11, s10, 31
	s_lshl_b64 s[10:11], s[10:11], 2
	s_add_u32 s2, s10, s12
	s_addc_u32 s12, s11, s13
	v_lshl_add_u64 v[32:33], s[14:15], 2, v[180:181]
	v_mad_u64_u32 v[32:33], s[10:11], s2, v187, v[32:33]
	s_mul_i32 s12, s12, 0x6c000
	v_add_u32_e32 v33, s12, v33
	v_add_co_u32_e32 v34, vcc, s17, v32
	global_store_dwordx4 v[32:33], v[160:163], off
	s_nop 0
	v_addc_co_u32_e32 v35, vcc, 0, v33, vcc
	global_store_dwordx4 v[34:35], v[156:159], off
	v_add_co_u32_e32 v34, vcc, 0x18000, v32
	s_nop 1
	v_addc_co_u32_e32 v35, vcc, 0, v33, vcc
	global_store_dwordx4 v[34:35], v[152:155], off
	v_add_co_u32_e32 v34, vcc, 0x24000, v32
	s_nop 1
	v_addc_co_u32_e32 v35, vcc, 0, v33, vcc
	global_store_dwordx4 v[34:35], v[148:151], off
	v_add_co_u32_e32 v34, vcc, 0x30000, v32
	s_nop 1
	v_addc_co_u32_e32 v35, vcc, 0, v33, vcc
	global_store_dwordx4 v[34:35], v[144:147], off
	v_add_co_u32_e32 v34, vcc, 0x3c000, v32
	s_nop 1
	v_addc_co_u32_e32 v35, vcc, 0, v33, vcc
	global_store_dwordx4 v[34:35], v[140:143], off
	v_add_co_u32_e32 v34, vcc, 0x48000, v32
	s_nop 1
	v_addc_co_u32_e32 v35, vcc, 0, v33, vcc
	global_store_dwordx4 v[34:35], v[136:139], off
	v_add_co_u32_e32 v34, vcc, 0x54000, v32
	s_nop 1
	v_addc_co_u32_e32 v35, vcc, 0, v33, vcc
	v_add_co_u32_e32 v32, vcc, 0x60000, v32
	global_store_dwordx4 v[34:35], v[132:135], off
	s_nop 0
	v_addc_co_u32_e32 v33, vcc, 0, v33, vcc
	global_store_dwordx4 v[32:33], v[128:131], off
	s_nop 1
	v_mov_b32_e32 v128, 0
	v_mov_b32_e32 v129, v128
	v_mov_b32_e32 v130, v128
	v_mov_b32_e32 v131, v128
	v_mov_b32_e32 v132, v128
	v_mov_b32_e32 v133, v128
	v_mov_b32_e32 v134, v128
	v_mov_b32_e32 v135, v128
	v_mov_b32_e32 v136, v128
	v_mov_b32_e32 v137, v128
	v_mov_b32_e32 v138, v128
	v_mov_b32_e32 v139, v128
	v_mov_b32_e32 v140, v128
	v_mov_b32_e32 v141, v128
	v_mov_b32_e32 v142, v128
	v_mov_b32_e32 v143, v128
	v_mov_b32_e32 v144, v128
	v_mov_b32_e32 v145, v128
	v_mov_b32_e32 v146, v128
	v_mov_b32_e32 v147, v128
	v_mov_b32_e32 v148, v128
	v_mov_b32_e32 v149, v128
	v_mov_b32_e32 v150, v128
	v_mov_b32_e32 v151, v128
	v_mov_b32_e32 v152, v128
	v_mov_b32_e32 v153, v128
	v_mov_b32_e32 v154, v128
	v_mov_b32_e32 v155, v128
	v_mov_b32_e32 v156, v128
	v_mov_b32_e32 v157, v128
	v_mov_b32_e32 v158, v128
	v_mov_b32_e32 v159, v128
	v_mov_b32_e32 v160, v128
	v_mov_b32_e32 v161, v128
	v_mov_b32_e32 v162, v128
	v_mov_b32_e32 v163, v128
	s_branch .LBB0_167

.LBB0_215:
	v_lshl_add_u64 v[64:65], s[24:25], 0, v[2:3]
	v_mul_u32_u24_e32 v2, s22, v1
	v_lshlrev_b32_e32 v2, 2, v2
	v_lshl_add_u64 v[40:41], v[64:65], 0, v[2:3]
	v_mul_u32_u24_e32 v2, s22, v6
	v_lshlrev_b32_e32 v2, 2, v2
	v_lshl_add_u64 v[42:43], v[64:65], 0, v[2:3]
	v_mul_u32_u24_e32 v2, s22, v7
	v_lshlrev_b32_e32 v2, 2, v2
	v_lshl_add_u64 v[44:45], v[64:65], 0, v[2:3]
	v_mul_u32_u24_e32 v2, s22, v8
	v_lshlrev_b32_e32 v2, 2, v2
	v_lshl_add_u64 v[46:47], v[64:65], 0, v[2:3]
	v_mul_u32_u24_e32 v2, s22, v9
	v_lshlrev_b32_e32 v2, 2, v2
	v_lshl_add_u64 v[48:49], v[64:65], 0, v[2:3]
	v_mul_u32_u24_e32 v2, s22, v10
	v_lshlrev_b32_e32 v2, 2, v2
	v_lshl_add_u64 v[50:51], v[64:65], 0, v[2:3]
	v_mul_u32_u24_e32 v2, s22, v11
	v_lshlrev_b32_e32 v2, 2, v2
	v_lshl_add_u64 v[52:53], v[64:65], 0, v[2:3]
	v_mul_u32_u24_e32 v2, s22, v12
	v_lshlrev_b32_e32 v2, 2, v2
	v_lshl_add_u64 v[54:55], v[64:65], 0, v[2:3]
	v_mul_u32_u24_e32 v2, s22, v13
	v_lshlrev_b32_e32 v2, 2, v2
	global_load_dword v40, v[40:41], off nt
	s_nop 0
	global_load_dword v41, v[42:43], off nt
	s_nop 0
	global_load_dword v42, v[44:45], off nt
	s_nop 0
	global_load_dword v44, v[46:47], off nt
	global_load_dword v43, v[48:49], off nt
	global_load_dword v45, v[50:51], off nt
	s_nop 0
	global_load_dword v46, v[52:53], off nt
	global_load_dword v47, v[54:55], off nt
	v_lshl_add_u64 v[48:49], v[64:65], 0, v[2:3]
	v_mul_u32_u24_e32 v2, s22, v14
	v_lshlrev_b32_e32 v2, 2, v2
	v_lshl_add_u64 v[50:51], v[64:65], 0, v[2:3]
	v_mul_u32_u24_e32 v2, s22, v15
	v_lshlrev_b32_e32 v2, 2, v2
	v_lshl_add_u64 v[52:53], v[64:65], 0, v[2:3]
	v_mul_u32_u24_e32 v2, s22, v16
	v_lshlrev_b32_e32 v2, 2, v2
	v_lshl_add_u64 v[54:55], v[64:65], 0, v[2:3]
	v_mul_u32_u24_e32 v2, s22, v17
	v_lshlrev_b32_e32 v2, 2, v2
	v_lshl_add_u64 v[56:57], v[64:65], 0, v[2:3]
	v_mul_u32_u24_e32 v2, s22, v18
	v_lshlrev_b32_e32 v2, 2, v2
	v_lshl_add_u64 v[58:59], v[64:65], 0, v[2:3]
	v_mul_u32_u24_e32 v2, s22, v19
	v_lshlrev_b32_e32 v2, 2, v2
	v_lshl_add_u64 v[60:61], v[64:65], 0, v[2:3]
	v_mul_u32_u24_e32 v2, s22, v20
	v_lshlrev_b32_e32 v2, 2, v2
	v_lshl_add_u64 v[62:63], v[64:65], 0, v[2:3]
	v_mul_u32_u24_e32 v2, s22, v21
	v_lshlrev_b32_e32 v2, 2, v2
	global_load_dword v48, v[48:49], off nt
	s_nop 0
	global_load_dword v49, v[50:51], off nt
	s_nop 0
	global_load_dword v50, v[52:53], off nt
	s_nop 0
	global_load_dword v52, v[54:55], off nt
	global_load_dword v51, v[56:57], off nt
	global_load_dword v53, v[58:59], off nt
	s_nop 0
	global_load_dword v54, v[60:61], off nt
	global_load_dword v55, v[62:63], off nt
	v_lshl_add_u64 v[56:57], v[64:65], 0, v[2:3]
	v_mul_u32_u24_e32 v2, s22, v22
	v_lshlrev_b32_e32 v2, 2, v2
	v_lshl_add_u64 v[58:59], v[64:65], 0, v[2:3]
	v_mul_u32_u24_e32 v2, s22, v23
	v_lshlrev_b32_e32 v2, 2, v2
	v_lshl_add_u64 v[60:61], v[64:65], 0, v[2:3]
	v_mul_u32_u24_e32 v2, s22, v24
	v_lshlrev_b32_e32 v2, 2, v2
	v_lshl_add_u64 v[62:63], v[64:65], 0, v[2:3]
	v_mul_u32_u24_e32 v2, s22, v25
	v_lshlrev_b32_e32 v2, 2, v2
	v_lshl_add_u64 v[66:67], v[64:65], 0, v[2:3]
	v_mul_u32_u24_e32 v2, s22, v26
	v_lshlrev_b32_e32 v2, 2, v2
	v_lshl_add_u64 v[68:69], v[64:65], 0, v[2:3]
	v_mul_u32_u24_e32 v2, s22, v27
	v_lshlrev_b32_e32 v2, 2, v2
	v_lshl_add_u64 v[70:71], v[64:65], 0, v[2:3]
	v_mul_u32_u24_e32 v2, s22, v28
	v_lshlrev_b32_e32 v2, 2, v2
	v_lshl_add_u64 v[112:113], v[64:65], 0, v[2:3]
	v_mul_u32_u24_e32 v2, s22, v29
	v_lshlrev_b32_e32 v2, 2, v2
	global_load_dword v56, v[56:57], off nt
	s_nop 0
	global_load_dword v57, v[58:59], off nt
	s_nop 0
	global_load_dword v58, v[60:61], off nt
	s_nop 0
	global_load_dword v60, v[62:63], off nt
	global_load_dword v59, v[66:67], off nt
	global_load_dword v61, v[68:69], off nt
	s_nop 0
	global_load_dword v62, v[70:71], off nt
	global_load_dword v63, v[112:113], off nt
	v_lshl_add_u64 v[66:67], v[64:65], 0, v[2:3]
	v_mul_u32_u24_e32 v2, s22, v30
	v_lshlrev_b32_e32 v2, 2, v2
	v_lshl_add_u64 v[68:69], v[64:65], 0, v[2:3]
	v_mul_u32_u24_e32 v2, s22, v31
	v_lshlrev_b32_e32 v2, 2, v2
	v_lshl_add_u64 v[70:71], v[64:65], 0, v[2:3]
	v_mul_u32_u24_e32 v2, s22, v32
	v_lshlrev_b32_e32 v2, 2, v2
	v_lshl_add_u64 v[112:113], v[64:65], 0, v[2:3]
	v_mul_u32_u24_e32 v2, s22, v33
	v_lshlrev_b32_e32 v2, 2, v2
	v_lshl_add_u64 v[114:115], v[64:65], 0, v[2:3]
	v_mul_u32_u24_e32 v2, s22, v34
	v_lshlrev_b32_e32 v2, 2, v2
	v_lshl_add_u64 v[116:117], v[64:65], 0, v[2:3]
	v_mul_u32_u24_e32 v2, s22, v35
	v_lshlrev_b32_e32 v2, 2, v2
	v_lshl_add_u64 v[118:119], v[64:65], 0, v[2:3]
	v_mul_u32_u24_e32 v2, s22, v36
	v_lshlrev_b32_e32 v2, 2, v2
	v_lshl_add_u64 v[120:121], v[64:65], 0, v[2:3]
	global_load_dword v64, v[66:67], off nt
	global_load_dword v65, v[68:69], off nt
	s_nop 0
	global_load_dword v66, v[70:71], off nt
	global_load_dword v68, v[112:113], off nt
	global_load_dword v67, v[114:115], off nt
	global_load_dword v69, v[116:117], off nt
	s_nop 0
	global_load_dword v70, v[118:119], off nt
	global_load_dword v71, v[120:121], off nt
	s_waitcnt vmcnt(62)
	ds_write2_b32 v39, v72, v73 offset1:66
	ds_write2_b32 v39, v74, v75 offset0:132 offset1:198
	ds_write2_b32 v104, v76, v77 offset0:8 offset1:74
	s_waitcnt vmcnt(60)
	ds_write2_b32 v104, v78, v79 offset0:140 offset1:206
	s_waitcnt vmcnt(58)
	ds_write2_b32 v105, v80, v81 offset0:16 offset1:82
	s_waitcnt vmcnt(56)
	ds_write2_b32 v105, v82, v83 offset0:148 offset1:214
	s_waitcnt vmcnt(54)
	ds_write2_b32 v106, v84, v85 offset0:24 offset1:90
	s_waitcnt vmcnt(52)
	ds_write2_b32 v106, v86, v87 offset0:156 offset1:222
	s_waitcnt vmcnt(50)
	ds_write2_b32 v107, v88, v89 offset0:32 offset1:98
	s_waitcnt vmcnt(48)
	ds_write2_b32 v107, v90, v91 offset0:164 offset1:230
	s_waitcnt vmcnt(46)
	ds_write2_b32 v108, v92, v93 offset0:40 offset1:106
	s_waitcnt vmcnt(44)
	ds_write2_b32 v108, v94, v95 offset0:172 offset1:238
	s_waitcnt vmcnt(42)
	ds_write2_b32 v109, v96, v97 offset0:48 offset1:114
	s_waitcnt vmcnt(40)
	ds_write2_b32 v109, v98, v99 offset0:180 offset1:246
	s_waitcnt vmcnt(38)
	ds_write2_b32 v110, v100, v101 offset0:56 offset1:122
	s_waitcnt vmcnt(36)
	ds_write2_b32 v110, v102, v103 offset0:188 offset1:254
	s_waitcnt lgkmcnt(0)
	ds_read2_b32 v[72:73], v38 offset1:33
	s_waitcnt lgkmcnt(0)
	v_cvt_pk_bf16_f32 v72, v72, v73
	ds_read2_b32 v[74:75], v38 offset0:66 offset1:99
	s_waitcnt lgkmcnt(0)
	v_cvt_pk_bf16_f32 v73, v74, v75
	ds_read2_b32 v[74:75], v38 offset0:132 offset1:165
	s_waitcnt lgkmcnt(0)
	v_cvt_pk_bf16_f32 v74, v74, v75
	ds_read2_b32 v[76:77], v38 offset0:198 offset1:231
	v_mul_u32_u24_e32 v5, s55, v37
	s_waitcnt lgkmcnt(0)
	v_cvt_pk_bf16_f32 v75, v76, v77
	v_mad_u64_u32 v[76:77], s[22:23], s16, v5, 0
	v_mov_b32_e32 v2, v77
	v_mad_u64_u32 v[78:79], s[22:23], s17, v5, v[2:3]
	v_mov_b32_e32 v77, v78
	v_lshl_add_u64 v[76:77], v[76:77], 1, s[14:15]
	v_mov_b32_e32 v5, v3
	v_lshl_add_u64 v[76:77], v[76:77], 0, v[4:5]
	ds_read2_b32 v[78:79], v38 offset0:8 offset1:41
	global_store_dwordx4 v[76:77], v[72:75], off nt
	s_lshl_b32 s2, s55, 3
	v_mov_b32_e32 v2, s2
	s_waitcnt lgkmcnt(0)
	v_cvt_pk_bf16_f32 v72, v78, v79
	ds_read2_b32 v[74:75], v38 offset0:74 offset1:107
	s_waitcnt lgkmcnt(0)
	v_cvt_pk_bf16_f32 v73, v74, v75
	ds_read2_b32 v[74:75], v38 offset0:140 offset1:173
	s_waitcnt lgkmcnt(0)
	v_cvt_pk_bf16_f32 v74, v74, v75
	ds_read2_b32 v[76:77], v38 offset0:206 offset1:239
	v_mad_u32_u24 v82, s55, v37, v2
	s_waitcnt lgkmcnt(0)
	v_cvt_pk_bf16_f32 v75, v76, v77
	v_mad_u64_u32 v[76:77], s[22:23], s16, v82, 0
	v_mov_b32_e32 v2, v77
	v_mad_u64_u32 v[78:79], s[22:23], s17, v82, v[2:3]
	v_mov_b32_e32 v77, v78
	v_lshl_add_u64 v[76:77], v[76:77], 1, s[14:15]
	v_lshl_add_u64 v[76:77], v[76:77], 0, v[4:5]
	ds_read2_b32 v[80:81], v38 offset0:16 offset1:49
	global_store_dwordx4 v[76:77], v[72:75], off nt
	v_add_u32_e32 v82, s2, v82
	s_waitcnt lgkmcnt(0)
	v_cvt_pk_bf16_f32 v72, v80, v81
	ds_read2_b32 v[74:75], v38 offset0:82 offset1:115
	s_waitcnt lgkmcnt(0)
	v_cvt_pk_bf16_f32 v73, v74, v75
	ds_read2_b32 v[74:75], v38 offset0:148 offset1:181
	s_waitcnt lgkmcnt(0)
	v_cvt_pk_bf16_f32 v74, v74, v75
	ds_read2_b32 v[76:77], v38 offset0:214 offset1:247
	s_waitcnt lgkmcnt(0)
	v_cvt_pk_bf16_f32 v75, v76, v77
	v_mad_u64_u32 v[76:77], s[22:23], s16, v82, 0
	v_mov_b32_e32 v2, v77
	v_mad_u64_u32 v[78:79], s[22:23], s17, v82, v[2:3]
	v_mov_b32_e32 v77, v78
	v_lshl_add_u64 v[76:77], v[76:77], 1, s[14:15]
	v_lshl_add_u64 v[76:77], v[76:77], 0, v[4:5]
	ds_read2_b32 v[80:81], v38 offset0:24 offset1:57
	global_store_dwordx4 v[76:77], v[72:75], off nt
	v_add_u32_e32 v78, s2, v82
	s_waitcnt lgkmcnt(0)
	v_cvt_pk_bf16_f32 v72, v80, v81
	ds_read2_b32 v[74:75], v38 offset0:90 offset1:123
	s_waitcnt lgkmcnt(0)
	v_cvt_pk_bf16_f32 v73, v74, v75
	ds_read2_b32 v[74:75], v38 offset0:156 offset1:189
	s_waitcnt lgkmcnt(0)
	v_cvt_pk_bf16_f32 v74, v74, v75
	ds_read2_b32 v[76:77], v38 offset0:222 offset1:255
	s_waitcnt lgkmcnt(0)
	v_cvt_pk_bf16_f32 v75, v76, v77
	v_mad_u64_u32 v[76:77], s[22:23], s16, v78, 0
	v_mov_b32_e32 v2, v77
	v_mad_u64_u32 v[78:79], s[16:17], s17, v78, v[2:3]
	v_mov_b32_e32 v77, v78
	v_lshl_add_u64 v[76:77], v[76:77], 1, s[14:15]
	v_lshl_add_u64 v[76:77], v[76:77], 0, v[4:5]
	global_store_dwordx4 v[76:77], v[72:75], off nt
.LBB0_216:
	s_and_b64 vcc, exec, s[20:21]
	s_mov_b32 s56, s57
	s_cbranch_vccnz .LBB0_302

.LBB0_258:
	v_mul_u32_u24_e32 v5, s22, v1
	s_waitcnt vmcnt(35)
	v_lshlrev_b32_e32 v72, 2, v5
	v_mul_u32_u24_e32 v5, s22, v6
	s_waitcnt vmcnt(33)
	v_lshlrev_b32_e32 v74, 2, v5
	v_mul_u32_u24_e32 v5, s22, v7
	s_waitcnt vmcnt(31)
	v_lshlrev_b32_e32 v76, 2, v5
	v_mul_u32_u24_e32 v5, s22, v8
	s_waitcnt vmcnt(29)
	v_lshlrev_b32_e32 v78, 2, v5
	v_mul_u32_u24_e32 v5, s22, v9
	s_waitcnt vmcnt(27)
	v_lshlrev_b32_e32 v80, 2, v5
	v_mul_u32_u24_e32 v5, s22, v10
	v_lshlrev_b32_e32 v2, 2, v0
	s_waitcnt vmcnt(25)
	v_lshlrev_b32_e32 v82, 2, v5
	v_mul_u32_u24_e32 v5, s22, v11
	s_waitcnt vmcnt(10)
	v_lshl_add_u64 v[96:97], s[24:25], 0, v[2:3]
	v_mov_b32_e32 v73, v3
	v_mov_b32_e32 v75, v3
	v_mov_b32_e32 v77, v3
	v_mov_b32_e32 v79, v3
	v_mov_b32_e32 v81, v3
	v_lshlrev_b32_e32 v84, 2, v5
	v_mul_u32_u24_e32 v5, s22, v12
	v_lshl_add_u64 v[72:73], v[96:97], 0, v[72:73]
	v_lshl_add_u64 v[74:75], v[96:97], 0, v[74:75]
	v_lshl_add_u64 v[76:77], v[96:97], 0, v[76:77]
	v_lshl_add_u64 v[78:79], v[96:97], 0, v[78:79]
	v_lshl_add_u64 v[80:81], v[96:97], 0, v[80:81]
	v_mov_b32_e32 v83, v3
	v_mov_b32_e32 v85, v3
	v_lshlrev_b32_e32 v86, 2, v5
	v_mov_b32_e32 v87, v3
	v_mul_u32_u24_e32 v5, s22, v13
	v_lshl_add_u64 v[82:83], v[96:97], 0, v[82:83]
	v_lshl_add_u64 v[84:85], v[96:97], 0, v[84:85]
	v_lshl_add_u64 v[86:87], v[96:97], 0, v[86:87]
	global_load_dword v72, v[72:73], off nt
	s_nop 0
	global_load_dword v73, v[74:75], off nt
	s_nop 0
	global_load_dword v74, v[76:77], off nt
	global_load_dword v75, v[78:79], off nt
	s_nop 0
	global_load_dword v76, v[80:81], off nt
	global_load_dword v77, v[82:83], off nt
	global_load_dword v78, v[84:85], off nt
	global_load_dword v79, v[86:87], off nt
	v_lshlrev_b32_e32 v80, 2, v5
	v_mul_u32_u24_e32 v5, s22, v14
	v_lshlrev_b32_e32 v82, 2, v5
	v_mul_u32_u24_e32 v5, s22, v15
	v_lshlrev_b32_e32 v84, 2, v5
	v_mul_u32_u24_e32 v5, s22, v16
	v_lshlrev_b32_e32 v86, 2, v5
	v_mul_u32_u24_e32 v5, s22, v17
	v_lshlrev_b32_e32 v88, 2, v5
	v_mul_u32_u24_e32 v5, s22, v18
	v_lshlrev_b32_e32 v90, 2, v5
	v_mul_u32_u24_e32 v5, s22, v19
	v_mov_b32_e32 v81, v3
	v_mov_b32_e32 v83, v3
	v_mov_b32_e32 v85, v3
	v_mov_b32_e32 v87, v3
	v_mov_b32_e32 v89, v3
	v_lshlrev_b32_e32 v92, 2, v5
	v_mul_u32_u24_e32 v5, s22, v20
	v_lshl_add_u64 v[80:81], v[96:97], 0, v[80:81]
	v_lshl_add_u64 v[82:83], v[96:97], 0, v[82:83]
	v_lshl_add_u64 v[84:85], v[96:97], 0, v[84:85]
	v_lshl_add_u64 v[86:87], v[96:97], 0, v[86:87]
	v_lshl_add_u64 v[88:89], v[96:97], 0, v[88:89]
	v_mov_b32_e32 v91, v3
	v_mov_b32_e32 v93, v3
	v_lshlrev_b32_e32 v94, 2, v5
	v_mov_b32_e32 v95, v3
	v_mul_u32_u24_e32 v5, s22, v21
	v_lshl_add_u64 v[90:91], v[96:97], 0, v[90:91]
	v_lshl_add_u64 v[92:93], v[96:97], 0, v[92:93]
	v_lshl_add_u64 v[94:95], v[96:97], 0, v[94:95]
	global_load_dword v80, v[80:81], off nt
	s_nop 0
	global_load_dword v81, v[82:83], off nt
	s_nop 0
	global_load_dword v82, v[84:85], off nt
	global_load_dword v83, v[86:87], off nt
	s_nop 0
	global_load_dword v84, v[88:89], off nt
	global_load_dword v85, v[90:91], off nt
	global_load_dword v86, v[92:93], off nt
	global_load_dword v87, v[94:95], off nt
	v_lshlrev_b32_e32 v88, 2, v5
	v_mul_u32_u24_e32 v5, s22, v22
	v_lshlrev_b32_e32 v90, 2, v5
	v_mul_u32_u24_e32 v5, s22, v23
	v_lshlrev_b32_e32 v92, 2, v5
	v_mul_u32_u24_e32 v5, s22, v24
	v_lshlrev_b32_e32 v94, 2, v5
	v_mul_u32_u24_e32 v5, s22, v25
	s_waitcnt vmcnt(25)
	v_lshlrev_b32_e32 v98, 2, v5
	v_mul_u32_u24_e32 v5, s22, v26
	s_waitcnt vmcnt(23)
	v_lshlrev_b32_e32 v100, 2, v5
	v_mul_u32_u24_e32 v5, s22, v27
	v_mov_b32_e32 v89, v3
	v_mov_b32_e32 v91, v3
	v_mov_b32_e32 v93, v3
	v_mov_b32_e32 v95, v3
	v_mov_b32_e32 v99, v3
	s_waitcnt vmcnt(21)
	v_lshlrev_b32_e32 v102, 2, v5
	v_mul_u32_u24_e32 v5, s22, v28
	v_lshl_add_u64 v[88:89], v[96:97], 0, v[88:89]
	v_lshl_add_u64 v[90:91], v[96:97], 0, v[90:91]
	v_lshl_add_u64 v[92:93], v[96:97], 0, v[92:93]
	v_lshl_add_u64 v[94:95], v[96:97], 0, v[94:95]
	v_lshl_add_u64 v[98:99], v[96:97], 0, v[98:99]
	v_mov_b32_e32 v101, v3
	s_waitcnt vmcnt(20)
	v_mov_b32_e32 v103, v3
	v_lshlrev_b32_e32 v104, 2, v5
	v_mov_b32_e32 v105, v3
	v_mul_u32_u24_e32 v5, s22, v29
	v_lshl_add_u64 v[100:101], v[96:97], 0, v[100:101]
	v_lshl_add_u64 v[102:103], v[96:97], 0, v[102:103]
	v_lshl_add_u64 v[104:105], v[96:97], 0, v[104:105]
	global_load_dword v88, v[88:89], off nt
	s_nop 0
	global_load_dword v89, v[90:91], off nt
	s_nop 0
	global_load_dword v90, v[92:93], off nt
	global_load_dword v91, v[94:95], off nt
	s_nop 0
	global_load_dword v92, v[98:99], off nt
	global_load_dword v93, v[100:101], off nt
	global_load_dword v94, v[102:103], off nt
	global_load_dword v95, v[104:105], off nt
	v_lshlrev_b32_e32 v98, 2, v5
	v_mul_u32_u24_e32 v5, s22, v30
	v_lshlrev_b32_e32 v100, 2, v5
	v_mul_u32_u24_e32 v5, s22, v31
	v_lshlrev_b32_e32 v102, 2, v5
	v_mul_u32_u24_e32 v5, s22, v32
	v_lshlrev_b32_e32 v104, 2, v5
	v_mul_u32_u24_e32 v5, s22, v33
	v_lshlrev_b32_e32 v106, 2, v5
	v_mul_u32_u24_e32 v5, s22, v34
	v_lshlrev_b32_e32 v108, 2, v5
	v_mul_u32_u24_e32 v5, s22, v35
	v_mov_b32_e32 v99, v3
	v_mov_b32_e32 v101, v3
	v_mov_b32_e32 v103, v3
	v_lshlrev_b32_e32 v110, 2, v5
	v_mul_u32_u24_e32 v5, s22, v36
	v_lshl_add_u64 v[98:99], v[96:97], 0, v[98:99]
	v_lshl_add_u64 v[100:101], v[96:97], 0, v[100:101]
	v_lshl_add_u64 v[102:103], v[96:97], 0, v[102:103]
	v_mov_b32_e32 v105, v3
	v_mov_b32_e32 v107, v3
	v_mov_b32_e32 v109, v3
	v_mov_b32_e32 v111, v3
	v_lshlrev_b32_e32 v112, 2, v5
	v_mov_b32_e32 v113, v3
	v_lshl_add_u64 v[104:105], v[96:97], 0, v[104:105]
	v_lshl_add_u64 v[106:107], v[96:97], 0, v[106:107]
	v_lshl_add_u64 v[108:109], v[96:97], 0, v[108:109]
	v_lshl_add_u64 v[110:111], v[96:97], 0, v[110:111]
	v_lshl_add_u64 v[112:113], v[96:97], 0, v[112:113]
	global_load_dword v96, v[98:99], off nt
	global_load_dword v97, v[100:101], off nt
	s_nop 0
	global_load_dword v98, v[102:103], off nt
	global_load_dword v99, v[104:105], off nt
	global_load_dword v100, v[106:107], off nt
	global_load_dword v101, v[108:109], off nt
	s_nop 0
	global_load_dword v102, v[110:111], off nt
	global_load_dword v103, v[112:113], off nt
	v_add_u32_e32 v104, 0x400, v39
	v_add_u32_e32 v105, 0x800, v39
	v_add_u32_e32 v106, 0xc00, v39
	v_add_u32_e32 v107, 0x1000, v39
	v_add_u32_e32 v108, 0x1400, v39
	v_add_u32_e32 v109, 0x1800, v39
	v_add_u32_e32 v110, 0x1c00, v39
	ds_write2_b32 v39, v40, v41 offset1:66
	ds_write2_b32 v39, v42, v44 offset0:132 offset1:198
	ds_write2_b32 v104, v43, v45 offset0:8 offset1:74
	ds_write2_b32 v104, v46, v47 offset0:140 offset1:206
	ds_write2_b32 v105, v48, v49 offset0:16 offset1:82
	ds_write2_b32 v105, v50, v52 offset0:148 offset1:214
	ds_write2_b32 v106, v51, v53 offset0:24 offset1:90
	ds_write2_b32 v106, v54, v55 offset0:156 offset1:222
	ds_write2_b32 v107, v56, v57 offset0:32 offset1:98
	ds_write2_b32 v107, v58, v60 offset0:164 offset1:230
	ds_write2_b32 v108, v59, v61 offset0:40 offset1:106
	ds_write2_b32 v108, v62, v63 offset0:172 offset1:238
	ds_write2_b32 v109, v64, v65 offset0:48 offset1:114
	ds_write2_b32 v109, v66, v68 offset0:180 offset1:246
	s_waitcnt vmcnt(34)
	ds_write2_b32 v110, v67, v69 offset0:56 offset1:122
	s_waitcnt vmcnt(32)
	ds_write2_b32 v110, v70, v71 offset0:188 offset1:254
	s_waitcnt lgkmcnt(0)
	ds_read2_b32 v[40:41], v38 offset1:33
	s_waitcnt lgkmcnt(0)
	v_cvt_pk_bf16_f32 v40, v40, v41
	ds_read2_b32 v[42:43], v38 offset0:66 offset1:99
	s_waitcnt lgkmcnt(0)
	v_cvt_pk_bf16_f32 v41, v42, v43
	ds_read2_b32 v[42:43], v38 offset0:132 offset1:165
	s_waitcnt lgkmcnt(0)
	v_cvt_pk_bf16_f32 v42, v42, v43
	ds_read2_b32 v[44:45], v38 offset0:198 offset1:231
	v_mul_i32_i24_e32 v5, s54, v37
	s_waitcnt lgkmcnt(0)
	v_cvt_pk_bf16_f32 v43, v44, v45
	v_mad_u64_u32 v[44:45], s[22:23], s10, v5, 0
	v_mov_b32_e32 v46, v45
	v_mad_u64_u32 v[46:47], s[22:23], s11, v5, v[46:47]
	v_mov_b32_e32 v45, v46
	v_lshl_add_u64 v[44:45], v[44:45], 1, s[8:9]
	v_mov_b32_e32 v5, v3
	v_lshl_add_u64 v[44:45], v[44:45], 0, v[4:5]
	ds_read2_b32 v[46:47], v38 offset0:8 offset1:41
	global_store_dwordx4 v[44:45], v[40:43], off nt
	s_lshl_b32 s2, s54, 3
	s_andn2_b64 vcc, exec, s[20:21]
	s_waitcnt lgkmcnt(0)
	v_cvt_pk_bf16_f32 v40, v46, v47
	ds_read2_b32 v[42:43], v38 offset0:74 offset1:107
	s_waitcnt lgkmcnt(0)
	v_cvt_pk_bf16_f32 v41, v42, v43
	ds_read2_b32 v[42:43], v38 offset0:140 offset1:173
	s_waitcnt lgkmcnt(0)
	v_cvt_pk_bf16_f32 v42, v42, v43
	ds_read2_b32 v[44:45], v38 offset0:206 offset1:239
	s_waitcnt lgkmcnt(0)
	v_cvt_pk_bf16_f32 v43, v44, v45
	v_mov_b32_e32 v44, s2
	v_mad_i32_i24 v50, s54, v37, v44
	v_mad_u64_u32 v[44:45], s[22:23], s10, v50, 0
	v_mov_b32_e32 v46, v45
	v_mad_u64_u32 v[46:47], s[22:23], s11, v50, v[46:47]
	v_mov_b32_e32 v45, v46
	v_lshl_add_u64 v[44:45], v[44:45], 1, s[8:9]
	v_lshl_add_u64 v[44:45], v[44:45], 0, v[4:5]
	ds_read2_b32 v[48:49], v38 offset0:16 offset1:49
	global_store_dwordx4 v[44:45], v[40:43], off nt
	v_add_u32_e32 v50, s2, v50
	s_mov_b64 s[20:21], -1
	s_waitcnt lgkmcnt(0)
	v_cvt_pk_bf16_f32 v40, v48, v49
	ds_read2_b32 v[42:43], v38 offset0:82 offset1:115
	s_waitcnt lgkmcnt(0)
	v_cvt_pk_bf16_f32 v41, v42, v43
	ds_read2_b32 v[42:43], v38 offset0:148 offset1:181
	s_waitcnt lgkmcnt(0)
	v_cvt_pk_bf16_f32 v42, v42, v43
	ds_read2_b32 v[44:45], v38 offset0:214 offset1:247
	s_waitcnt lgkmcnt(0)
	v_cvt_pk_bf16_f32 v43, v44, v45
	v_mad_u64_u32 v[44:45], s[22:23], s10, v50, 0
	v_mov_b32_e32 v46, v45
	v_mad_u64_u32 v[46:47], s[22:23], s11, v50, v[46:47]
	v_mov_b32_e32 v45, v46
	v_lshl_add_u64 v[44:45], v[44:45], 1, s[8:9]
	v_lshl_add_u64 v[44:45], v[44:45], 0, v[4:5]
	ds_read2_b32 v[48:49], v38 offset0:24 offset1:57
	global_store_dwordx4 v[44:45], v[40:43], off nt
	v_add_u32_e32 v47, s2, v50
	s_waitcnt lgkmcnt(0)
	v_cvt_pk_bf16_f32 v40, v48, v49
	ds_read2_b32 v[42:43], v38 offset0:90 offset1:123
	s_waitcnt lgkmcnt(0)
	v_cvt_pk_bf16_f32 v41, v42, v43
	ds_read2_b32 v[42:43], v38 offset0:156 offset1:189
	s_waitcnt lgkmcnt(0)
	v_cvt_pk_bf16_f32 v42, v42, v43
	ds_read2_b32 v[44:45], v38 offset0:222 offset1:255
	s_waitcnt lgkmcnt(0)
	v_cvt_pk_bf16_f32 v43, v44, v45
	v_mad_u64_u32 v[44:45], s[22:23], s10, v47, 0
	v_mov_b32_e32 v46, v45
	v_mad_u64_u32 v[46:47], s[10:11], s11, v47, v[46:47]
	v_mov_b32_e32 v45, v46
	v_lshl_add_u64 v[44:45], v[44:45], 1, s[8:9]
	v_lshl_add_u64 v[44:45], v[44:45], 0, v[4:5]
	global_store_dwordx4 v[44:45], v[40:43], off nt
	s_cbranch_vccnz .LBB0_216
	s_add_i32 s57, s56, 0x1000
	s_cmp_gt_i32 s56, 0x1cb3f
	s_cselect_b64 s[20:21], -1, 0
	s_cmp_lt_i32 s56, 0x1cb40
	s_cselect_b32 s56, s57, s58
	s_cmpk_gt_i32 s56, 0x73ff
	s_cselect_b64 s[8:9], -1, 0
	s_cmp_gt_i32 s56, 0xe73f
	v_cndmask_b32_e64 v5, 0, 1, s[8:9]
	s_cselect_b64 s[8:9], -1, 0
	s_cmp_gt_i32 s56, 0x1673f
	v_cndmask_b32_e64 v40, 0, 1, s[8:9]
	s_cselect_b64 s[8:9], -1, 0
	v_readfirstlane_b32 s2, v5
	v_readfirstlane_b32 s10, v40
	s_cmp_lg_u64 s[8:9], 0
	s_addc_u32 s58, s2, s10
	s_cmp_lt_i32 s58, 1
	s_mov_b32 s2, s58
	s_cbranch_scc1 .LBB0_264
	s_cmp_eq_u32 s58, 1
	s_mov_b64 s[8:9], -1
	s_cbranch_scc1 .LBB0_262
	s_cmp_eq_u32 s58, 2
	s_cselect_b32 s2, s53, 0xfffe98c0
	s_mov_b64 s[8:9], 0

.LBB0_641:
	s_mov_b64 s[8:9], s[90:91]
	v_mbcnt_lo_u32_b32 v0, -1, 0
	v_mbcnt_hi_u32_b32 v0, -1, v0
	s_load_dwordx2 s[6:7], s[8:9], 0xe0
	s_load_dwordx4 s[60:63], s[8:9], 0x68
	s_waitcnt lgkmcnt(0)
	v_readlane_b32 s12, v253, 16
	v_and_b32_e32 v114, 63, v0
	s_mul_hi_i32 s13, s86, 0xa00
	s_add_u32 s2, s6, 0x2d400000
	s_addc_u32 s3, s7, 0
	s_add_u32 s10, s6, 0x46d00000
	s_addc_u32 s11, s7, 0
	s_add_u32 s8, s6, 0x46d40000
	s_addc_u32 s9, s7, 0
	s_add_u32 s12, s2, s12
	s_addc_u32 s13, s3, s13
	v_lshlrev_b32_e32 v128, 4, v114
	global_load_dwordx4 v[68:71], v128, s[12:13]
	global_load_dwordx4 v[64:67], v128, s[12:13] offset:1024
	v_and_b32_e32 v0, 31, v0
	s_waitcnt vmcnt(0)
	v_lshlrev_b32_e32 v73, 1, v0
	v_or_b32_e32 v72, 0xffffe000, v0
	global_load_ushort v110, v73, s[12:13] offset:2048
	global_load_ushort v111, v73, s[12:13] offset:2112
	v_readlane_b32 s12, v253, 1
	v_mov_b32_e32 v1, v129
	v_readlane_b32 s13, v254, 12
	v_add_u32_e32 v0, s12, v72
	v_readlane_b32 s12, v253, 2
	v_lshlrev_b64 v[0:1], 2, v[0:1]
	s_add_u32 s12, s2, s12
	v_lshl_add_u64 v[2:3], s[10:11], 0, v[0:1]
	v_lshl_add_u64 v[0:1], s[8:9], 0, v[0:1]
	s_addc_u32 s13, s3, s13
	global_load_dword v112, v[2:3], off
	global_load_dword v113, v[0:1], off
	global_load_dwordx4 v[60:63], v128, s[12:13]
	global_load_dwordx4 v[56:59], v128, s[12:13] offset:1024
	global_load_ushort v106, v73, s[12:13] offset:2048
	global_load_ushort v107, v73, s[12:13] offset:2112
	v_readlane_b32 s12, v253, 3
	v_mov_b32_e32 v1, v129
	v_readlane_b32 s13, v254, 13
	v_add_u32_e32 v0, s12, v72
	v_readlane_b32 s12, v253, 4
	v_lshlrev_b64 v[0:1], 2, v[0:1]
	s_add_u32 s12, s2, s12
	v_lshl_add_u64 v[2:3], s[10:11], 0, v[0:1]
	v_lshl_add_u64 v[0:1], s[8:9], 0, v[0:1]
	s_addc_u32 s13, s3, s13
	global_load_dword v108, v[2:3], off
	global_load_dword v109, v[0:1], off
	global_load_dwordx4 v[52:55], v128, s[12:13]
	global_load_dwordx4 v[48:51], v128, s[12:13] offset:1024
	global_load_ushort v102, v73, s[12:13] offset:2048
	global_load_ushort v103, v73, s[12:13] offset:2112
	v_readlane_b32 s12, v253, 5
	v_mov_b32_e32 v1, v129
	v_readlane_b32 s13, v254, 14
	v_add_u32_e32 v0, s12, v72
	v_readlane_b32 s12, v253, 6
	v_lshlrev_b64 v[0:1], 2, v[0:1]
	s_add_u32 s12, s2, s12
	v_lshl_add_u64 v[2:3], s[10:11], 0, v[0:1]
	v_lshl_add_u64 v[0:1], s[8:9], 0, v[0:1]
	s_addc_u32 s13, s3, s13
	global_load_dword v104, v[2:3], off
	global_load_dword v105, v[0:1], off
	global_load_dwordx4 v[44:47], v128, s[12:13]
	global_load_dwordx4 v[40:43], v128, s[12:13] offset:1024
	global_load_ushort v98, v73, s[12:13] offset:2048
	global_load_ushort v99, v73, s[12:13] offset:2112
	v_readlane_b32 s12, v253, 7
	v_mov_b32_e32 v1, v129
	v_readlane_b32 s13, v254, 15
	v_add_u32_e32 v0, s12, v72
	v_readlane_b32 s12, v253, 8
	v_lshlrev_b64 v[0:1], 2, v[0:1]
	s_add_u32 s12, s2, s12
	v_lshl_add_u64 v[2:3], s[10:11], 0, v[0:1]
	v_lshl_add_u64 v[0:1], s[8:9], 0, v[0:1]
	s_addc_u32 s13, s3, s13
	global_load_dword v100, v[2:3], off
	global_load_dword v101, v[0:1], off
	global_load_dwordx4 v[36:39], v128, s[12:13]
	global_load_dwordx4 v[32:35], v128, s[12:13] offset:1024
	global_load_ushort v94, v73, s[12:13] offset:2048
	global_load_ushort v95, v73, s[12:13] offset:2112
	v_readlane_b32 s12, v253, 9
	v_mov_b32_e32 v1, v129
	v_readlane_b32 s13, v254, 16
	v_add_u32_e32 v0, s12, v72
	v_readlane_b32 s12, v253, 10
	v_lshlrev_b64 v[0:1], 2, v[0:1]
	s_add_u32 s12, s2, s12
	v_lshl_add_u64 v[2:3], s[10:11], 0, v[0:1]
	v_lshl_add_u64 v[0:1], s[8:9], 0, v[0:1]
	s_addc_u32 s13, s3, s13
	global_load_dword v96, v[2:3], off
	global_load_dword v97, v[0:1], off
	global_load_dwordx4 v[28:31], v128, s[12:13]
	global_load_dwordx4 v[24:27], v128, s[12:13] offset:1024
	global_load_ushort v90, v73, s[12:13] offset:2048
	global_load_ushort v91, v73, s[12:13] offset:2112
	v_readlane_b32 s12, v253, 11
	v_mov_b32_e32 v1, v129
	v_readlane_b32 s13, v254, 17
	v_add_u32_e32 v0, s12, v72
	v_readlane_b32 s12, v253, 12
	v_lshlrev_b64 v[0:1], 2, v[0:1]
	s_add_u32 s12, s2, s12
	v_lshl_add_u64 v[2:3], s[10:11], 0, v[0:1]
	v_lshl_add_u64 v[0:1], s[8:9], 0, v[0:1]
	v_and_b32_e32 v119, 0xffff0000, v68
	v_lshlrev_b32_e32 v118, 16, v68
	v_mul_f32_e32 v68, v119, v119
	s_addc_u32 s13, s3, s13
	v_lshlrev_b32_e32 v120, 16, v69
	v_fmac_f32_e32 v68, v118, v118
	global_load_dword v92, v[2:3], off
	global_load_dword v93, v[0:1], off
	global_load_dwordx4 v[20:23], v128, s[12:13]
	global_load_dwordx4 v[16:19], v128, s[12:13] offset:1024
	global_load_ushort v86, v73, s[12:13] offset:2048
	global_load_ushort v87, v73, s[12:13] offset:2112
	v_readlane_b32 s12, v253, 13
	v_and_b32_e32 v121, 0xffff0000, v69
	v_fmac_f32_e32 v68, v120, v120
	v_add_u32_e32 v0, s12, v72
	v_mov_b32_e32 v1, v129
	v_readlane_b32 s12, v253, 14
	v_lshlrev_b32_e32 v122, 16, v70
	v_fmac_f32_e32 v68, v121, v121
	v_lshlrev_b64 v[0:1], 2, v[0:1]
	s_add_u32 s12, s2, s12
	v_readlane_b32 s13, v254, 18
	v_and_b32_e32 v123, 0xffff0000, v70
	v_fmac_f32_e32 v68, v122, v122
	v_lshl_add_u64 v[2:3], s[10:11], 0, v[0:1]
	v_lshl_add_u64 v[0:1], s[8:9], 0, v[0:1]
	s_addc_u32 s13, s3, s13
	v_lshlrev_b32_e32 v124, 16, v71
	v_fmac_f32_e32 v68, v123, v123
	global_load_dword v88, v[2:3], off
	global_load_dword v89, v[0:1], off
	global_load_dwordx4 v[12:15], v128, s[12:13]
	global_load_dwordx4 v[8:11], v128, s[12:13] offset:1024
	global_load_ushort v82, v73, s[12:13] offset:2048
	global_load_ushort v83, v73, s[12:13] offset:2112
	v_readlane_b32 s12, v253, 15
	v_and_b32_e32 v125, 0xffff0000, v71
	v_fmac_f32_e32 v68, v124, v124
	v_add_u32_e32 v0, s12, v72
	v_mov_b32_e32 v1, v129
	v_readlane_b32 s12, v253, 17
	v_fmac_f32_e32 v68, v125, v125
	v_lshlrev_b64 v[0:1], 2, v[0:1]
	s_add_u32 s2, s2, s12
	v_readlane_b32 s12, v254, 19
	v_add_f32_dpp v68, v68, v68 quad_perm:[1,0,3,2] row_mask:0xf bank_mask:0xf bound_ctrl:1
	v_lshl_add_u64 v[2:3], s[10:11], 0, v[0:1]
	v_lshl_add_u64 v[0:1], s[8:9], 0, v[0:1]
	s_addc_u32 s3, s3, s12
	v_add_f32_dpp v68, v68, v68 quad_perm:[2,3,0,1] row_mask:0xf bank_mask:0xf bound_ctrl:1
	global_load_dword v84, v[2:3], off
	global_load_dword v85, v[0:1], off
	global_load_dwordx4 v[4:7], v128, s[2:3]
	s_nop 0
	global_load_dwordx4 v[0:3], v128, s[2:3] offset:1024
	global_load_ushort v78, v73, s[2:3] offset:2048
	global_load_ushort v79, v73, s[2:3] offset:2112
	v_readlane_b32 s2, v253, 18
	v_add_f32_dpp v68, v68, v68 row_half_mirror row_mask:0xf bank_mask:0xf bound_ctrl:1
	v_mov_b32_e32 v73, v129
	v_add_u32_e32 v72, s2, v72
	v_add_f32_dpp v68, v68, v68 row_mirror row_mask:0xf bank_mask:0xf bound_ctrl:1
	v_lshlrev_b64 v[72:73], 2, v[72:73]
	v_mov_b32_e32 v69, v68
	v_lshl_add_u64 v[74:75], s[10:11], 0, v[72:73]
	v_lshl_add_u64 v[72:73], s[8:9], 0, v[72:73]
	v_permlane16_swap_b32_e32 v68, v69
	global_load_dword v80, v[74:75], off
	global_load_dword v81, v[72:73], off
	v_lshl_add_u64 v[74:75], s[6:7], 0, v[128:129]
	v_lshlrev_b32_e32 v128, 1, v114
	v_add_f32_e32 v68, v68, v69
	v_lshl_add_u64 v[72:73], s[6:7], 0, v[128:129]
	s_mov_b64 s[2:3], 0x32500000
	v_mov_b32_e32 v69, v68
	v_lshl_add_u64 v[72:73], v[72:73], 0, s[2:3]
	v_readlane_b32 s2, v253, 19
	v_permlane32_swap_b32_e32 v68, v69
	v_readlane_b32 s3, v253, 20
	v_add_f32_e32 v68, v68, v69
	v_fmamk_f32 v68, v68, 0x3b000000, v248
	v_lshl_add_u64 v[76:77], v[74:75], 0, s[2:3]
	s_mov_b32 s2, 0x800000
	v_cmp_gt_f32_e32 vcc, s2, v68
	v_mul_f32_e32 v69, 0x4b800000, v68
	v_lshlrev_b32_e32 v128, 5, v114
	v_cndmask_b32_e32 v68, v68, v69, vcc
	v_rsq_f32_e32 v68, v68
	v_cmp_gt_u32_e64 s[58:59], 32, v114
	s_mov_b32 s3, 0x30100000
	v_mul_f32_e32 v69, 0x45800000, v68
	v_cndmask_b32_e32 v126, v68, v69, vcc
	global_load_dwordx4 v[68:71], v128, s[60:61] offset:16
	global_load_dwordx4 v[114:117], v128, s[60:61]
	v_mul_f32_e32 v118, v126, v118
	s_waitcnt vmcnt(0)
	v_mul_f32_e32 v114, v114, v118
	v_mul_f32_e32 v118, v126, v119
	v_mul_f32_e32 v115, v115, v118
	v_cvt_pk_bf16_f32 v114, v114, v115
	v_mul_f32_e32 v115, v126, v120
	v_mul_f32_e32 v115, v116, v115
	v_mul_f32_e32 v116, v126, v121
	v_mul_f32_e32 v116, v117, v116
	v_cvt_pk_bf16_f32 v115, v115, v116
	v_mul_f32_e32 v116, v126, v122
	v_mul_f32_e32 v68, v68, v116
	v_mul_f32_e32 v116, v126, v123
	v_mul_f32_e32 v69, v69, v116
	v_cvt_pk_bf16_f32 v116, v68, v69
	v_mul_f32_e32 v68, v126, v124
	v_mul_f32_e32 v68, v70, v68
	v_mul_f32_e32 v69, v126, v125
	v_mul_f32_e32 v69, v71, v69
	v_cvt_pk_bf16_f32 v117, v68, v69
	v_add_co_u32_e32 v68, vcc, s3, v76
	v_lshlrev_b32_e32 v118, 16, v66
	s_nop 0
	v_addc_co_u32_e32 v69, vcc, 0, v77, vcc
	global_store_dwordx4 v[68:69], v[114:117], off
	v_and_b32_e32 v119, 0xffff0000, v66
	v_lshlrev_b32_e32 v120, 16, v67
	v_and_b32_e32 v115, 0xffff0000, v64
	v_lshlrev_b32_e32 v114, 16, v64
	v_mul_f32_e32 v64, v115, v115
	v_lshlrev_b32_e32 v116, 16, v65
	v_fmac_f32_e32 v64, v114, v114
	v_and_b32_e32 v117, 0xffff0000, v65
	v_fmac_f32_e32 v64, v116, v116
	v_fmac_f32_e32 v64, v117, v117
	v_fmac_f32_e32 v64, v118, v118
	v_fmac_f32_e32 v64, v119, v119
	v_and_b32_e32 v121, 0xffff0000, v67
	v_fmac_f32_e32 v64, v120, v120
	v_fmac_f32_e32 v64, v121, v121
	s_nop 1
	v_add_f32_dpp v64, v64, v64 quad_perm:[1,0,3,2] row_mask:0xf bank_mask:0xf bound_ctrl:1
	s_nop 1
	v_add_f32_dpp v64, v64, v64 quad_perm:[2,3,0,1] row_mask:0xf bank_mask:0xf bound_ctrl:1
	s_nop 1
	v_add_f32_dpp v64, v64, v64 row_half_mirror row_mask:0xf bank_mask:0xf bound_ctrl:1
	s_nop 1
	v_add_f32_dpp v64, v64, v64 row_mirror row_mask:0xf bank_mask:0xf bound_ctrl:1
	v_mov_b32_e32 v65, v64
	s_nop 1
	v_permlane16_swap_b32_e32 v64, v65
	v_add_f32_e32 v64, v64, v65
	v_mov_b32_e32 v65, v64
	s_nop 1
	v_permlane32_swap_b32_e32 v64, v65
	v_add_f32_e32 v64, v64, v65
	v_fmamk_f32 v64, v64, 0x3b000000, v248
	v_cmp_gt_f32_e32 vcc, s2, v64
	v_mul_f32_e32 v65, 0x4b800000, v64
	s_nop 0
	v_cndmask_b32_e32 v64, v64, v65, vcc
	v_rsq_f32_e32 v64, v64
	s_nop 0
	v_mul_f32_e32 v65, 0x45800000, v64
	v_cndmask_b32_e32 v122, v64, v65, vcc
	global_load_dwordx4 v[64:67], v128, s[62:63] offset:16
	global_load_dwordx4 v[68:71], v128, s[62:63]
	v_mul_f32_e32 v114, v122, v114
	s_waitcnt vmcnt(0)
	v_mul_f32_e32 v68, v68, v114
	v_mul_f32_e32 v114, v122, v115
	v_mul_f32_e32 v69, v69, v114
	v_cvt_pk_bf16_f32 v68, v68, v69
	v_mul_f32_e32 v69, v122, v116
	v_mul_f32_e32 v69, v70, v69
	v_mul_f32_e32 v70, v122, v117
	v_mul_f32_e32 v70, v71, v70
	v_cvt_pk_bf16_f32 v69, v69, v70
	v_mul_f32_e32 v70, v122, v118
	v_mul_f32_e32 v64, v64, v70
	v_mul_f32_e32 v70, v122, v119
	v_mul_f32_e32 v65, v65, v70
	v_cvt_pk_bf16_f32 v70, v64, v65
	v_mul_f32_e32 v64, v122, v120
	v_mul_f32_e32 v64, v66, v64
	v_mul_f32_e32 v65, v122, v121
	v_mul_f32_e32 v65, v67, v65
	v_cvt_pk_bf16_f32 v71, v64, v65
	v_add_co_u32_e32 v64, vcc, 0x31300000, v76
	s_nop 1
	v_addc_co_u32_e32 v65, vcc, 0, v77, vcc
	global_store_dwordx4 v[64:65], v[68:71], off
	s_and_saveexec_b64 s[6:7], s[58:59]
	s_cbranch_execz .LBB0_643
	v_readlane_b32 s2, v252, 47
	v_readlane_b32 s3, v252, 48
	v_lshlrev_b32_e32 v67, 16, v111
	v_lshlrev_b32_e32 v66, 16, v110
	v_cndmask_b32_e64 v69, 0, v113, s[2:3]
	v_cndmask_b32_e64 v68, 1.0, v112, s[2:3]
	v_mul_f32_e32 v64, v69, v67
	v_readlane_b32 s2, v253, 21
	v_fma_f32 v64, v68, v66, -v64
	v_readlane_b32 s3, v253, 22
	v_mul_f32_e32 v66, v69, v66
	v_cvt_pk_bf16_f32 v70, v64, v129
	v_fmac_f32_e32 v66, v68, v67
	v_lshl_add_u64 v[64:65], v[72:73], 0, s[2:3]
	global_store_short v[64:65], v70, off
	v_cvt_pk_bf16_f32 v66, v66, v129
	global_store_short v[64:65], v66, off offset:64

.LBB0_812:
	s_or_b64 exec, exec, s[6:7]
	s_lshl_b32 s6, s16, 8
	s_mul_i32 s8, s30, 0x900
	s_ashr_i32 s7, s6, 31
	s_mul_hi_i32 s3, s30, 0x900
	s_add_u32 s78, s8, s6
	s_addc_u32 s79, s3, s7
	s_mul_i32 s6, s78, s69
	s_mul_hi_u32 s7, s78, s68
	s_add_i32 s6, s7, s6
	s_mul_i32 s7, s79, s68
	s_add_i32 s7, s6, s7
	s_mul_i32 s6, s78, s68
	s_lshl_b64 s[6:7], s[6:7], 1
	s_add_u32 s9, s60, s6
	s_mul_i32 s6, s15, s26
	s_addc_u32 s11, s61, s7
	s_ashr_i32 s7, s6, 31
	s_lshl_b64 s[6:7], s[6:7], 1
	s_add_u32 s10, s9, s6
	s_mul_i32 s3, s3, s62
	s_mul_hi_u32 s6, s8, s62
	s_addc_u32 s11, s11, s7
	s_add_i32 s7, s6, s3
	s_mul_i32 s6, s8, s62
	s_lshl_b64 s[8:9], s[6:7], 1
	s_add_u32 s3, s66, s8
	s_addc_u32 s22, s67, s9
	s_abs_i32 s7, s15
	s_mul_hi_u32 s20, s7, s13
	s_mul_i32 s21, s20, s89
	s_sub_i32 s7, s7, s21
	s_ashr_i32 s6, s15, 31
	s_add_i32 s21, s20, 1
	s_sub_i32 s23, s7, s89
	s_cmp_ge_u32 s7, s89
	s_cselect_b32 s20, s21, s20
	v_ashrrev_i32_e32 v20, 4, v8
	v_and_b32_e32 v3, 0xfffff0, v20
	v_lshlrev_b32_e32 v4, 1, v20
	s_cselect_b32 s7, s23, s7
	s_add_i32 s21, s20, 1
	v_lshlrev_b32_e32 v1, 3, v8
	v_and_or_b32 v3, v4, 8, v3
	s_cmp_ge_u32 s7, s89
	v_and_b32_e32 v2, 0x78, v1
	v_lshrrev_b32_e32 v3, 1, v3
	v_bfe_u32 v1, v1, 5, 2
	s_cselect_b32 s7, s21, s20
	v_or_b32_e32 v3, v3, v1
	s_xor_b32 s7, s7, s6
	v_lshrrev_b32_e32 v4, 1, v20
	v_lshlrev_b32_e32 v21, 9, v3
	v_and_b32_e32 v3, 3, v20
	s_sub_i32 s6, s7, s6
	v_and_or_b32 v3, v4, 4, v3
	v_add_u32_e32 v24, 32, v20
	s_mul_i32 s6, s6, s27
	v_lshlrev_b32_e32 v22, 6, v3
	v_and_b32_e32 v3, 0xfffff0, v24
	v_lshlrev_b32_e32 v4, 1, v24
	s_ashr_i32 s7, s6, 31
	v_and_or_b32 v3, v4, 8, v3
	s_lshl_b64 s[20:21], s[6:7], 1
	v_lshrrev_b32_e32 v3, 1, v3
	s_add_u32 s6, s3, s20
	v_or_b32_e32 v1, v3, v1
	s_addc_u32 s7, s22, s21
	v_lshlrev_b32_e32 v25, 9, v1
	v_mul_lo_u32 v1, v20, s62
	s_add_u32 s3, s85, s8
	v_or_b32_e32 v3, v1, v2
	v_add_u32_e32 v1, s14, v1
	s_addc_u32 s9, s81, s9
	v_and_b32_e32 v0, 63, v8
	v_or_b32_e32 v1, v1, v2
	v_lshlrev_b32_e32 v26, 4, v8
	s_add_u32 s8, s3, s20
	v_lshlrev_b32_e32 v23, 1, v2
	v_lshlrev_b32_e32 v178, 1, v1
	v_lshlrev_b32_e32 v0, 3, v0
	v_and_b32_e32 v1, 0xc0, v26
	v_lshlrev_b32_e32 v2, 1, v8
	s_addc_u32 s9, s9, s21
	v_lshlrev_b32_e32 v128, 1, v3
	v_and_or_b32 v1, v0, 24, v1
	v_and_b32_e32 v2, 32, v2
	v_and_b32_e32 v0, 0x100, v0
	v_or3_b32 v181, v1, v2, v0
	global_load_dwordx4 v[10:13], v128, s[8:9]
	global_load_dwordx4 v[14:17], v178, s[8:9]
	global_load_dwordx4 v[4:7], v128, s[6:7]
	global_load_dwordx4 v[0:3], v178, s[6:7]
	v_ashrrev_i32_e32 v27, 1, v8
	v_bfi_b32 v18, s84, v27, v8
	v_ashrrev_i32_e32 v19, 31, v27
	v_mul_lo_u32 v28, s68, v19
	v_mul_lo_u32 v29, s69, v18
	v_mad_u64_u32 v[18:19], s[20:21], s68, v18, 0
	v_bfe_u32 v182, v8, 5, 1
	v_add3_u32 v19, v19, v28, v29
	v_lshl_add_u64 v[18:19], v[18:19], 1, s[10:11]
	v_lshlrev_b32_e32 v32, 4, v182
	v_mov_b32_e32 v33, v129
	v_lshl_add_u64 v[18:19], v[18:19], 0, v[32:33]
	global_load_dwordx4 v[120:123], v[18:19], off
	global_load_dwordx4 v[124:127], v[18:19], off offset:32
	global_load_dwordx4 v[116:119], v[18:19], off offset:64
	global_load_dwordx4 v[112:115], v[18:19], off offset:96
	global_load_dwordx4 v[108:111], v[18:19], off offset:128
	global_load_dwordx4 v[104:107], v[18:19], off offset:160
	global_load_dwordx4 v[100:103], v[18:19], off offset:192
	global_load_dwordx4 v[96:99], v[18:19], off offset:224
	v_and_b32_e32 v18, 48, v23
	v_or3_b32 v19, v21, v22, v18
	v_add_u32_e32 v201, 0, v19
	v_lshrrev_b32_e32 v19, 3, v201
	v_xor_b32_e32 v19, v19, v201
	v_and_b32_e32 v19, 0x100, v19
	v_xor_b32_e32 v201, v201, v19
	v_lshlrev_b32_e32 v19, 3, v19
	v_xor_b32_e32 v201, v201, v19
	v_and_b32_e32 v9, 31, v8
	v_ashrrev_i32_e32 v21, 7, v8
	s_waitcnt vmcnt(0)
	v_and_b32_e32 v8, 0x70, v8
	v_or3_b32 v18, v25, v22, v18
	v_add_u32_e32 v202, 0, v18
	v_lshrrev_b32_e32 v18, 3, v202
	v_xor_b32_e32 v18, v18, v202
	v_and_b32_e32 v18, 0x100, v18
	v_xor_b32_e32 v202, v202, v18
	v_lshlrev_b32_e32 v18, 3, v18
	v_xor_b32_e32 v202, v202, v18
	v_lshlrev_b32_e32 v33, 8, v9
	v_and_b32_e32 v42, 0x70, v26
	v_add_u32_e32 v184, s2, v21
	v_max_i32_e32 v21, 4, v184
	v_add_u32_e32 v21, -4, v21
	v_min_u32_e32 v185, 24, v21
	v_and_or_b32 v183, v27, 32, v9
	v_or_b32_e32 v34, 32, v32
	v_bitop3_b32 v34, v34, v33, v42 bitop3:0xde
	v_add_u32_e32 v200, 0, v34
	s_cmp_lg_u32 0, -1
	s_cselect_b32 s3, 0, 0
	v_add_u32_e32 v186, s3, v181
	v_add_u32_e32 v188, 7, v185
	ds_write_b128 v201, v[10:13]
	v_lshlrev_b32_e32 v10, 8, v20
	v_bitop3_b32 v10, v23, v10, v8 bitop3:0xde
	v_add_u32_e32 v203, 0, v10
	ds_write_b128 v202, v[14:17]
	ds_write_b128 v203, v[4:7] offset:32768
	v_lshlrev_b32_e32 v4, 8, v24
	v_bitop3_b32 v4, v23, v4, v8 bitop3:0xde
	v_add_u32_e32 v204, 0, v4
	ds_write_b128 v204, v[0:3] offset:32768
	v_bitop3_b32 v0, v32, v33, v42 bitop3:0xde
	v_add_u32_e32 v198, 0, v0
	s_waitcnt lgkmcnt(0)
	s_barrier
	ds_read_b128 v[0:3], v198 offset:32768
	ds_read_b128 v[4:7], v198 offset:40960
	s_waitcnt vmcnt(7) lgkmcnt(1)
	v_mfma_f32_32x32x16_bf16 v[16:31], v[0:3], v[120:123], 0
	ds_read_b128 v[34:37], v200 offset:32768
	ds_read_b128 v[38:41], v200 offset:40960
	s_waitcnt lgkmcnt(2)
	v_mfma_f32_32x32x16_bf16 v[0:15], v[4:7], v[120:123], 0
	s_waitcnt vmcnt(6) lgkmcnt(1)
	v_mfma_f32_32x32x16_bf16 v[16:31], v[34:37], v[124:127], v[16:31]
	v_or_b32_e32 v34, 64, v32
	v_bitop3_b32 v34, v34, v33, v42 bitop3:0xde
	v_add_u32_e32 v199, 0, v34
	s_waitcnt lgkmcnt(0)
	v_mfma_f32_32x32x16_bf16 v[0:15], v[38:41], v[124:127], v[0:15]
	ds_read_b128 v[34:37], v199 offset:32768
	ds_read_b128 v[38:41], v199 offset:40960
	s_waitcnt vmcnt(5) lgkmcnt(1)
	v_mfma_f32_32x32x16_bf16 v[16:31], v[34:37], v[116:119], v[16:31]
	v_or_b32_e32 v34, 0x60, v32
	v_bitop3_b32 v34, v34, v33, v42 bitop3:0xde
	v_add_u32_e32 v193, 0, v34
	s_waitcnt lgkmcnt(0)
	v_mfma_f32_32x32x16_bf16 v[0:15], v[38:41], v[116:119], v[0:15]
	ds_read_b128 v[34:37], v193 offset:32768
	ds_read_b128 v[38:41], v193 offset:40960
	s_waitcnt vmcnt(4) lgkmcnt(1)
	v_mfma_f32_32x32x16_bf16 v[16:31], v[34:37], v[112:115], v[16:31]
	v_or_b32_e32 v34, 0x80, v32
	v_bitop3_b32 v34, v34, v33, v42 bitop3:0xde
	v_add_u32_e32 v192, 0, v34
	s_waitcnt lgkmcnt(0)
	v_mfma_f32_32x32x16_bf16 v[0:15], v[38:41], v[112:115], v[0:15]
	ds_read_b128 v[34:37], v192 offset:32768
	ds_read_b128 v[38:41], v192 offset:40960
	s_waitcnt vmcnt(3) lgkmcnt(1)
	v_mfma_f32_32x32x16_bf16 v[16:31], v[34:37], v[108:111], v[16:31]
	v_or_b32_e32 v34, 0xa0, v32
	v_bitop3_b32 v34, v34, v33, v42 bitop3:0xde
	v_add_u32_e32 v191, 0, v34
	s_waitcnt lgkmcnt(0)
	v_mfma_f32_32x32x16_bf16 v[0:15], v[38:41], v[108:111], v[0:15]
	ds_read_b128 v[34:37], v191 offset:32768
	ds_read_b128 v[38:41], v191 offset:40960
	s_waitcnt vmcnt(2) lgkmcnt(1)
	v_mfma_f32_32x32x16_bf16 v[16:31], v[34:37], v[104:107], v[16:31]
	v_or_b32_e32 v34, 0xc0, v32
	v_bitop3_b32 v34, v34, v33, v42 bitop3:0xde
	v_add_u32_e32 v190, 0, v34
	v_or_b32_e32 v32, 0xe0, v32
	v_bitop3_b32 v32, v32, v33, v42 bitop3:0xde
	v_add_u32_e32 v189, 0, v32
	s_waitcnt lgkmcnt(0)
	v_mfma_f32_32x32x16_bf16 v[0:15], v[38:41], v[104:107], v[0:15]
	ds_read_b128 v[34:37], v190 offset:32768
	ds_read_b128 v[38:41], v190 offset:40960
	s_waitcnt vmcnt(1) lgkmcnt(1)
	v_mfma_f32_32x32x16_bf16 v[16:31], v[34:37], v[100:103], v[16:31]
	s_waitcnt lgkmcnt(0)
	v_mfma_f32_32x32x16_bf16 v[0:15], v[38:41], v[100:103], v[0:15]
	ds_read_b128 v[32:35], v189 offset:32768
	ds_read_b128 v[36:39], v189 offset:40960
	s_waitcnt vmcnt(0) lgkmcnt(1)
	v_mfma_f32_32x32x16_bf16 v[16:31], v[32:35], v[96:99], v[16:31]
	s_waitcnt lgkmcnt(0)
	v_mfma_f32_32x32x16_bf16 v[0:15], v[36:39], v[96:99], v[0:15]
	s_nop 9
	v_max_f32_e32 v32, v17, v17
	v_max_f32_e32 v33, v16, v16
	v_max_f32_e32 v32, v33, v32
	v_max_f32_e32 v33, v25, v25
	v_max_f32_e32 v34, v24, v24
	v_max_f32_e32 v33, v34, v33
	v_max3_f32 v32, v32, v18, v19
	v_max_f32_e32 v34, v9, v9
	v_max_f32_e32 v35, v8, v8
	v_max_f32_e32 v34, v35, v34
	v_max3_f32 v35, v0, v1, v2
	v_max3_f32 v34, v34, v10, v11
	v_max3_f32 v33, v33, v26, v27
	v_max3_f32 v35, v35, v3, v4
	v_max3_f32 v34, v34, v12, v13
	v_max3_f32 v32, v32, v20, v21
	v_max3_f32 v33, v33, v28, v29
	v_max3_f32 v35, v35, v5, v6
	v_max3_f32 v34, v34, v14, v15
	v_max3_f32 v32, v32, v22, v23
	v_max3_f32 v33, v33, v30, v31
	v_max3_f32 v34, v35, v7, v34
	v_max3_f32 v32, v32, v33, v34
	v_mov_b32_e32 v33, v32
	s_nop 1
	v_permlane32_swap_b32_e32 v32, v33
	v_max_f32_e32 v33, v33, v33
	v_max_f32_e32 v32, v32, v32
	v_max_f32_e32 v32, v32, v33
	v_add_f32_e32 v33, 0x7149f2ca, v32
	v_max_f32_e32 v32, 0xf149f2ca, v32
	v_cmp_ge_f32_e32 vcc, s31, v33
	v_sub_f32_e32 v33, 0xf149f2ca, v32
	v_mul_f32_e32 v33, 0x3e0293ee, v33
	s_cmp_eq_u64 vcc, exec
	v_exp_f32_e32 v33, v33
	s_cselect_b64 vcc, -1, 0
	v_cndmask_b32_e32 v206, v32, v230, vcc
	s_add_u32 s2, s8, s76
	v_mul_f32_e32 v32, 0xbe0293ee, v206
	s_addc_u32 s3, s9, s77
	v_cndmask_b32_e64 v205, v33, 1.0, vcc
	v_mov_b32_e32 v33, v32
	s_add_u32 s10, s6, s76
	v_fmac_f32_e32 v33, 0x3e0293ee, v31
	s_addc_u32 s11, s7, s77
	v_pk_fma_f32 v[146:147], v[14:15], s[52:53], v[32:33] op_sel_hi:[1,0,0]
	v_pk_fma_f32 v[148:149], v[12:13], s[52:53], v[32:33] op_sel_hi:[1,0,0]
	v_pk_fma_f32 v[150:151], v[10:11], s[52:53], v[32:33] op_sel_hi:[1,0,0]
	v_pk_fma_f32 v[152:153], v[8:9], s[52:53], v[32:33] op_sel_hi:[1,0,0]
	v_pk_fma_f32 v[154:155], v[6:7], s[52:53], v[32:33] op_sel_hi:[1,0,0]
	v_pk_fma_f32 v[156:157], v[4:5], s[52:53], v[32:33] op_sel_hi:[1,0,0]
	v_pk_fma_f32 v[158:159], v[2:3], s[52:53], v[32:33] op_sel_hi:[1,0,0]
	v_pk_fma_f32 v[160:161], v[0:1], s[52:53], v[32:33] op_sel_hi:[1,0,0]
	global_load_dwordx4 v[0:3], v128, s[2:3]
	global_load_dwordx4 v[4:7], v178, s[2:3]
	global_load_dwordx4 v[8:11], v128, s[10:11]
	global_load_dwordx4 v[12:15], v178, s[10:11]
	s_add_u32 s2, s2, s76
	s_addc_u32 s3, s3, s77
	s_add_u32 s10, s10, s76
	s_addc_u32 s11, s11, s77
	global_load_dwordx4 v[130:133], v128, s[2:3]
	global_load_dwordx4 v[134:137], v178, s[2:3]
	global_load_dwordx4 v[138:141], v128, s[10:11]
	global_load_dwordx4 v[142:145], v178, s[10:11]
	v_fmamk_f32 v16, v16, 0x3e0293ee, v32
	v_fmamk_f32 v17, v17, 0x3e0293ee, v32
	v_fmamk_f32 v18, v18, 0x3e0293ee, v32
	v_fmamk_f32 v19, v19, 0x3e0293ee, v32
	v_fmamk_f32 v20, v20, 0x3e0293ee, v32
	v_fmamk_f32 v21, v21, 0x3e0293ee, v32
	v_fmamk_f32 v22, v22, 0x3e0293ee, v32
	v_fmamk_f32 v23, v23, 0x3e0293ee, v32
	v_fmamk_f32 v24, v24, 0x3e0293ee, v32
	v_fmamk_f32 v25, v25, 0x3e0293ee, v32
	v_fmamk_f32 v26, v26, 0x3e0293ee, v32
	v_fmamk_f32 v27, v27, 0x3e0293ee, v32
	v_fmamk_f32 v28, v28, 0x3e0293ee, v32
	v_fmamk_f32 v29, v29, 0x3e0293ee, v32
	v_fmamk_f32 v30, v30, 0x3e0293ee, v32
	v_exp_f32_e32 v176, v16
	v_exp_f32_e32 v211, v17
	v_exp_f32_e32 v163, v18
	v_exp_f32_e32 v177, v19
	v_exp_f32_e32 v164, v20
	v_exp_f32_e32 v175, v21
	v_exp_f32_e32 v165, v22
	v_exp_f32_e32 v174, v23
	v_exp_f32_e32 v166, v24
	v_exp_f32_e32 v173, v25
	v_exp_f32_e32 v167, v26
	v_exp_f32_e32 v172, v27
	v_exp_f32_e32 v168, v28
	v_exp_f32_e32 v171, v29
	v_exp_f32_e32 v169, v30
	v_exp_f32_e32 v170, v33
	s_waitcnt vmcnt(4)
	ds_write_b128 v201, v[0:3] offset:16384
	ds_write_b128 v202, v[4:7] offset:16384
	ds_write_b128 v203, v[8:11] offset:49152
	ds_write_b128 v204, v[12:15] offset:49152
	v_mov_b32_e32 v15, 0
	s_cmp_lt_i32 s19, 3
	s_waitcnt lgkmcnt(0)
	s_barrier
	s_cbranch_scc1 .LBB0_838
	s_add_i32 s20, s17, -4
	s_add_i32 s21, s19, -1
	s_cmp_lg_u32 0, -1
	s_cselect_b32 s2, 0, 0
	s_addk_i32 s2, 0x4000
	s_movk_i32 s3, 0x7c
	v_add_u32_e32 v207, s2, v181
	s_mul_i32 s2, s17, 0x7c
	v_mul_lo_u32 v0, v184, s3
	v_sub_u32_e32 v0, s2, v0
	s_add_i32 s2, 0, 0x14a2c
	v_mov_b32_e32 v187, 0
	v_mov_b32_e32 v179, v129
	v_add_u32_e32 v208, s2, v0
	s_mov_b32 s23, 4
	s_movk_i32 s22, 0xc0
	v_mov_b32_e32 v48, 0
	v_mov_b32_e32 v49, v187
	v_mov_b32_e32 v50, v187
	v_mov_b32_e32 v51, v187
	v_mov_b32_e32 v52, v187
	v_mov_b32_e32 v53, v187
	v_mov_b32_e32 v54, v187
	v_mov_b32_e32 v55, v187
	v_mov_b32_e32 v56, v187
	v_mov_b32_e32 v57, v187
	v_mov_b32_e32 v58, v187
	v_mov_b32_e32 v59, v187
	v_mov_b32_e32 v60, v187
	v_mov_b32_e32 v61, v187
	v_mov_b32_e32 v62, v187
	v_mov_b32_e32 v63, v187
	v_mov_b32_e32 v32, 0
	v_mov_b32_e32 v33, v187
	v_mov_b32_e32 v34, v187
	v_mov_b32_e32 v35, v187
	v_mov_b32_e32 v36, v187
	v_mov_b32_e32 v37, v187
	v_mov_b32_e32 v38, v187
	v_mov_b32_e32 v39, v187
	v_mov_b32_e32 v40, v187
	v_mov_b32_e32 v41, v187
	v_mov_b32_e32 v42, v187
	v_mov_b32_e32 v43, v187
	v_mov_b32_e32 v44, v187
	v_mov_b32_e32 v45, v187
	v_mov_b32_e32 v46, v187
	v_mov_b32_e32 v47, v187
	v_mov_b32_e32 v16, 0
	v_mov_b32_e32 v17, v187
	v_mov_b32_e32 v18, v187
	v_mov_b32_e32 v19, v187
	v_mov_b32_e32 v20, v187
	v_mov_b32_e32 v21, v187
	v_mov_b32_e32 v22, v187
	v_mov_b32_e32 v23, v187
	v_mov_b32_e32 v24, v187
	v_mov_b32_e32 v25, v187
	v_mov_b32_e32 v26, v187
	v_mov_b32_e32 v27, v187
	v_mov_b32_e32 v28, v187
	v_mov_b32_e32 v29, v187
	v_mov_b32_e32 v30, v187
	v_mov_b32_e32 v31, v187
	v_mov_b32_e32 v0, 0
	v_mov_b32_e32 v1, v187
	v_mov_b32_e32 v2, v187
	v_mov_b32_e32 v3, v187
	v_mov_b32_e32 v4, v187
	v_mov_b32_e32 v5, v187
	v_mov_b32_e32 v6, v187
	v_mov_b32_e32 v7, v187
	v_mov_b32_e32 v8, v187
	v_mov_b32_e32 v9, v187
	v_mov_b32_e32 v10, v187
	v_mov_b32_e32 v11, v187
	v_mov_b32_e32 v12, v187
	v_mov_b32_e32 v13, v187
	v_mov_b32_e32 v14, v187
	v_mov_b32_e32 v15, v187

.LBB0_823:
	v_max_f32_e32 v65, v162, v163
	v_max_f32_e32 v66, v170, v171
	v_max_f32_e32 v67, v72, v217
	v_max3_f32 v68, v64, v211, v212
	v_max3_f32 v67, v67, v218, v219
	v_max3_f32 v65, v65, v164, v165
	v_max3_f32 v66, v66, v172, v173
	v_max3_f32 v68, v68, v213, v214
	v_max3_f32 v67, v67, v220, v221
	v_max3_f32 v65, v65, v166, v167
	v_max3_f32 v66, v66, v174, v175
	v_max3_f32 v68, v68, v215, v216
	v_max3_f32 v67, v67, v222, v79
	v_max3_f32 v65, v65, v168, v169
	v_max3_f32 v66, v66, v176, v177
	v_max3_f32 v67, v68, v71, v67
	v_max3_f32 v65, v65, v66, v67
	v_mov_b32_e32 v66, v65
	s_nop 1
	v_permlane32_swap_b32_e32 v65, v66
	v_max_f32_e32 v65, v65, v66
	v_sub_f32_e32 v66, v65, v206
	v_max_f32_e32 v65, v206, v65
	v_sub_f32_e32 v67, v206, v65
	v_mul_f32_e32 v67, 0x3e0293ee, v67
	v_exp_f32_e32 v67, v67
	v_cmp_ge_f32_e32 vcc, s31, v66
	s_cmp_eq_u64 vcc, exec
	s_cselect_b64 s[58:59], -1, 0
	s_barrier
	s_waitcnt vmcnt(4)
	v_cndmask_b32_e64 v180, v67, 1.0, s[58:59]
	v_cmp_gt_f32_e32 vcc, 1.0, v180
	ds_write_b128 v201, v[130:133]
	ds_write_b128 v202, v[134:137]
	ds_write_b128 v203, v[138:141] offset:32768
	ds_write_b128 v204, v[142:145] offset:32768
	s_cbranch_vccz .LBB0_825
	v_pk_mul_f32 v[62:63], v[62:63], v[180:181] op_sel_hi:[1,0]
	v_pk_mul_f32 v[60:61], v[60:61], v[180:181] op_sel_hi:[1,0]
	v_pk_mul_f32 v[58:59], v[58:59], v[180:181] op_sel_hi:[1,0]
	v_pk_mul_f32 v[56:57], v[56:57], v[180:181] op_sel_hi:[1,0]
	v_pk_mul_f32 v[54:55], v[54:55], v[180:181] op_sel_hi:[1,0]
	v_pk_mul_f32 v[52:53], v[52:53], v[180:181] op_sel_hi:[1,0]
	v_pk_mul_f32 v[50:51], v[50:51], v[180:181] op_sel_hi:[1,0]
	v_pk_mul_f32 v[48:49], v[48:49], v[180:181] op_sel_hi:[1,0]
	v_pk_mul_f32 v[46:47], v[46:47], v[180:181] op_sel_hi:[1,0]
	v_pk_mul_f32 v[44:45], v[44:45], v[180:181] op_sel_hi:[1,0]
	v_pk_mul_f32 v[42:43], v[42:43], v[180:181] op_sel_hi:[1,0]
	v_pk_mul_f32 v[40:41], v[40:41], v[180:181] op_sel_hi:[1,0]
	v_pk_mul_f32 v[38:39], v[38:39], v[180:181] op_sel_hi:[1,0]
	v_pk_mul_f32 v[36:37], v[36:37], v[180:181] op_sel_hi:[1,0]
	v_pk_mul_f32 v[34:35], v[34:35], v[180:181] op_sel_hi:[1,0]
	v_pk_mul_f32 v[32:33], v[32:33], v[180:181] op_sel_hi:[1,0]
	v_pk_mul_f32 v[30:31], v[30:31], v[180:181] op_sel_hi:[1,0]
	v_pk_mul_f32 v[28:29], v[28:29], v[180:181] op_sel_hi:[1,0]
	v_pk_mul_f32 v[26:27], v[26:27], v[180:181] op_sel_hi:[1,0]
	v_pk_mul_f32 v[24:25], v[24:25], v[180:181] op_sel_hi:[1,0]
	v_pk_mul_f32 v[22:23], v[22:23], v[180:181] op_sel_hi:[1,0]
	v_pk_mul_f32 v[20:21], v[20:21], v[180:181] op_sel_hi:[1,0]
	v_pk_mul_f32 v[18:19], v[18:19], v[180:181] op_sel_hi:[1,0]
	v_pk_mul_f32 v[16:17], v[16:17], v[180:181] op_sel_hi:[1,0]
	v_pk_mul_f32 v[14:15], v[14:15], v[180:181] op_sel_hi:[1,0]
	v_pk_mul_f32 v[12:13], v[12:13], v[180:181] op_sel_hi:[1,0]
	v_pk_mul_f32 v[10:11], v[10:11], v[180:181] op_sel_hi:[1,0]
	v_pk_mul_f32 v[8:9], v[8:9], v[180:181] op_sel_hi:[1,0]
	v_pk_mul_f32 v[6:7], v[6:7], v[180:181] op_sel_hi:[1,0]
	v_pk_mul_f32 v[4:5], v[4:5], v[180:181] op_sel_hi:[1,0]
	v_pk_mul_f32 v[2:3], v[2:3], v[180:181] op_sel_hi:[1,0]
	v_pk_mul_f32 v[0:1], v[0:1], v[180:181] op_sel_hi:[1,0]

.LBB0_834:
	v_max_f32_e32 v66, v163, v172
	v_max_f32_e32 v67, v214, v215
	v_max_f32_e32 v68, v72, v73
	v_max3_f32 v69, v64, v65, v164
	v_max3_f32 v68, v68, v168, v169
	v_max3_f32 v66, v66, v173, v174
	v_max3_f32 v67, v67, v216, v217
	v_max3_f32 v69, v69, v165, v166
	v_max3_f32 v68, v68, v170, v171
	v_max3_f32 v66, v66, v175, v176
	v_max3_f32 v67, v67, v218, v219
	v_max3_f32 v69, v69, v167, v70
	v_max3_f32 v68, v68, v78, v79
	v_max3_f32 v66, v66, v177, v211
	v_max3_f32 v67, v67, v221, v220
	v_max3_f32 v68, v69, v71, v68
	v_max3_f32 v66, v66, v67, v68
	v_mov_b32_e32 v67, v66
	s_nop 1
	v_permlane32_swap_b32_e32 v66, v67
	v_max_f32_e32 v66, v66, v67
	v_sub_f32_e32 v67, v66, v206
	v_max_f32_e32 v66, v206, v66
	v_sub_f32_e32 v68, v206, v66
	v_mul_f32_e32 v68, 0x3e0293ee, v68
	v_exp_f32_e32 v68, v68
	v_cmp_ge_f32_e32 vcc, s31, v67
	s_cmp_eq_u64 vcc, exec
	s_cselect_b64 s[58:59], -1, 0
	s_barrier
	s_waitcnt vmcnt(4)
	v_cndmask_b32_e64 v162, v68, 1.0, s[58:59]
	v_cmp_gt_f32_e32 vcc, 1.0, v162
	ds_write_b128 v201, v[146:149] offset:16384
	ds_write_b128 v202, v[150:153] offset:16384
	ds_write_b128 v203, v[154:157] offset:49152
	ds_write_b128 v204, v[158:161] offset:49152
	s_cbranch_vccz .LBB0_836
	v_pk_mul_f32 v[62:63], v[62:63], v[162:163] op_sel_hi:[1,0]
	v_pk_mul_f32 v[60:61], v[60:61], v[162:163] op_sel_hi:[1,0]
	v_pk_mul_f32 v[58:59], v[58:59], v[162:163] op_sel_hi:[1,0]
	v_pk_mul_f32 v[56:57], v[56:57], v[162:163] op_sel_hi:[1,0]
	v_pk_mul_f32 v[54:55], v[54:55], v[162:163] op_sel_hi:[1,0]
	v_pk_mul_f32 v[52:53], v[52:53], v[162:163] op_sel_hi:[1,0]
	v_pk_mul_f32 v[50:51], v[50:51], v[162:163] op_sel_hi:[1,0]
	v_pk_mul_f32 v[48:49], v[48:49], v[162:163] op_sel_hi:[1,0]
	v_pk_mul_f32 v[46:47], v[46:47], v[162:163] op_sel_hi:[1,0]
	v_pk_mul_f32 v[44:45], v[44:45], v[162:163] op_sel_hi:[1,0]
	v_pk_mul_f32 v[42:43], v[42:43], v[162:163] op_sel_hi:[1,0]
	v_pk_mul_f32 v[40:41], v[40:41], v[162:163] op_sel_hi:[1,0]
	v_pk_mul_f32 v[38:39], v[38:39], v[162:163] op_sel_hi:[1,0]
	v_pk_mul_f32 v[36:37], v[36:37], v[162:163] op_sel_hi:[1,0]
	v_pk_mul_f32 v[34:35], v[34:35], v[162:163] op_sel_hi:[1,0]
	v_pk_mul_f32 v[32:33], v[32:33], v[162:163] op_sel_hi:[1,0]
	v_pk_mul_f32 v[30:31], v[30:31], v[162:163] op_sel_hi:[1,0]
	v_pk_mul_f32 v[28:29], v[28:29], v[162:163] op_sel_hi:[1,0]
	v_pk_mul_f32 v[26:27], v[26:27], v[162:163] op_sel_hi:[1,0]
	v_pk_mul_f32 v[24:25], v[24:25], v[162:163] op_sel_hi:[1,0]
	v_pk_mul_f32 v[22:23], v[22:23], v[162:163] op_sel_hi:[1,0]
	v_pk_mul_f32 v[20:21], v[20:21], v[162:163] op_sel_hi:[1,0]
	v_pk_mul_f32 v[18:19], v[18:19], v[162:163] op_sel_hi:[1,0]
	v_pk_mul_f32 v[16:17], v[16:17], v[162:163] op_sel_hi:[1,0]
	v_pk_mul_f32 v[14:15], v[14:15], v[162:163] op_sel_hi:[1,0]
	v_pk_mul_f32 v[12:13], v[12:13], v[162:163] op_sel_hi:[1,0]
	v_pk_mul_f32 v[10:11], v[10:11], v[162:163] op_sel_hi:[1,0]
	v_pk_mul_f32 v[8:9], v[8:9], v[162:163] op_sel_hi:[1,0]
	v_pk_mul_f32 v[6:7], v[6:7], v[162:163] op_sel_hi:[1,0]
	v_pk_mul_f32 v[4:5], v[4:5], v[162:163] op_sel_hi:[1,0]
	v_pk_mul_f32 v[2:3], v[2:3], v[162:163] op_sel_hi:[1,0]
	v_pk_mul_f32 v[0:1], v[0:1], v[162:163] op_sel_hi:[1,0]

.LBB0_860:
	s_waitcnt vmcnt(4)
	v_add_u32_e32 v41, 32, v72
	v_and_b32_e32 v36, 63, v71
	v_and_b32_e32 v37, 0xfffff0, v72
	v_lshlrev_b32_e32 v38, 1, v72
	v_and_b32_e32 v42, 0xfffff0, v41
	v_lshlrev_b32_e32 v43, 1, v41
	v_and_or_b32 v37, v38, 8, v37
	v_and_or_b32 v42, v43, 8, v42
	v_lshlrev_b32_e32 v44, 4, v36
	s_and_b64 s[2:3], s[22:23], exec
	v_lshrrev_b32_e32 v38, 1, v72
	v_lshrrev_b32_e32 v37, 1, v37
	v_lshrrev_b32_e32 v39, 5, v74
	v_and_b32_e32 v40, 3, v72
	v_lshrrev_b32_e32 v42, 1, v42
	v_lshlrev_b32_e32 v43, 3, v36
	v_and_b32_e32 v45, 0xc0, v44
	v_lshlrev_b32_e32 v36, 1, v36
	s_cselect_b32 s22, 4, 36
	v_or_b32_e32 v37, v37, v39
	v_and_or_b32 v38, v38, 4, v40
	v_lshlrev_b32_e32 v40, 1, v74
	v_or_b32_e32 v39, v42, v39
	v_and_or_b32 v45, v43, 24, v45
	v_and_b32_e32 v36, 32, v36
	v_and_b32_e32 v43, 0x100, v43
	s_cmp_lg_u32 0, -1
	v_lshlrev_b32_e32 v37, 9, v37
	v_lshlrev_b32_e32 v38, 6, v38
	v_lshlrev_b32_e32 v39, 9, v39
	v_or3_b32 v48, v45, v36, v43
	v_and_b32_e32 v36, 48, v40
	s_cselect_b32 s24, 0, 0
	s_add_i32 s2, 0, 0x15000
	v_or3_b32 v37, v37, v38, v36
	v_or3_b32 v36, v39, v38, v36
	v_lshl_add_u32 v38, v73, 12, s2
	v_add_u32_e32 v204, v38, v44
	s_waitcnt vmcnt(3)
	ds_write_b128 v204, v[24:27]
	s_waitcnt vmcnt(2)
	ds_write_b128 v204, v[20:23] offset:1024
	s_waitcnt vmcnt(1)
	ds_write_b128 v204, v[32:35] offset:2048
	s_waitcnt vmcnt(0)
	ds_write_b128 v204, v[28:31] offset:3072
	v_add_u32_e32 v205, 0, v37
	v_lshrrev_b32_e32 v37, 3, v205
	v_xor_b32_e32 v37, v37, v205
	v_and_b32_e32 v37, 0x100, v37
	v_xor_b32_e32 v205, v205, v37
	v_lshlrev_b32_e32 v37, 3, v37
	v_xor_b32_e32 v205, v205, v37
	ds_write_b128 v205, v[12:15]
	v_lshlrev_b32_e32 v12, 8, v72
	v_and_b32_e32 v13, 0x70, v71
	v_bitop3_b32 v12, v40, v12, v13 bitop3:0xde
	v_add_u32_e32 v206, 0, v36
	v_lshrrev_b32_e32 v36, 3, v206
	v_xor_b32_e32 v36, v36, v206
	v_and_b32_e32 v36, 0x100, v36
	v_xor_b32_e32 v206, v206, v36
	v_lshlrev_b32_e32 v36, 3, v36
	v_xor_b32_e32 v206, v206, v36
	v_add_u32_e32 v207, 0, v12
	ds_write_b128 v206, v[16:19]
	ds_write_b128 v207, v[8:11] offset:32768
	v_lshlrev_b32_e32 v8, 8, v41
	v_bitop3_b32 v8, v40, v8, v13 bitop3:0xde
	v_add_u32_e32 v208, 0, v8
	v_and_b32_e32 v42, 0xffffff80, v96
	ds_write_b128 v208, v[4:7] offset:32768
	v_xor_b32_e32 v4, v96, v71
	s_movk_i32 s2, 0x70
	v_and_or_b32 v49, v4, s2, v42
	s_add_i32 s2, 0, 0x10000
	v_add_u32_e32 v4, s2, v49
	ds_write_b128 v4, v[0:3]
	v_lshlrev_b32_e32 v0, 4, v70
	v_lshlrev_b32_e32 v58, 8, v70
	v_and_b32_e32 v59, 0x70, v0
	v_bitop3_b32 v0, v68, v58, v59 bitop3:0xde
	v_add_u32_e32 v209, 0, v0
	s_waitcnt lgkmcnt(0)
	s_barrier
	ds_read_b128 v[16:19], v209 offset:32768
	ds_read_b128 v[20:23], v209 offset:40960
	s_waitcnt lgkmcnt(1)
	v_mfma_f32_32x32x16_bf16 v[32:47], v[16:19], v[158:161], 0
	v_or_b32_e32 v62, 32, v68
	v_bitop3_b32 v50, v62, v58, v59 bitop3:0xde
	v_add_u32_e32 v211, 0, v50
	ds_read_b128 v[50:53], v211 offset:32768
	ds_read_b128 v[54:57], v211 offset:40960
	v_or_b32_e32 v63, 64, v68
	v_or_b32_e32 v64, 0x60, v68
	v_lshlrev_b32_e32 v65, 7, v70
	s_waitcnt lgkmcnt(2)
	v_mfma_f32_32x32x16_bf16 v[16:31], v[20:23], v[158:161], 0
	s_mov_b32 s72, s73
	s_mov_b32 s74, s73
	s_mov_b32 s75, s73
	s_mov_b32 s76, s73
	s_mov_b32 s77, s73
	s_mov_b32 s78, s73
	s_mov_b32 s79, s73
	s_waitcnt lgkmcnt(1)
	v_mfma_f32_32x32x16_bf16 v[32:47], v[50:53], v[154:157], v[32:47]
	v_bitop3_b32 v50, v63, v58, v59 bitop3:0xde
	v_add_u32_e32 v212, 0, v50
	s_mov_b32 s80, s73
	s_mov_b32 s81, s73
	s_mov_b32 s82, s73
	s_mov_b32 s83, s73
	s_mov_b32 s84, s73
	s_waitcnt lgkmcnt(0)
	v_mfma_f32_32x32x16_bf16 v[16:31], v[54:57], v[154:157], v[16:31]
	ds_read_b128 v[50:53], v212 offset:32768
	ds_read_b128 v[54:57], v212 offset:40960
	s_mov_b32 s85, s73
	s_mov_b32 s86, s73
	s_mov_b32 s87, s73
	v_mov_b64_e32 v[0:1], s[72:73]
	v_mov_b32_e32 v183, v129
	v_mov_b32_e32 v97, v129
	s_waitcnt lgkmcnt(1)
	v_mfma_f32_32x32x16_bf16 v[32:47], v[50:53], v[150:153], v[32:47]
	v_bitop3_b32 v50, v64, v58, v59 bitop3:0xde
	v_add_u32_e32 v213, 0, v50
	v_mov_b64_e32 v[2:3], s[74:75]
	v_mov_b64_e32 v[4:5], s[76:77]
	v_mov_b64_e32 v[6:7], s[78:79]
	v_mov_b64_e32 v[8:9], s[80:81]
	v_mov_b64_e32 v[10:11], s[82:83]
	s_waitcnt lgkmcnt(0)
	v_mfma_f32_32x32x16_bf16 v[16:31], v[54:57], v[150:153], v[16:31]
	ds_read_b128 v[50:53], v213 offset:32768
	ds_read_b128 v[54:57], v213 offset:40960
	v_mov_b64_e32 v[12:13], s[84:85]
	v_mov_b64_e32 v[14:15], s[86:87]
	v_add_u32_e32 v228, 0, v49
	v_add_u32_e32 v201, s24, v48
	v_add_u32_e32 v229, 0x12000, v228
	s_waitcnt lgkmcnt(1)
	v_mfma_f32_32x32x16_bf16 v[32:47], v[50:53], v[146:149], v[32:47]
	v_or_b32_e32 v50, 0x80, v68
	v_bitop3_b32 v50, v50, v58, v59 bitop3:0xde
	v_add_u32_e32 v215, 0, v50
	v_lshl_add_u64 v[184:185], s[58:59], 0, v[96:97]
	v_lshl_add_u64 v[186:187], s[8:9], 0, v[96:97]
	v_mov_b32_e32 v210, 0
	v_readlane_b32 s80, v255, 48
	s_waitcnt lgkmcnt(0)
	v_mfma_f32_32x32x16_bf16 v[16:31], v[54:57], v[146:149], v[16:31]
	ds_read_b128 v[50:53], v215 offset:32768
	ds_read_b128 v[54:57], v215 offset:40960
	s_movk_i32 s84, 0xffe0
	s_waitcnt lgkmcnt(1)
	v_mfma_f32_32x32x16_bf16 v[32:47], v[50:53], v[142:145], v[32:47]
	v_or_b32_e32 v50, 0xa0, v68
	v_bitop3_b32 v50, v50, v58, v59 bitop3:0xde
	v_add_u32_e32 v217, 0, v50
	s_waitcnt lgkmcnt(0)
	v_mfma_f32_32x32x16_bf16 v[16:31], v[54:57], v[142:145], v[16:31]
	ds_read_b128 v[50:53], v217 offset:32768
	ds_read_b128 v[54:57], v217 offset:40960
	s_waitcnt lgkmcnt(1)
	v_mfma_f32_32x32x16_bf16 v[32:47], v[50:53], v[138:141], v[32:47]
	v_or_b32_e32 v50, 0xc0, v68
	v_bitop3_b32 v50, v50, v58, v59 bitop3:0xde
	v_add_u32_e32 v214, 0, v50
	s_waitcnt lgkmcnt(0)
	v_mfma_f32_32x32x16_bf16 v[16:31], v[54:57], v[138:141], v[16:31]
	ds_read_b128 v[50:53], v214 offset:32768
	ds_read_b128 v[54:57], v214 offset:40960
	s_waitcnt lgkmcnt(1)
	v_mfma_f32_32x32x16_bf16 v[32:47], v[50:53], v[134:137], v[32:47]
	v_or_b32_e32 v50, 0xe0, v68
	v_bitop3_b32 v50, v50, v58, v59 bitop3:0xde
	v_add_u32_e32 v216, 0, v50
	s_waitcnt lgkmcnt(0)
	v_mfma_f32_32x32x16_bf16 v[16:31], v[54:57], v[134:137], v[16:31]
	ds_read_b128 v[50:53], v216 offset:32768
	ds_read_b128 v[54:57], v216 offset:40960
	s_waitcnt lgkmcnt(1)
	v_mfma_f32_32x32x16_bf16 v[32:47], v[50:53], v[130:133], v[32:47]
	v_lshlrev_b32_e32 v50, 3, v70
	v_and_b32_e32 v66, 0x70, v50
	v_bitop3_b32 v218, v68, v65, v66 bitop3:0xde
	v_add_u32_e32 v219, s2, v218
	v_bitop3_b32 v220, v62, v65, v66 bitop3:0xde
	v_add_u32_e32 v221, s2, v220
	v_bitop3_b32 v222, v63, v65, v66 bitop3:0xde
	s_waitcnt lgkmcnt(0)
	v_mfma_f32_32x32x16_bf16 v[16:31], v[54:57], v[130:133], v[16:31]
	ds_read_b128 v[50:53], v219
	ds_read_b128 v[54:57], v219 offset:4096
	ds_read_b128 v[58:61], v204
	v_add_u32_e32 v223, s2, v222
	v_bitop3_b32 v224, v64, v65, v66 bitop3:0xde
	v_add_u32_e32 v225, s2, v224
	s_waitcnt lgkmcnt(0)
	v_mfma_f32_32x32x16_bf16 v[32:47], v[50:53], v[58:61], v[32:47]
	v_mfma_f32_32x32x16_bf16 v[16:31], v[54:57], v[58:61], v[16:31]
	ds_read_b128 v[50:53], v221
	ds_read_b128 v[54:57], v221 offset:4096
	ds_read_b128 v[58:61], v204 offset:1024
	s_waitcnt lgkmcnt(0)
	v_mfma_f32_32x32x16_bf16 v[32:47], v[50:53], v[58:61], v[32:47]
	v_mfma_f32_32x32x16_bf16 v[16:31], v[54:57], v[58:61], v[16:31]
	ds_read_b128 v[50:53], v223
	ds_read_b128 v[54:57], v223 offset:4096
	ds_read_b128 v[58:61], v204 offset:2048
	s_waitcnt lgkmcnt(0)
	v_mfma_f32_32x32x16_bf16 v[32:47], v[50:53], v[58:61], v[32:47]
	v_mfma_f32_32x32x16_bf16 v[16:31], v[54:57], v[58:61], v[16:31]
	ds_read_b128 v[50:53], v225
	ds_read_b128 v[54:57], v225 offset:4096
	ds_read_b128 v[58:61], v204 offset:3072
	s_waitcnt lgkmcnt(0)
	v_mfma_f32_32x32x16_bf16 v[32:47], v[50:53], v[58:61], v[32:47]
	v_mfma_f32_32x32x16_bf16 v[16:31], v[54:57], v[58:61], v[16:31]
	s_nop 10
	v_max_f32_e32 v50, v33, v33
	v_max_f32_e32 v51, v32, v32
	v_max_f32_e32 v50, v51, v50
	v_max_f32_e32 v51, v41, v41
	v_max_f32_e32 v52, v40, v40
	v_max_f32_e32 v51, v52, v51
	v_max3_f32 v50, v50, v34, v35
	v_max_f32_e32 v52, v25, v25
	v_max_f32_e32 v53, v24, v24
	v_max_f32_e32 v52, v53, v52
	v_max3_f32 v53, v16, v17, v18
	v_max3_f32 v52, v52, v26, v27
	v_max3_f32 v51, v51, v42, v43
	v_max3_f32 v53, v53, v19, v20
	v_max3_f32 v52, v52, v28, v29
	v_max3_f32 v50, v50, v36, v37
	v_max3_f32 v51, v51, v44, v45
	v_max3_f32 v53, v53, v21, v22
	v_max3_f32 v52, v52, v30, v31
	v_max3_f32 v50, v50, v38, v39
	v_max3_f32 v51, v51, v46, v47
	v_max3_f32 v52, v53, v23, v52
	v_max3_f32 v50, v50, v51, v52
	v_mov_b32_e32 v51, v50
	s_nop 1
	v_permlane32_swap_b32_e32 v50, v51
	v_max_f32_e32 v51, v51, v51
	v_max_f32_e32 v50, v50, v50
	v_max_f32_e32 v50, v50, v51
	v_add_f32_e32 v51, 0x7149f2ca, v50
	v_max_f32_e32 v50, 0xf149f2ca, v50
	v_cmp_ge_f32_e32 vcc, s34, v51
	v_sub_f32_e32 v51, 0xf149f2ca, v50
	v_mul_f32_e32 v51, 0x3dd53b94, v51
	s_cmp_eq_u64 vcc, exec
	v_exp_f32_e32 v51, v51
	s_cselect_b64 vcc, -1, 0
	v_cndmask_b32_e32 v227, v50, v230, vcc
	v_mul_f32_e32 v50, 0xbdd53b94, v227
	v_cndmask_b32_e64 v226, v51, 1.0, vcc
	v_mov_b32_e32 v51, v50
	s_add_u32 s2, s18, s92
	v_fmac_f32_e32 v51, 0x3dd53b94, v47
	s_addc_u32 s3, s19, s93
	v_fmamk_f32 v32, v32, 0x3dd53b94, v50
	v_fmamk_f32 v33, v33, 0x3dd53b94, v50
	v_pk_fma_f32 v[80:81], v[16:17], s[54:55], v[50:51] op_sel_hi:[1,0,0]
	s_add_u32 s74, s16, s92
	v_lshl_add_u64 v[16:17], s[2:3], 0, v[128:129]
	v_fmamk_f32 v34, v34, 0x3dd53b94, v50
	v_fmamk_f32 v35, v35, 0x3dd53b94, v50
	v_pk_fma_f32 v[84:85], v[20:21], s[54:55], v[50:51] op_sel_hi:[1,0,0]
	v_pk_fma_f32 v[82:83], v[18:19], s[54:55], v[50:51] op_sel_hi:[1,0,0]
	v_exp_f32_e32 v64, v32
	v_exp_f32_e32 v65, v33
	s_addc_u32 s75, s17, s93
	global_load_dwordx4 v[16:19], v[16:17], off
	v_lshl_add_u64 v[20:21], s[2:3], 0, v[182:183]
	v_lshl_add_u64 v[32:33], s[96:97], 0, v[96:97]
	v_pk_fma_f32 v[88:89], v[24:25], s[54:55], v[50:51] op_sel_hi:[1,0,0]
	v_pk_fma_f32 v[86:87], v[22:23], s[54:55], v[50:51] op_sel_hi:[1,0,0]
	v_exp_f32_e32 v66, v34
	v_exp_f32_e32 v67, v35
	global_load_dwordx4 v[20:23], v[20:21], off
	v_lshl_add_u64 v[24:25], s[74:75], 0, v[128:129]
	global_load_dwordx4 v[32:35], v[32:33], off
	v_pk_fma_f32 v[92:93], v[28:29], s[54:55], v[50:51] op_sel_hi:[1,0,0]
	v_pk_fma_f32 v[90:91], v[26:27], s[54:55], v[50:51] op_sel_hi:[1,0,0]
	global_load_dwordx4 v[24:27], v[24:25], off
	v_lshl_add_u64 v[28:29], s[74:75], 0, v[182:183]
	v_pk_fma_f32 v[94:95], v[30:31], s[54:55], v[50:51] op_sel_hi:[1,0,0]
	global_load_dwordx4 v[28:31], v[28:29], off
	v_fmamk_f32 v36, v36, 0x3dd53b94, v50
	v_fmamk_f32 v37, v37, 0x3dd53b94, v50
	v_fmamk_f32 v38, v38, 0x3dd53b94, v50
	v_fmamk_f32 v39, v39, 0x3dd53b94, v50
	v_fmamk_f32 v40, v40, 0x3dd53b94, v50
	v_fmamk_f32 v41, v41, 0x3dd53b94, v50
	v_fmamk_f32 v42, v42, 0x3dd53b94, v50
	v_fmamk_f32 v43, v43, 0x3dd53b94, v50
	v_fmamk_f32 v44, v44, 0x3dd53b94, v50
	v_fmamk_f32 v45, v45, 0x3dd53b94, v50
	v_fmamk_f32 v46, v46, 0x3dd53b94, v50
	v_exp_f32_e32 v68, v36
	v_exp_f32_e32 v69, v37
	v_exp_f32_e32 v70, v38
	v_exp_f32_e32 v71, v39
	v_exp_f32_e32 v72, v40
	v_exp_f32_e32 v73, v41
	v_exp_f32_e32 v74, v42
	v_exp_f32_e32 v75, v43
	v_exp_f32_e32 v76, v44
	v_exp_f32_e32 v77, v45
	v_exp_f32_e32 v78, v46
	v_exp_f32_e32 v79, v51
	s_waitcnt vmcnt(0)
	ds_write_b128 v205, v[16:19] offset:16384
	ds_write_b128 v206, v[20:23] offset:16384
	ds_write_b128 v207, v[24:27] offset:49152
	ds_write_b128 v208, v[28:31] offset:49152
	s_addk_i32 s24, 0x4000
	v_lshl_add_u64 v[16:17], s[20:21], 0, v[128:129]
	v_lshl_add_u64 v[18:19], s[20:21], 0, v[182:183]
	ds_write_b128 v229, v[32:35]
	v_add_u32_e32 v203, s24, v48
	v_lshl_add_u64 v[188:189], s[12:13], 0, v[16:17]
	v_lshl_add_u64 v[190:191], s[12:13], 0, v[18:19]
	v_lshl_add_u64 v[192:193], s[14:15], 0, v[16:17]
	v_lshl_add_u64 v[198:199], s[14:15], 0, v[18:19]
	v_mov_b64_e32 v[62:63], v[14:15]
	v_mov_b64_e32 v[46:47], v[14:15]
	v_mov_b64_e32 v[30:31], v[14:15]
	s_add_i32 s23, s22, -1
	s_mov_b32 s20, 2
	v_mov_b64_e32 v[60:61], v[12:13]
	v_mov_b64_e32 v[58:59], v[10:11]
	v_mov_b64_e32 v[56:57], v[8:9]
	v_mov_b64_e32 v[54:55], v[6:7]
	v_mov_b64_e32 v[52:53], v[4:5]
	v_mov_b64_e32 v[50:51], v[2:3]
	v_mov_b64_e32 v[48:49], v[0:1]
	v_mov_b64_e32 v[44:45], v[12:13]
	v_mov_b64_e32 v[42:43], v[10:11]
	v_mov_b64_e32 v[40:41], v[8:9]
	v_mov_b64_e32 v[38:39], v[6:7]
	v_mov_b64_e32 v[36:37], v[4:5]
	v_mov_b64_e32 v[34:35], v[2:3]
	v_mov_b64_e32 v[32:33], v[0:1]
	v_mov_b64_e32 v[28:29], v[12:13]
	v_mov_b64_e32 v[26:27], v[10:11]
	v_mov_b64_e32 v[24:25], v[8:9]
	v_mov_b64_e32 v[22:23], v[6:7]
	v_mov_b64_e32 v[20:21], v[4:5]
	v_mov_b64_e32 v[18:19], v[2:3]
	v_mov_b64_e32 v[16:17], v[0:1]
	v_readlane_b32 s21, v252, 17
	s_waitcnt lgkmcnt(0)
	s_barrier

.Lmla_resc_back_0:
	v_mfma_f32_32x32x16_bf16 v[48:63], v[92:95], v[64:67], v[48:63]
	ds_read_b64_tr_b16 v[80:81], v201 offset:0x400
	ds_read_b64_tr_b16 v[82:83], v201 offset:0xc00
	ds_read_b64_tr_b16 v[84:85], v201 offset:0x1400
	ds_read_b64_tr_b16 v[86:87], v201 offset:0x1c00
	v_mfma_f32_32x32x16_bf16 v[48:63], v[178:181], v[68:71], v[48:63]
	ds_read_b64_tr_b16 v[92:93], v201 offset:0x2400
	v_mul_f32_e32 v178, 0xbdd53b94, v227
	ds_read_b64_tr_b16 v[94:95], v201 offset:0x2c00
	v_fmamk_f32 v179, v112, 0x3dd53b94, v178
	v_fmamk_f32 v180, v113, 0x3dd53b94, v178
	ds_read_b64_tr_b16 v[112:113], v201 offset:0x3400
	v_fmamk_f32 v181, v114, 0x3dd53b94, v178
	v_fmamk_f32 v194, v115, 0x3dd53b94, v178
	ds_read_b64_tr_b16 v[114:115], v201 offset:0x3c00
	s_waitcnt lgkmcnt(0)
	v_fmamk_f32 v195, v116, 0x3dd53b94, v178
	v_fmamk_f32 v196, v117, 0x3dd53b94, v178
	v_fmamk_f32 v197, v118, 0x3dd53b94, v178
	v_fmamk_f32 v200, v119, 0x3dd53b94, v178
	v_fmamk_f32 v239, v120, 0x3dd53b94, v178
	v_fmamk_f32 v240, v121, 0x3dd53b94, v178
	v_fmamk_f32 v241, v122, 0x3dd53b94, v178
	v_fmamk_f32 v242, v123, 0x3dd53b94, v178
	v_fmamk_f32 v243, v124, 0x3dd53b94, v178
	v_fmamk_f32 v244, v125, 0x3dd53b94, v178
	v_fmamk_f32 v245, v126, 0x3dd53b94, v178
	v_fmamk_f32 v246, v127, 0x3dd53b94, v178
	v_mfma_f32_32x32x16_bf16 v[32:47], v[80:83], v[88:91], v[32:47]
	v_fma_f32 v116, v100, s54, v178
	v_fma_f32 v117, v101, s54, v178
	v_fma_f32 v118, v102, s54, v178
	v_fma_f32 v119, v103, s54, v178
	v_fma_f32 v120, v104, s54, v178
	v_fma_f32 v121, v105, s54, v178
	v_pk_fma_f32 v[122:123], v[106:107], s[54:55], v[178:179] op_sel_hi:[1,0,0]
	v_exp_f32_e32 v80, v179
	v_exp_f32_e32 v81, v180
	v_exp_f32_e32 v82, v181
	v_mfma_f32_32x32x16_bf16 v[32:47], v[84:87], v[72:75], v[32:47]
	v_exp_f32_e32 v83, v194
	v_exp_f32_e32 v84, v195
	v_exp_f32_e32 v85, v196
	v_exp_f32_e32 v86, v197
	v_exp_f32_e32 v87, v200
	v_pk_fma_f32 v[126:127], v[110:111], s[54:55], v[178:179] op_sel_hi:[1,0,0]
	v_pk_fma_f32 v[124:125], v[108:109], s[54:55], v[178:179] op_sel_hi:[1,0,0]
	v_mfma_f32_32x32x16_bf16 v[32:47], v[92:95], v[64:67], v[32:47]
	ds_read_b64_tr_b16 v[92:93], v201 offset:0x600
	ds_read_b64_tr_b16 v[94:95], v201 offset:0xe00
	v_mfma_f32_32x32x16_bf16 v[32:47], v[112:115], v[68:71], v[32:47]
	v_fma_f32 v112, v96, s54, v178
	v_fma_f32 v113, v97, s54, v178
	ds_read_b64_tr_b16 v[96:97], v201 offset:0x1600
	v_fma_f32 v114, v98, s54, v178
	v_fma_f32 v115, v99, s54, v178
	ds_read_b64_tr_b16 v[98:99], v201 offset:0x1e00
	ds_read_b64_tr_b16 v[100:101], v201 offset:0x2600
	ds_read_b64_tr_b16 v[102:103], v201 offset:0x2e00
	ds_read_b64_tr_b16 v[104:105], v201 offset:0x3600
	ds_read_b64_tr_b16 v[106:107], v201 offset:0x3e00
	s_waitcnt lgkmcnt(0)
	v_mfma_f32_32x32x16_bf16 v[16:31], v[92:95], v[88:91], v[16:31]
	v_exp_f32_e32 v88, v239
	v_exp_f32_e32 v89, v240
	v_exp_f32_e32 v90, v241
	v_exp_f32_e32 v91, v242
	v_exp_f32_e32 v92, v243
	v_exp_f32_e32 v93, v244
	v_exp_f32_e32 v94, v245
	v_mfma_f32_32x32x16_bf16 v[16:31], v[96:99], v[72:75], v[16:31]
	v_exp_f32_e32 v95, v246
	s_barrier
	s_waitcnt vmcnt(0)
	v_cmp_gt_f32_e32 vcc, 1.0, v202
	v_mfma_f32_32x32x16_bf16 v[16:31], v[100:103], v[64:67], v[16:31]
	v_add_u32_e32 v64, 0x10000, v228
	ds_write_b128 v205, v[76:79]
	ds_write_b128 v206, v[162:165]
	ds_write_b128 v207, v[166:169] offset:32768
	ds_write_b128 v208, v[174:177] offset:32768
	ds_write_b128 v64, v[170:173]
	v_mfma_f32_32x32x16_bf16 v[16:31], v[104:107], v[68:71], v[16:31]
	s_cbranch_vccz .LBB0_863
	v_pk_mul_f32 v[14:15], v[14:15], v[202:203] op_sel_hi:[1,0]
	v_pk_mul_f32 v[12:13], v[12:13], v[202:203] op_sel_hi:[1,0]
	v_pk_mul_f32 v[10:11], v[10:11], v[202:203] op_sel_hi:[1,0]
	v_pk_mul_f32 v[8:9], v[8:9], v[202:203] op_sel_hi:[1,0]
	v_pk_mul_f32 v[6:7], v[6:7], v[202:203] op_sel_hi:[1,0]
	v_pk_mul_f32 v[4:5], v[4:5], v[202:203] op_sel_hi:[1,0]
	v_pk_mul_f32 v[2:3], v[2:3], v[202:203] op_sel_hi:[1,0]
	v_pk_mul_f32 v[0:1], v[0:1], v[202:203] op_sel_hi:[1,0]
	v_pk_mul_f32 v[62:63], v[62:63], v[202:203] op_sel_hi:[1,0]
	v_pk_mul_f32 v[60:61], v[60:61], v[202:203] op_sel_hi:[1,0]
	v_pk_mul_f32 v[58:59], v[58:59], v[202:203] op_sel_hi:[1,0]
	v_pk_mul_f32 v[56:57], v[56:57], v[202:203] op_sel_hi:[1,0]
	v_pk_mul_f32 v[54:55], v[54:55], v[202:203] op_sel_hi:[1,0]
	v_pk_mul_f32 v[52:53], v[52:53], v[202:203] op_sel_hi:[1,0]
	v_pk_mul_f32 v[50:51], v[50:51], v[202:203] op_sel_hi:[1,0]
	v_pk_mul_f32 v[48:49], v[48:49], v[202:203] op_sel_hi:[1,0]
	v_pk_mul_f32 v[46:47], v[202:203], v[46:47] op_sel_hi:[0,1]
	v_pk_mul_f32 v[44:45], v[202:203], v[44:45] op_sel_hi:[0,1]
	v_pk_mul_f32 v[42:43], v[202:203], v[42:43] op_sel_hi:[0,1]
	v_pk_mul_f32 v[40:41], v[202:203], v[40:41] op_sel_hi:[0,1]
	v_pk_mul_f32 v[38:39], v[202:203], v[38:39] op_sel_hi:[0,1]
	v_pk_mul_f32 v[36:37], v[202:203], v[36:37] op_sel_hi:[0,1]
	v_pk_mul_f32 v[34:35], v[202:203], v[34:35] op_sel_hi:[0,1]
	v_pk_mul_f32 v[32:33], v[202:203], v[32:33] op_sel_hi:[0,1]
	v_pk_mul_f32 v[30:31], v[202:203], v[30:31] op_sel_hi:[0,1]
	v_pk_mul_f32 v[28:29], v[202:203], v[28:29] op_sel_hi:[0,1]
	v_pk_mul_f32 v[26:27], v[202:203], v[26:27] op_sel_hi:[0,1]
	v_pk_mul_f32 v[24:25], v[202:203], v[24:25] op_sel_hi:[0,1]
	v_pk_mul_f32 v[22:23], v[202:203], v[22:23] op_sel_hi:[0,1]
	v_pk_mul_f32 v[20:21], v[202:203], v[20:21] op_sel_hi:[0,1]
	v_pk_mul_f32 v[18:19], v[202:203], v[18:19] op_sel_hi:[0,1]
	v_pk_mul_f32 v[16:17], v[202:203], v[16:17] op_sel_hi:[0,1]

.Lmla_resc_back_1:
	v_mfma_f32_32x32x16_bf16 v[48:63], v[88:91], v[112:115], v[48:63]
	ds_read_b64_tr_b16 v[80:81], v203 offset:0x400
	ds_read_b64_tr_b16 v[82:83], v203 offset:0xc00
	ds_read_b64_tr_b16 v[84:85], v203 offset:0x1400
	ds_read_b64_tr_b16 v[86:87], v203 offset:0x1c00
	v_mfma_f32_32x32x16_bf16 v[48:63], v[92:95], v[116:119], v[48:63]
	ds_read_b64_tr_b16 v[88:89], v203 offset:0x2400
	ds_read_b64_tr_b16 v[90:91], v203 offset:0x2c00
	ds_read_b64_tr_b16 v[92:93], v203 offset:0x3400
	ds_read_b64_tr_b16 v[94:95], v203 offset:0x3c00
	s_waitcnt lgkmcnt(0)
	v_mul_f32_e32 v242, 0xbdd53b94, v227
	v_fmamk_f32 v96, v96, 0x3dd53b94, v242
	v_fmamk_f32 v97, v97, 0x3dd53b94, v242
	v_fmamk_f32 v98, v98, 0x3dd53b94, v242
	v_fmamk_f32 v99, v99, 0x3dd53b94, v242
	v_fmamk_f32 v100, v100, 0x3dd53b94, v242
	v_fmamk_f32 v101, v101, 0x3dd53b94, v242
	v_fmamk_f32 v102, v102, 0x3dd53b94, v242
	v_fmamk_f32 v103, v103, 0x3dd53b94, v242
	v_fmamk_f32 v194, v104, 0x3dd53b94, v242
	v_fmamk_f32 v195, v105, 0x3dd53b94, v242
	v_fmamk_f32 v196, v106, 0x3dd53b94, v242
	v_fmamk_f32 v197, v107, 0x3dd53b94, v242
	v_fmamk_f32 v108, v108, 0x3dd53b94, v242
	v_fmamk_f32 v109, v109, 0x3dd53b94, v242
	v_fmamk_f32 v110, v110, 0x3dd53b94, v242
	v_fmamk_f32 v111, v111, 0x3dd53b94, v242
	v_mfma_f32_32x32x16_bf16 v[32:47], v[80:83], v[124:127], v[32:47]
	v_fma_f32 v80, v64, s54, v242
	v_fma_f32 v81, v65, s54, v242
	v_exp_f32_e32 v64, v96
	v_exp_f32_e32 v65, v97
	v_pk_fma_f32 v[82:83], v[66:67], s[54:55], v[242:243] op_sel_hi:[1,0,0]
	v_exp_f32_e32 v66, v98
	v_exp_f32_e32 v67, v99
	v_mfma_f32_32x32x16_bf16 v[32:47], v[84:87], v[120:123], v[32:47]
	v_fma_f32 v84, v68, s54, v242
	v_fma_f32 v85, v69, s54, v242
	v_exp_f32_e32 v68, v100
	v_exp_f32_e32 v69, v101
	v_pk_fma_f32 v[86:87], v[70:71], s[54:55], v[242:243] op_sel_hi:[1,0,0]
	v_exp_f32_e32 v70, v102
	v_exp_f32_e32 v71, v103
	v_mfma_f32_32x32x16_bf16 v[32:47], v[88:91], v[112:115], v[32:47]
	v_fma_f32 v88, v72, s54, v242
	v_fma_f32 v89, v73, s54, v242
	ds_read_b64_tr_b16 v[72:73], v203 offset:0x600
	v_fma_f32 v90, v74, s54, v242
	v_fma_f32 v91, v75, s54, v242
	ds_read_b64_tr_b16 v[74:75], v203 offset:0xe00
	ds_read_b64_tr_b16 v[96:97], v203 offset:0x1600
	ds_read_b64_tr_b16 v[98:99], v203 offset:0x1e00
	ds_read_b64_tr_b16 v[100:101], v203 offset:0x2600
	v_mfma_f32_32x32x16_bf16 v[32:47], v[92:95], v[116:119], v[32:47]
	ds_read_b64_tr_b16 v[102:103], v203 offset:0x2e00
	ds_read_b64_tr_b16 v[104:105], v203 offset:0x3600
	ds_read_b64_tr_b16 v[106:107], v203 offset:0x3e00
	s_waitcnt lgkmcnt(0)
	v_fma_f32 v94, v78, s54, v242
	v_fma_f32 v95, v79, s54, v242
	v_fma_f32 v92, v76, s54, v242
	v_fma_f32 v93, v77, s54, v242
	v_mfma_f32_32x32x16_bf16 v[16:31], v[72:75], v[124:127], v[16:31]
	v_exp_f32_e32 v72, v194
	v_exp_f32_e32 v73, v195
	v_exp_f32_e32 v74, v196
	v_exp_f32_e32 v75, v197
	v_exp_f32_e32 v76, v108
	v_exp_f32_e32 v77, v109
	v_exp_f32_e32 v78, v110
	v_mfma_f32_32x32x16_bf16 v[16:31], v[96:99], v[120:123], v[16:31]
	v_exp_f32_e32 v79, v111
	s_barrier
	s_waitcnt vmcnt(0)
	v_cmp_gt_f32_e32 vcc, 1.0, v200
	v_mfma_f32_32x32x16_bf16 v[16:31], v[100:103], v[112:115], v[16:31]
	ds_write_b128 v205, v[162:165] offset:16384
	ds_write_b128 v206, v[166:169] offset:16384
	ds_write_b128 v207, v[170:173] offset:49152
	ds_write_b128 v208, v[174:177] offset:49152
	ds_write_b128 v229, v[178:181]
	v_mfma_f32_32x32x16_bf16 v[16:31], v[104:107], v[116:119], v[16:31]
	s_cbranch_vccz .LBB0_865
	v_pk_mul_f32 v[14:15], v[14:15], v[200:201] op_sel_hi:[1,0]
	v_pk_mul_f32 v[12:13], v[12:13], v[200:201] op_sel_hi:[1,0]
	v_pk_mul_f32 v[10:11], v[10:11], v[200:201] op_sel_hi:[1,0]
	v_pk_mul_f32 v[8:9], v[8:9], v[200:201] op_sel_hi:[1,0]
	v_pk_mul_f32 v[6:7], v[6:7], v[200:201] op_sel_hi:[1,0]
	v_pk_mul_f32 v[4:5], v[4:5], v[200:201] op_sel_hi:[1,0]
	v_pk_mul_f32 v[2:3], v[2:3], v[200:201] op_sel_hi:[1,0]
	v_pk_mul_f32 v[0:1], v[0:1], v[200:201] op_sel_hi:[1,0]
	v_pk_mul_f32 v[62:63], v[62:63], v[200:201] op_sel_hi:[1,0]
	v_pk_mul_f32 v[60:61], v[60:61], v[200:201] op_sel_hi:[1,0]
	v_pk_mul_f32 v[58:59], v[58:59], v[200:201] op_sel_hi:[1,0]
	v_pk_mul_f32 v[56:57], v[56:57], v[200:201] op_sel_hi:[1,0]
	v_pk_mul_f32 v[54:55], v[54:55], v[200:201] op_sel_hi:[1,0]
	v_pk_mul_f32 v[52:53], v[52:53], v[200:201] op_sel_hi:[1,0]
	v_pk_mul_f32 v[50:51], v[50:51], v[200:201] op_sel_hi:[1,0]
	v_pk_mul_f32 v[48:49], v[48:49], v[200:201] op_sel_hi:[1,0]
	v_pk_mul_f32 v[46:47], v[200:201], v[46:47] op_sel_hi:[0,1]
	v_pk_mul_f32 v[44:45], v[200:201], v[44:45] op_sel_hi:[0,1]
	v_pk_mul_f32 v[42:43], v[200:201], v[42:43] op_sel_hi:[0,1]
	v_pk_mul_f32 v[40:41], v[200:201], v[40:41] op_sel_hi:[0,1]
	v_pk_mul_f32 v[38:39], v[200:201], v[38:39] op_sel_hi:[0,1]
	v_pk_mul_f32 v[36:37], v[200:201], v[36:37] op_sel_hi:[0,1]
	v_pk_mul_f32 v[34:35], v[200:201], v[34:35] op_sel_hi:[0,1]
	v_pk_mul_f32 v[32:33], v[200:201], v[32:33] op_sel_hi:[0,1]
	v_pk_mul_f32 v[30:31], v[200:201], v[30:31] op_sel_hi:[0,1]
	v_pk_mul_f32 v[28:29], v[200:201], v[28:29] op_sel_hi:[0,1]
	v_pk_mul_f32 v[26:27], v[200:201], v[26:27] op_sel_hi:[0,1]
	v_pk_mul_f32 v[24:25], v[200:201], v[24:25] op_sel_hi:[0,1]
	v_pk_mul_f32 v[22:23], v[200:201], v[22:23] op_sel_hi:[0,1]
	v_pk_mul_f32 v[20:21], v[200:201], v[20:21] op_sel_hi:[0,1]
	v_pk_mul_f32 v[18:19], v[200:201], v[18:19] op_sel_hi:[0,1]
	v_pk_mul_f32 v[16:17], v[200:201], v[16:17] op_sel_hi:[0,1]

.LBB0_881:
	ds_read_b128 v[96:99], v216 offset:49152
	ds_read_b128 v[100:103], v216 offset:57344
	ds_read_b128 v[178:181], v218 offset:49152
	ds_read_b128 v[182:185], v218 offset:57344
	ds_read_b128 v[240:243], v219 offset:49152
	ds_read_b128 v[244:247], v219 offset:57344
	v_add_f32_e32 v88, v64, v65
	v_add_f32_e32 v89, v72, v73
	v_add_f32_e32 v90, v80, v81
	v_add_f32_e32 v91, v194, v195
	v_add_f32_e32 v88, v66, v88
	v_add_f32_e32 v89, v74, v89
	v_add_f32_e32 v90, v82, v90
	s_waitcnt lgkmcnt(4)
	v_mfma_f32_32x32x16_bf16 v[112:127], v[96:99], v[138:141], 0
	v_mfma_f32_32x32x16_bf16 v[96:111], v[100:103], v[138:141], 0
	v_add_f32_e32 v91, v196, v91
	v_add_f32_e32 v88, v67, v88
	v_add_f32_e32 v89, v75, v89
	v_add_f32_e32 v90, v83, v90
	v_add_f32_e32 v91, v197, v91
	v_add_f32_e32 v88, v68, v88
	v_add_f32_e32 v89, v76, v89
	s_waitcnt lgkmcnt(2)
	v_mfma_f32_32x32x16_bf16 v[112:127], v[178:181], v[154:157], v[112:127]
	v_mfma_f32_32x32x16_bf16 v[96:111], v[182:185], v[154:157], v[96:111]
	ds_read_b128 v[178:181], v220 offset:49152
	ds_read_b128 v[182:185], v220 offset:57344
	v_add_f32_e32 v90, v84, v90
	v_add_f32_e32 v91, v92, v91
	v_add_f32_e32 v88, v69, v88
	v_add_f32_e32 v89, v77, v89
	v_add_f32_e32 v90, v85, v90
	v_add_f32_e32 v91, v93, v91
	v_add_f32_e32 v88, v70, v88
	s_waitcnt lgkmcnt(2)
	v_mfma_f32_32x32x16_bf16 v[112:127], v[240:243], v[158:161], v[112:127]
	v_mfma_f32_32x32x16_bf16 v[96:111], v[244:247], v[158:161], v[96:111]
	ds_read_b128 v[240:243], v221 offset:49152
	ds_read_b128 v[244:247], v221 offset:57344
	v_add_f32_e32 v89, v78, v89
	v_add_f32_e32 v90, v86, v90
	v_add_f32_e32 v91, v94, v91
	v_add_f32_e32 v88, v71, v88
	v_add_f32_e32 v89, v79, v89
	v_add_f32_e32 v90, v87, v90
	v_add_f32_e32 v91, v95, v91
	s_waitcnt lgkmcnt(2)
	v_mfma_f32_32x32x16_bf16 v[112:127], v[178:181], v[150:153], v[112:127]
	v_mfma_f32_32x32x16_bf16 v[96:111], v[182:185], v[150:153], v[96:111]
	ds_read_b128 v[178:181], v222 offset:49152
	ds_read_b128 v[182:185], v222 offset:57344
	v_add_f32_e32 v88, v89, v88
	v_add_f32_e32 v89, v91, v90
	v_add_f32_e32 v227, v88, v89
	v_cvt_pk_bf16_f32 v88, v64, v65
	v_cvt_pk_bf16_f32 v89, v66, v67
	v_cvt_pk_bf16_f32 v90, v68, v69
	v_cvt_pk_bf16_f32 v91, v70, v71
	s_waitcnt lgkmcnt(2)
	v_mfma_f32_32x32x16_bf16 v[112:127], v[240:243], v[146:149], v[112:127]
	v_mfma_f32_32x32x16_bf16 v[96:111], v[244:247], v[146:149], v[96:111]
	ds_read_b128 v[240:243], v224 offset:49152
	ds_read_b128 v[244:247], v224 offset:57344
	v_cvt_pk_bf16_f32 v72, v72, v73
	v_cvt_pk_bf16_f32 v73, v74, v75
	v_cvt_pk_bf16_f32 v74, v76, v77
	v_cvt_pk_bf16_f32 v75, v78, v79
	s_waitcnt lgkmcnt(2)
	v_mfma_f32_32x32x16_bf16 v[112:127], v[178:181], v[142:145], v[112:127]
	v_mfma_f32_32x32x16_bf16 v[96:111], v[182:185], v[142:145], v[96:111]
	ds_read_b128 v[178:181], v223 offset:49152
	ds_read_b128 v[182:185], v223 offset:57344
	v_cvt_pk_bf16_f32 v64, v80, v81
	v_cvt_pk_bf16_f32 v65, v82, v83
	v_cvt_pk_bf16_f32 v66, v84, v85
	v_cvt_pk_bf16_f32 v67, v86, v87
	v_cvt_pk_bf16_f32 v68, v194, v195
	v_cvt_pk_bf16_f32 v69, v196, v197
	v_cvt_pk_bf16_f32 v70, v92, v93
	s_waitcnt lgkmcnt(2)
	v_mfma_f32_32x32x16_bf16 v[112:127], v[240:243], v[134:137], v[112:127]
	v_mfma_f32_32x32x16_bf16 v[96:111], v[244:247], v[134:137], v[96:111]
	v_cvt_pk_bf16_f32 v71, v94, v95
	s_waitcnt lgkmcnt(0)
	v_mfma_f32_32x32x16_bf16 v[112:127], v[178:181], v[130:133], v[112:127]
	v_mfma_f32_32x32x16_bf16 v[96:111], v[182:185], v[130:133], v[96:111]
	s_add_i32 s2, s39, -1
	s_mul_i32 s2, s2, s62
	s_lshl_b32 s72, s2, 6
	s_lshl_b64 s[2:3], s[72:73], 1
	s_add_u32 s12, s10, s2
	s_addc_u32 s13, s11, s3
	s_add_u32 s2, s8, s2
	s_addc_u32 s3, s9, s3
	global_load_dwordx4 v[178:181], v128, s[12:13]
	global_load_dwordx4 v[182:185], v198, s[12:13]
	global_load_dwordx4 v[186:189], v128, s[2:3]
	global_load_dwordx4 v[190:193], v198, s[2:3]
	ds_read_b64_tr_b16 v[76:77], v209 offset:0
	ds_read_b64_tr_b16 v[78:79], v209 offset:0x800
	ds_read_b64_tr_b16 v[80:81], v209 offset:0x1000
	ds_read_b64_tr_b16 v[82:83], v209 offset:0x1800
	ds_read_b64_tr_b16 v[84:85], v209 offset:0x2000
	ds_read_b64_tr_b16 v[86:87], v209 offset:0x2800
	ds_read_b64_tr_b16 v[92:93], v209 offset:0x3000
	ds_read_b64_tr_b16 v[94:95], v209 offset:0x3800
	s_waitcnt lgkmcnt(0)
	s_nop 0
	v_mfma_f32_32x32x16_bf16 v[0:15], v[76:79], v[88:91], v[0:15]
	v_mfma_f32_32x32x16_bf16 v[0:15], v[80:83], v[72:75], v[0:15]
	v_mfma_f32_32x32x16_bf16 v[0:15], v[84:87], v[64:67], v[0:15]
	ds_read_b64_tr_b16 v[76:77], v209 offset:0x200
	ds_read_b64_tr_b16 v[78:79], v209 offset:0xa00
	ds_read_b64_tr_b16 v[80:81], v209 offset:0x1200
	v_mfma_f32_32x32x16_bf16 v[0:15], v[92:95], v[68:71], v[0:15]
	ds_read_b64_tr_b16 v[82:83], v209 offset:0x1a00
	ds_read_b64_tr_b16 v[84:85], v209 offset:0x2200
	ds_read_b64_tr_b16 v[86:87], v209 offset:0x2a00
	ds_read_b64_tr_b16 v[92:93], v209 offset:0x3200
	ds_read_b64_tr_b16 v[94:95], v209 offset:0x3a00
	s_waitcnt lgkmcnt(0)
	v_mfma_f32_32x32x16_bf16 v[48:63], v[76:79], v[88:91], v[48:63]
	v_mfma_f32_32x32x16_bf16 v[48:63], v[80:83], v[72:75], v[48:63]
	v_mfma_f32_32x32x16_bf16 v[48:63], v[84:87], v[64:67], v[48:63]
	ds_read_b64_tr_b16 v[76:77], v209 offset:0x400
	ds_read_b64_tr_b16 v[78:79], v209 offset:0xc00
	ds_read_b64_tr_b16 v[80:81], v209 offset:0x1400
	ds_read_b64_tr_b16 v[82:83], v209 offset:0x1c00
	v_mfma_f32_32x32x16_bf16 v[48:63], v[92:95], v[68:71], v[48:63]
	ds_read_b64_tr_b16 v[84:85], v209 offset:0x2400
	ds_read_b64_tr_b16 v[86:87], v209 offset:0x2c00
	ds_read_b64_tr_b16 v[92:93], v209 offset:0x3400
	ds_read_b64_tr_b16 v[94:95], v209 offset:0x3c00
	s_waitcnt lgkmcnt(0)
	v_mfma_f32_32x32x16_bf16 v[32:47], v[76:79], v[88:91], v[32:47]
	ds_read_b64_tr_b16 v[76:77], v209 offset:0x600
	ds_read_b64_tr_b16 v[78:79], v209 offset:0xe00
	v_exp_f32_e32 v234, v104
	v_exp_f32_e32 v235, v105
	v_exp_f32_e32 v236, v106
	v_exp_f32_e32 v237, v107
	v_exp_f32_e32 v238, v108
	v_exp_f32_e32 v239, v109
	v_exp_f32_e32 v231, v110
	v_exp_f32_e32 v249, v111
	v_mfma_f32_32x32x16_bf16 v[32:47], v[80:83], v[72:75], v[32:47]
	v_exp_f32_e32 v80, v112
	v_exp_f32_e32 v81, v113
	v_exp_f32_e32 v82, v114
	v_exp_f32_e32 v83, v115
	v_mfma_f32_32x32x16_bf16 v[32:47], v[84:87], v[64:67], v[32:47]
	v_exp_f32_e32 v84, v116
	v_exp_f32_e32 v85, v117
	v_exp_f32_e32 v86, v118
	v_exp_f32_e32 v87, v119
	v_exp_f32_e32 v112, v96
	v_exp_f32_e32 v113, v97
	v_exp_f32_e32 v114, v98
	v_exp_f32_e32 v115, v99
	v_exp_f32_e32 v116, v100
	v_exp_f32_e32 v117, v101
	v_exp_f32_e32 v118, v102
	v_exp_f32_e32 v119, v103
	v_mfma_f32_32x32x16_bf16 v[32:47], v[92:95], v[68:71], v[32:47]
	ds_read_b64_tr_b16 v[92:93], v209 offset:0x1600
	ds_read_b64_tr_b16 v[94:95], v209 offset:0x1e00
	ds_read_b64_tr_b16 v[96:97], v209 offset:0x2600
	ds_read_b64_tr_b16 v[98:99], v209 offset:0x2e00
	ds_read_b64_tr_b16 v[100:101], v209 offset:0x3600
	ds_read_b64_tr_b16 v[102:103], v209 offset:0x3e00
	s_waitcnt lgkmcnt(0)
	v_mfma_f32_32x32x16_bf16 v[16:31], v[76:79], v[88:91], v[16:31]
	v_exp_f32_e32 v88, v120
	v_exp_f32_e32 v89, v121
	v_exp_f32_e32 v90, v122
	v_exp_f32_e32 v91, v123
	v_mfma_f32_32x32x16_bf16 v[16:31], v[92:95], v[72:75], v[16:31]
	v_exp_f32_e32 v92, v124
	v_exp_f32_e32 v93, v125
	v_exp_f32_e32 v94, v126
	v_exp_f32_e32 v95, v127
	s_barrier
	v_mfma_f32_32x32x16_bf16 v[16:31], v[96:99], v[64:67], v[16:31]
	s_waitcnt vmcnt(4)
	ds_write_b128 v212, v[162:165]
	ds_write_b128 v213, v[166:169]
	ds_write_b128 v214, v[170:173] offset:32768
	ds_write_b128 v215, v[174:177] offset:32768
	v_mfma_f32_32x32x16_bf16 v[16:31], v[100:103], v[68:71], v[16:31]
.LBB0_883:
	s_waitcnt lgkmcnt(0)
	s_barrier
	ds_read_b128 v[64:67], v216 offset:32768
	ds_read_b128 v[68:71], v216 offset:40960
	ds_read_b128 v[162:165], v218 offset:32768
	ds_read_b128 v[166:169], v218 offset:40960
	ds_read_b128 v[240:243], v219 offset:32768
	ds_read_b128 v[244:247], v219 offset:40960
	v_add_f32_e32 v120, v80, v81
	v_add_f32_e32 v121, v88, v89
	v_add_f32_e32 v122, v112, v113
	v_add_f32_e32 v123, v234, v235
	v_add_f32_e32 v120, v82, v120
	v_add_f32_e32 v121, v90, v121
	v_add_f32_e32 v122, v114, v122
	s_waitcnt lgkmcnt(4)
	v_mfma_f32_32x32x16_bf16 v[96:111], v[64:67], v[138:141], 0
	v_mfma_f32_32x32x16_bf16 v[64:79], v[68:71], v[138:141], 0
	v_add_f32_e32 v123, v236, v123
	v_add_f32_e32 v120, v83, v120
	v_add_f32_e32 v121, v91, v121
	v_add_f32_e32 v122, v115, v122
	v_add_f32_e32 v123, v237, v123
	v_add_f32_e32 v120, v84, v120
	v_add_f32_e32 v121, v92, v121
	s_waitcnt lgkmcnt(2)
	v_mfma_f32_32x32x16_bf16 v[96:111], v[162:165], v[154:157], v[96:111]
	v_mfma_f32_32x32x16_bf16 v[64:79], v[166:169], v[154:157], v[64:79]
	ds_read_b128 v[162:165], v220 offset:32768
	ds_read_b128 v[166:169], v220 offset:40960
	v_add_f32_e32 v122, v116, v122
	v_add_f32_e32 v123, v238, v123
	v_add_f32_e32 v120, v85, v120
	v_add_f32_e32 v121, v93, v121
	v_add_f32_e32 v122, v117, v122
	v_add_f32_e32 v123, v239, v123
	v_add_f32_e32 v120, v86, v120
	s_waitcnt lgkmcnt(2)
	v_mfma_f32_32x32x16_bf16 v[96:111], v[240:243], v[158:161], v[96:111]
	v_mfma_f32_32x32x16_bf16 v[64:79], v[244:247], v[158:161], v[64:79]
	ds_read_b128 v[240:243], v221 offset:32768
	ds_read_b128 v[244:247], v221 offset:40960
	v_add_f32_e32 v121, v94, v121
	v_add_f32_e32 v122, v118, v122
	v_add_f32_e32 v123, v231, v123
	v_add_f32_e32 v120, v87, v120
	v_add_f32_e32 v121, v95, v121
	v_add_f32_e32 v122, v119, v122
	v_add_f32_e32 v123, v249, v123
	s_waitcnt lgkmcnt(2)
	v_mfma_f32_32x32x16_bf16 v[96:111], v[162:165], v[150:153], v[96:111]
	v_mfma_f32_32x32x16_bf16 v[64:79], v[166:169], v[150:153], v[64:79]
	ds_read_b128 v[162:165], v222 offset:32768
	ds_read_b128 v[166:169], v222 offset:40960
	v_add_f32_e32 v120, v121, v120
	v_add_f32_e32 v121, v123, v122
	v_add_f32_e32 v229, v120, v121
	v_cvt_pk_bf16_f32 v124, v80, v81
	v_cvt_pk_bf16_f32 v125, v82, v83
	v_cvt_pk_bf16_f32 v126, v84, v85
	s_waitcnt lgkmcnt(2)
	v_mfma_f32_32x32x16_bf16 v[96:111], v[240:243], v[146:149], v[96:111]
	v_mfma_f32_32x32x16_bf16 v[64:79], v[244:247], v[146:149], v[64:79]
	ds_read_b128 v[240:243], v224 offset:32768
	ds_read_b128 v[244:247], v224 offset:40960
	v_cvt_pk_bf16_f32 v127, v86, v87
	v_cvt_pk_bf16_f32 v120, v88, v89
	v_cvt_pk_bf16_f32 v121, v90, v91
	v_cvt_pk_bf16_f32 v122, v92, v93
	v_cvt_pk_bf16_f32 v123, v94, v95
	v_cvt_pk_bf16_f32 v112, v112, v113
	v_cvt_pk_bf16_f32 v113, v114, v115
	s_waitcnt lgkmcnt(2)
	v_mfma_f32_32x32x16_bf16 v[96:111], v[162:165], v[142:145], v[96:111]
	v_mfma_f32_32x32x16_bf16 v[64:79], v[166:169], v[142:145], v[64:79]
	ds_read_b128 v[162:165], v223 offset:32768
	ds_read_b128 v[166:169], v223 offset:40960
	v_cvt_pk_bf16_f32 v114, v116, v117
	v_cvt_pk_bf16_f32 v115, v118, v119
	v_cvt_pk_bf16_f32 v116, v234, v235
	v_cvt_pk_bf16_f32 v117, v236, v237
	v_cvt_pk_bf16_f32 v118, v238, v239
	v_cvt_pk_bf16_f32 v119, v231, v249
	s_waitcnt lgkmcnt(2)
	v_mfma_f32_32x32x16_bf16 v[96:111], v[240:243], v[134:137], v[96:111]
	v_mfma_f32_32x32x16_bf16 v[64:79], v[244:247], v[134:137], v[64:79]
	s_waitcnt lgkmcnt(0)
	v_mfma_f32_32x32x16_bf16 v[96:111], v[162:165], v[130:133], v[96:111]
	v_mfma_f32_32x32x16_bf16 v[64:79], v[166:169], v[130:133], v[64:79]
	s_min_i32 s2, s39, s14
	s_mul_i32 s2, s2, s62
	s_lshl_b32 s72, s2, 6
	s_lshl_b64 s[2:3], s[72:73], 1
	s_add_u32 s12, s10, s2
	s_addc_u32 s13, s11, s3
	s_add_u32 s2, s8, s2
	s_addc_u32 s3, s9, s3
	global_load_dwordx4 v[162:165], v128, s[12:13]
	global_load_dwordx4 v[166:169], v198, s[12:13]
	global_load_dwordx4 v[170:173], v128, s[2:3]
	global_load_dwordx4 v[174:177], v198, s[2:3]
	ds_read_b64_tr_b16 v[80:81], v211 offset:0
	ds_read_b64_tr_b16 v[82:83], v211 offset:0x800
	ds_read_b64_tr_b16 v[84:85], v211 offset:0x1000
	ds_read_b64_tr_b16 v[86:87], v211 offset:0x1800
	ds_read_b64_tr_b16 v[88:89], v211 offset:0x2000
	ds_read_b64_tr_b16 v[90:91], v211 offset:0x2800
	ds_read_b64_tr_b16 v[92:93], v211 offset:0x3000
	ds_read_b64_tr_b16 v[94:95], v211 offset:0x3800
	s_waitcnt lgkmcnt(0)
	s_nop 0
	v_mfma_f32_32x32x16_bf16 v[0:15], v[80:83], v[124:127], v[0:15]
	v_mfma_f32_32x32x16_bf16 v[0:15], v[84:87], v[120:123], v[0:15]
	v_mfma_f32_32x32x16_bf16 v[0:15], v[88:91], v[112:115], v[0:15]
	ds_read_b64_tr_b16 v[80:81], v211 offset:0x200
	ds_read_b64_tr_b16 v[82:83], v211 offset:0xa00
	ds_read_b64_tr_b16 v[84:85], v211 offset:0x1200
	v_mfma_f32_32x32x16_bf16 v[0:15], v[92:95], v[116:119], v[0:15]
	ds_read_b64_tr_b16 v[86:87], v211 offset:0x1a00
	ds_read_b64_tr_b16 v[88:89], v211 offset:0x2200
	ds_read_b64_tr_b16 v[90:91], v211 offset:0x2a00
	ds_read_b64_tr_b16 v[92:93], v211 offset:0x3200
	ds_read_b64_tr_b16 v[94:95], v211 offset:0x3a00
	s_waitcnt lgkmcnt(0)
	v_mfma_f32_32x32x16_bf16 v[48:63], v[80:83], v[124:127], v[48:63]
	v_mfma_f32_32x32x16_bf16 v[48:63], v[84:87], v[120:123], v[48:63]
	v_mfma_f32_32x32x16_bf16 v[48:63], v[88:91], v[112:115], v[48:63]
	ds_read_b64_tr_b16 v[80:81], v211 offset:0x400
	ds_read_b64_tr_b16 v[82:83], v211 offset:0xc00
	ds_read_b64_tr_b16 v[84:85], v211 offset:0x1400
	ds_read_b64_tr_b16 v[86:87], v211 offset:0x1c00
	v_mfma_f32_32x32x16_bf16 v[48:63], v[92:95], v[116:119], v[48:63]
	ds_read_b64_tr_b16 v[88:89], v211 offset:0x2400
	ds_read_b64_tr_b16 v[90:91], v211 offset:0x2c00
	ds_read_b64_tr_b16 v[92:93], v211 offset:0x3400
	ds_read_b64_tr_b16 v[94:95], v211 offset:0x3c00
	s_waitcnt lgkmcnt(0)
	v_mfma_f32_32x32x16_bf16 v[32:47], v[80:83], v[124:127], v[32:47]
	v_exp_f32_e32 v80, v64
	v_exp_f32_e32 v81, v65
	v_exp_f32_e32 v64, v96
	v_exp_f32_e32 v65, v97
	v_exp_f32_e32 v82, v66
	v_exp_f32_e32 v83, v67
	v_exp_f32_e32 v66, v98
	v_exp_f32_e32 v67, v99
	v_mfma_f32_32x32x16_bf16 v[32:47], v[84:87], v[120:123], v[32:47]
	v_exp_f32_e32 v84, v68
	v_exp_f32_e32 v85, v69
	v_exp_f32_e32 v68, v100
	v_exp_f32_e32 v69, v101
	v_exp_f32_e32 v86, v70
	v_exp_f32_e32 v87, v71
	v_exp_f32_e32 v70, v102
	v_exp_f32_e32 v71, v103
	v_mfma_f32_32x32x16_bf16 v[32:47], v[88:91], v[112:115], v[32:47]
	v_exp_f32_e32 v194, v72
	v_exp_f32_e32 v195, v73
	ds_read_b64_tr_b16 v[72:73], v211 offset:0x600
	v_exp_f32_e32 v196, v74
	v_exp_f32_e32 v197, v75
	ds_read_b64_tr_b16 v[74:75], v211 offset:0xe00
	v_mfma_f32_32x32x16_bf16 v[32:47], v[92:95], v[116:119], v[32:47]
	v_exp_f32_e32 v92, v76
	v_exp_f32_e32 v93, v77
	ds_read_b64_tr_b16 v[76:77], v211 offset:0x1600
	v_exp_f32_e32 v94, v78
	v_exp_f32_e32 v95, v79
	ds_read_b64_tr_b16 v[78:79], v211 offset:0x1e00
	ds_read_b64_tr_b16 v[96:97], v211 offset:0x2600
	ds_read_b64_tr_b16 v[98:99], v211 offset:0x2e00
	ds_read_b64_tr_b16 v[100:101], v211 offset:0x3600
	ds_read_b64_tr_b16 v[102:103], v211 offset:0x3e00
	s_waitcnt lgkmcnt(0)
	v_mfma_f32_32x32x16_bf16 v[16:31], v[72:75], v[124:127], v[16:31]
	v_exp_f32_e32 v72, v104
	v_exp_f32_e32 v73, v105
	v_exp_f32_e32 v74, v106
	v_exp_f32_e32 v75, v107
	v_mfma_f32_32x32x16_bf16 v[16:31], v[76:79], v[120:123], v[16:31]
	v_exp_f32_e32 v76, v108
	v_exp_f32_e32 v77, v109
	v_exp_f32_e32 v78, v110
	v_exp_f32_e32 v79, v111
	s_barrier
	v_mfma_f32_32x32x16_bf16 v[16:31], v[96:99], v[112:115], v[16:31]
	s_waitcnt vmcnt(4)
	ds_write_b128 v212, v[178:181] offset:16384
	ds_write_b128 v213, v[182:185] offset:16384
	ds_write_b128 v214, v[186:189] offset:49152
	ds_write_b128 v215, v[190:193] offset:49152
	v_mfma_f32_32x32x16_bf16 v[16:31], v[100:103], v[116:119], v[16:31]

.LBB0_967:
	s_and_b64 s[2:3], s[86:87], exec
	s_cselect_b32 s2, s79, s38
	s_lshr_b32 s2, s2, 12
	s_and_b32 s72, s2, 0x80000
	s_and_b64 s[2:3], s[86:87], exec
	s_cselect_b32 s15, s83, s19
	s_cselect_b32 s17, s82, s18
	s_cselect_b32 s67, s23, s85
	s_cselect_b32 s3, s22, s84
	s_cmp_lt_i32 s38, 0
	s_cselect_b64 s[96:97], -1, 0
	s_add_u32 s24, s18, 0x80
	s_addc_u32 s25, s19, 0
	v_lshl_add_u64 v[0:1], s[24:25], 0, v[202:203]
	v_lshl_add_u64 v[206:207], v[0:1], 0, s[20:21]
	v_lshl_add_u64 v[0:1], s[24:25], 0, v[204:205]
	v_mov_b32_e32 v128, v129
	v_lshl_add_u64 v[208:209], v[0:1], 0, s[20:21]
	s_add_u32 s2, s84, 0x100
	s_waitcnt vmcnt(0)
	v_mov_b32_e32 v130, v129
	v_mov_b32_e32 v131, v129
	v_mov_b32_e32 v64, 0
	v_mov_b64_e32 v[0:1], v[128:129]
	v_mov_b64_e32 v[4:5], v[128:129]
	v_mov_b64_e32 v[16:17], v[128:129]
	v_mov_b64_e32 v[20:21], v[128:129]
	v_mov_b64_e32 v[32:33], v[128:129]
	v_mov_b64_e32 v[36:37], v[128:129]
	v_mov_b64_e32 v[48:49], v[128:129]
	v_mov_b64_e32 v[52:53], v[128:129]
	v_mov_b64_e32 v[8:9], v[128:129]
	v_mov_b64_e32 v[12:13], v[128:129]
	v_mov_b64_e32 v[24:25], v[128:129]
	v_mov_b64_e32 v[28:29], v[128:129]
	v_mov_b64_e32 v[40:41], v[128:129]
	v_mov_b64_e32 v[44:45], v[128:129]
	v_mov_b64_e32 v[56:57], v[128:129]
	v_mov_b64_e32 v[60:61], v[128:129]
	s_addc_u32 s29, s85, 0
	s_mov_b32 s30, -2
	v_mov_b64_e32 v[2:3], v[130:131]
	v_mov_b64_e32 v[6:7], v[130:131]
	v_mov_b64_e32 v[18:19], v[130:131]
	v_mov_b64_e32 v[22:23], v[130:131]
	v_mov_b64_e32 v[34:35], v[130:131]
	v_mov_b64_e32 v[38:39], v[130:131]
	v_mov_b64_e32 v[50:51], v[130:131]
	v_mov_b64_e32 v[54:55], v[130:131]
	v_mov_b64_e32 v[10:11], v[130:131]
	v_mov_b64_e32 v[14:15], v[130:131]
	v_mov_b64_e32 v[26:27], v[130:131]
	v_mov_b64_e32 v[30:31], v[130:131]
	v_mov_b64_e32 v[42:43], v[130:131]
	v_mov_b64_e32 v[46:47], v[130:131]
	v_mov_b64_e32 v[58:59], v[130:131]
	v_mov_b64_e32 v[62:63], v[130:131]
	v_mov_b32_e32 v65, v64
	v_mov_b32_e32 v66, v64
	v_mov_b32_e32 v67, v64
	v_mov_b32_e32 v68, v64
	v_mov_b32_e32 v69, v64
	v_mov_b32_e32 v70, v64
	v_mov_b32_e32 v71, v64
	v_mov_b32_e32 v80, v64
	v_mov_b32_e32 v81, v64
	v_mov_b32_e32 v82, v64
	v_mov_b32_e32 v83, v64
	v_mov_b32_e32 v84, v64
	v_mov_b32_e32 v85, v64
	v_mov_b32_e32 v86, v64
	v_mov_b32_e32 v87, v64
	v_mov_b32_e32 v96, v64
	v_mov_b32_e32 v97, v64
	v_mov_b32_e32 v98, v64
	v_mov_b32_e32 v99, v64
	v_mov_b32_e32 v100, v64
	v_mov_b32_e32 v101, v64
	v_mov_b32_e32 v102, v64
	v_mov_b32_e32 v103, v64
	v_mov_b32_e32 v124, v64
	v_mov_b32_e32 v125, v64
	v_mov_b32_e32 v126, v64
	v_mov_b32_e32 v127, v64
	v_mov_b32_e32 v134, v64
	v_mov_b32_e32 v135, v64
	v_mov_b32_e32 v136, v64
	v_mov_b32_e32 v137, v64
	v_mov_b32_e32 v72, v64
	v_mov_b32_e32 v73, v64
	v_mov_b32_e32 v74, v64
	v_mov_b32_e32 v75, v64
	v_mov_b32_e32 v76, v64
	v_mov_b32_e32 v77, v64
	v_mov_b32_e32 v78, v64
	v_mov_b32_e32 v79, v64
	v_mov_b32_e32 v88, v64
	v_mov_b32_e32 v89, v64
	v_mov_b32_e32 v90, v64
	v_mov_b32_e32 v91, v64
	v_mov_b32_e32 v92, v64
	v_mov_b32_e32 v93, v64
	v_mov_b32_e32 v94, v64
	v_mov_b32_e32 v95, v64
	v_mov_b32_e32 v112, v64
	v_mov_b32_e32 v113, v64
	v_mov_b32_e32 v114, v64
	v_mov_b32_e32 v115, v64
	v_mov_b32_e32 v120, v64
	v_mov_b32_e32 v121, v64
	v_mov_b32_e32 v122, v64
	v_mov_b32_e32 v123, v64
	v_mov_b32_e32 v138, v64
	v_mov_b32_e32 v139, v64
	v_mov_b32_e32 v140, v64
	v_mov_b32_e32 v141, v64
	v_mov_b32_e32 v142, v64
	v_mov_b32_e32 v143, v64
	v_mov_b32_e32 v144, v64
	v_mov_b32_e32 v145, v64
	s_branch .LBB0_969

.LBB0_1535:
	s_mov_b32 s16, s8
	s_waitcnt vmcnt(8)
	v_mov_b32_e32 v90, v69
	v_mov_b32_e32 v88, v71
	v_mov_b32_e32 v86, v72
	v_mov_b32_e32 v63, v74
	s_waitcnt vmcnt(6)
	v_mov_b32_e32 v61, v76
	s_waitcnt vmcnt(4)
	v_mov_b32_e32 v59, v77
	s_waitcnt vmcnt(2)
	v_mov_b32_e32 v57, v79
	s_waitcnt vmcnt(0)
	v_mov_b32_e32 v54, v83
	v_mov_b32_e32 v91, v68
	v_mov_b32_e32 v89, v70
	v_mov_b32_e32 v87, v73
	v_mov_b32_e32 v85, v75
	v_mov_b32_e32 v62, v78
	v_mov_b32_e32 v60, v80
	v_mov_b32_e32 v58, v81
	v_mov_b32_e32 v56, v82

.Lgqa_slow_881:
	ds_read_b128 v[96:99], v216 offset:49152
	ds_read_b128 v[100:103], v216 offset:57344
	ds_read_b128 v[178:181], v218 offset:49152
	ds_read_b128 v[182:185], v218 offset:57344
	v_exp_f32_e32 v80, v80
	v_exp_f32_e32 v81, v81
	s_waitcnt lgkmcnt(3)
	v_mfma_f32_32x32x16_bf16 v[112:127], v[96:99], v[138:141], 0
	v_exp_f32_e32 v82, v82
	v_exp_f32_e32 v83, v83
	v_exp_f32_e32 v84, v84
	v_exp_f32_e32 v92, v92
	v_exp_f32_e32 v85, v85
	v_exp_f32_e32 v93, v93
	v_exp_f32_e32 v86, v86
	s_waitcnt lgkmcnt(2)
	v_mfma_f32_32x32x16_bf16 v[96:111], v[100:103], v[138:141], 0
	v_exp_f32_e32 v94, v94
	v_exp_f32_e32 v87, v87
	v_exp_f32_e32 v95, v95
	s_waitcnt lgkmcnt(1)
	v_mfma_f32_32x32x16_bf16 v[112:127], v[178:181], v[154:157], v[112:127]
	s_waitcnt lgkmcnt(0)
	v_mfma_f32_32x32x16_bf16 v[96:111], v[182:185], v[154:157], v[96:111]
	ds_read_b128 v[178:181], v219 offset:49152
	ds_read_b128 v[182:185], v219 offset:57344
	s_waitcnt lgkmcnt(1)
	v_mfma_f32_32x32x16_bf16 v[112:127], v[178:181], v[158:161], v[112:127]
	s_waitcnt lgkmcnt(0)
	v_mfma_f32_32x32x16_bf16 v[96:111], v[182:185], v[158:161], v[96:111]
	ds_read_b128 v[178:181], v220 offset:49152
	ds_read_b128 v[182:185], v220 offset:57344
	s_waitcnt lgkmcnt(1)
	v_mfma_f32_32x32x16_bf16 v[112:127], v[178:181], v[150:153], v[112:127]
	s_waitcnt lgkmcnt(0)
	v_mfma_f32_32x32x16_bf16 v[96:111], v[182:185], v[150:153], v[96:111]
	ds_read_b128 v[178:181], v221 offset:49152
	ds_read_b128 v[182:185], v221 offset:57344
	s_waitcnt lgkmcnt(1)
	v_mfma_f32_32x32x16_bf16 v[112:127], v[178:181], v[146:149], v[112:127]
	s_waitcnt lgkmcnt(0)
	v_mfma_f32_32x32x16_bf16 v[96:111], v[182:185], v[146:149], v[96:111]
	ds_read_b128 v[178:181], v222 offset:49152
	ds_read_b128 v[182:185], v222 offset:57344
	s_waitcnt lgkmcnt(1)
	v_mfma_f32_32x32x16_bf16 v[112:127], v[178:181], v[142:145], v[112:127]
	s_waitcnt lgkmcnt(0)
	v_mfma_f32_32x32x16_bf16 v[96:111], v[182:185], v[142:145], v[96:111]
	ds_read_b128 v[178:181], v224 offset:49152
	ds_read_b128 v[182:185], v224 offset:57344
	s_waitcnt lgkmcnt(1)
	v_mfma_f32_32x32x16_bf16 v[112:127], v[178:181], v[134:137], v[112:127]
	s_waitcnt lgkmcnt(0)
	v_mfma_f32_32x32x16_bf16 v[96:111], v[182:185], v[134:137], v[96:111]
	ds_read_b128 v[178:181], v223 offset:49152
	ds_read_b128 v[182:185], v223 offset:57344
	s_waitcnt lgkmcnt(1)
	v_mfma_f32_32x32x16_bf16 v[112:127], v[178:181], v[130:133], v[112:127]
	v_exp_f32_e32 v178, v88
	v_exp_f32_e32 v179, v89
	v_exp_f32_e32 v180, v90
	v_exp_f32_e32 v181, v91
	v_add_f32_e32 v88, v64, v65
	v_add_f32_e32 v89, v72, v73
	v_add_f32_e32 v90, v80, v81
	v_add_f32_e32 v91, v178, v179
	v_add_f32_e32 v88, v66, v88
	v_add_f32_e32 v89, v74, v89
	v_add_f32_e32 v90, v82, v90
	v_add_f32_e32 v91, v180, v91
	v_add_f32_e32 v88, v67, v88
	v_add_f32_e32 v89, v75, v89
	v_add_f32_e32 v90, v83, v90
	v_add_f32_e32 v91, v181, v91
	v_add_f32_e32 v88, v68, v88
	v_add_f32_e32 v89, v76, v89
	v_add_f32_e32 v90, v84, v90
	v_add_f32_e32 v91, v92, v91
	v_add_f32_e32 v88, v69, v88
	v_add_f32_e32 v89, v77, v89
	v_add_f32_e32 v90, v85, v90
	v_add_f32_e32 v91, v93, v91
	v_add_f32_e32 v88, v70, v88
	v_add_f32_e32 v89, v78, v89
	v_add_f32_e32 v90, v86, v90
	v_add_f32_e32 v91, v94, v91
	v_add_f32_e32 v88, v71, v88
	v_add_f32_e32 v89, v79, v89
	v_add_f32_e32 v90, v87, v90
	v_add_f32_e32 v91, v95, v91
	v_add_f32_e32 v88, v89, v88
	v_add_f32_e32 v89, v91, v90
	v_add_f32_e32 v227, v88, v89
	v_mov_b32_e32 v228, v227
	v_cvt_pk_bf16_f32 v88, v64, v65
	v_cvt_pk_bf16_f32 v89, v66, v67
	v_cvt_pk_bf16_f32 v90, v68, v69
	v_cvt_pk_bf16_f32 v91, v70, v71
	s_nop 1
	v_permlane32_swap_b32_e32 v227, v228
	v_cvt_pk_bf16_f32 v72, v72, v73
	v_cvt_pk_bf16_f32 v73, v74, v75
	v_cvt_pk_bf16_f32 v74, v76, v77
	v_cvt_pk_bf16_f32 v75, v78, v79
	v_cvt_pk_bf16_f32 v64, v80, v81
	v_cvt_pk_bf16_f32 v65, v82, v83
	v_cvt_pk_bf16_f32 v66, v84, v85
	v_cvt_pk_bf16_f32 v67, v86, v87
	v_cvt_pk_bf16_f32 v68, v178, v179
	v_cvt_pk_bf16_f32 v69, v180, v181
	v_cvt_pk_bf16_f32 v70, v92, v93
	v_cvt_pk_bf16_f32 v71, v94, v95
	s_waitcnt lgkmcnt(0)
	v_mfma_f32_32x32x16_bf16 v[96:111], v[182:185], v[130:133], v[96:111]
	v_lshl_add_u64 v[76:77], v[200:201], 0, s[92:93]
	global_load_dwordx4 v[178:181], v[76:77], off
	v_lshl_add_u64 v[76:77], v[202:203], 0, s[92:93]
	global_load_dwordx4 v[182:185], v[76:77], off
	v_lshl_add_u64 v[76:77], v[204:205], 0, s[92:93]
	global_load_dwordx4 v[186:189], v[76:77], off
	v_lshl_add_u64 v[76:77], v[206:207], 0, s[92:93]
	global_load_dwordx4 v[190:193], v[76:77], off
	ds_read_b64_tr_b16 v[76:77], v209 offset:0
	ds_read_b64_tr_b16 v[78:79], v209 offset:0x800
	ds_read_b64_tr_b16 v[80:81], v209 offset:0x1000
	ds_read_b64_tr_b16 v[82:83], v209 offset:0x1800
	ds_read_b64_tr_b16 v[84:85], v209 offset:0x2000
	ds_read_b64_tr_b16 v[86:87], v209 offset:0x2800
	ds_read_b64_tr_b16 v[92:93], v209 offset:0x3000
	ds_read_b64_tr_b16 v[94:95], v209 offset:0x3800
	s_waitcnt lgkmcnt(0)
	s_nop 0
	v_mfma_f32_32x32x16_bf16 v[0:15], v[76:79], v[88:91], v[0:15]
	v_max_f32_e32 v76, v97, v97
	v_max_f32_e32 v77, v96, v96
	v_max_f32_e32 v76, v77, v76
	v_max3_f32 v77, v112, v113, v114
	v_max3_f32 v76, v76, v98, v99
	v_max3_f32 v77, v77, v115, v116
	v_max3_f32 v76, v76, v100, v101
	v_mfma_f32_32x32x16_bf16 v[0:15], v[80:83], v[72:75], v[0:15]
	v_max3_f32 v77, v77, v117, v118
	v_max3_f32 v76, v76, v102, v103
	v_max3_f32 v77, v77, v119, v120
	v_max3_f32 v76, v76, v104, v105
	v_max3_f32 v77, v77, v121, v122
	v_max3_f32 v76, v76, v106, v107
	v_max3_f32 v77, v77, v123, v124
	v_mfma_f32_32x32x16_bf16 v[0:15], v[84:87], v[64:67], v[0:15]
	v_max3_f32 v76, v76, v108, v109
	v_max3_f32 v77, v77, v125, v126
	v_max3_f32 v76, v76, v110, v111
	v_max3_f32 v194, v77, v127, v76
	ds_read_b64_tr_b16 v[76:77], v209 offset:0x200
	ds_read_b64_tr_b16 v[78:79], v209 offset:0xa00
	ds_read_b64_tr_b16 v[80:81], v209 offset:0x1200
	v_mfma_f32_32x32x16_bf16 v[0:15], v[92:95], v[68:71], v[0:15]
	ds_read_b64_tr_b16 v[82:83], v209 offset:0x1a00
	ds_read_b64_tr_b16 v[84:85], v209 offset:0x2200
	ds_read_b64_tr_b16 v[86:87], v209 offset:0x2a00
	ds_read_b64_tr_b16 v[92:93], v209 offset:0x3200
	ds_read_b64_tr_b16 v[94:95], v209 offset:0x3a00
	s_waitcnt lgkmcnt(0)
	v_mfma_f32_32x32x16_bf16 v[48:63], v[76:79], v[88:91], v[48:63]
	v_mov_b32_e32 v76, v194
	s_nop 1
	v_permlane32_swap_b32_e32 v194, v76
	v_max_f32_e32 v76, v76, v76
	v_max_f32_e32 v77, v194, v194
	v_max_f32_e32 v76, v77, v76
	v_sub_f32_e32 v77, v76, v226
	v_mfma_f32_32x32x16_bf16 v[48:63], v[80:83], v[72:75], v[48:63]
	v_cmp_ge_f32_e32 vcc, s31, v77
	v_max_f32_e32 v77, v226, v226
	v_max_f32_e32 v76, v77, v76
	v_sub_f32_e32 v77, v226, v76
	v_mul_f32_e32 v77, 0x3e0293ee, v77
	v_exp_f32_e32 v77, v77
	s_cmp_eq_u64 vcc, exec
	v_mfma_f32_32x32x16_bf16 v[48:63], v[84:87], v[64:67], v[48:63]
	s_cselect_b64 vcc, -1, 0
	v_cndmask_b32_e64 v210, v77, 1.0, vcc
	v_cndmask_b32_e32 v226, v76, v226, vcc
	ds_read_b64_tr_b16 v[76:77], v209 offset:0x400
	ds_read_b64_tr_b16 v[78:79], v209 offset:0xc00
	ds_read_b64_tr_b16 v[80:81], v209 offset:0x1400
	ds_read_b64_tr_b16 v[82:83], v209 offset:0x1c00
	v_mfma_f32_32x32x16_bf16 v[48:63], v[92:95], v[68:71], v[48:63]
	ds_read_b64_tr_b16 v[84:85], v209 offset:0x2400
	ds_read_b64_tr_b16 v[86:87], v209 offset:0x2c00
	ds_read_b64_tr_b16 v[92:93], v209 offset:0x3400
	ds_read_b64_tr_b16 v[94:95], v209 offset:0x3c00
	s_waitcnt lgkmcnt(0)
	v_mul_f32_e32 v208, 0xbe0293ee, v226
	v_fmamk_f32 v194, v112, 0x3e0293ee, v208
	v_fmamk_f32 v195, v113, 0x3e0293ee, v208
	v_fmamk_f32 v196, v114, 0x3e0293ee, v208
	v_fmamk_f32 v197, v115, 0x3e0293ee, v208
	v_fmamk_f32 v229, v116, 0x3e0293ee, v208
	v_fmamk_f32 v233, v117, 0x3e0293ee, v208
	v_fmamk_f32 v234, v118, 0x3e0293ee, v208
	v_fmamk_f32 v235, v119, 0x3e0293ee, v208
	v_fmamk_f32 v236, v120, 0x3e0293ee, v208
	v_fmamk_f32 v237, v121, 0x3e0293ee, v208
	v_fmamk_f32 v238, v122, 0x3e0293ee, v208
	v_fmamk_f32 v239, v123, 0x3e0293ee, v208
	v_fmamk_f32 v240, v124, 0x3e0293ee, v208
	v_fmamk_f32 v241, v125, 0x3e0293ee, v208
	v_fmamk_f32 v242, v126, 0x3e0293ee, v208
	v_fmamk_f32 v243, v127, 0x3e0293ee, v208
	v_mfma_f32_32x32x16_bf16 v[32:47], v[76:79], v[88:91], v[32:47]
	ds_read_b64_tr_b16 v[76:77], v209 offset:0x600
	ds_read_b64_tr_b16 v[78:79], v209 offset:0xe00
	v_fma_f32 v112, v96, s52, v208
	v_fma_f32 v113, v97, s52, v208
	v_fma_f32 v114, v98, s52, v208
	v_fma_f32 v115, v99, s52, v208
	v_fma_f32 v116, v100, s52, v208
	v_fma_f32 v117, v101, s52, v208
	v_pk_fma_f32 v[118:119], v[102:103], s[52:53], v[208:209] op_sel_hi:[1,0,0]
	v_pk_fma_f32 v[126:127], v[110:111], s[52:53], v[208:209] op_sel_hi:[1,0,0]
	v_mfma_f32_32x32x16_bf16 v[32:47], v[80:83], v[72:75], v[32:47]
	v_exp_f32_e32 v80, v194
	v_exp_f32_e32 v81, v195
	v_exp_f32_e32 v82, v196
	v_exp_f32_e32 v83, v197
	v_pk_fma_f32 v[124:125], v[108:109], s[52:53], v[208:209] op_sel_hi:[1,0,0]
	v_pk_fma_f32 v[122:123], v[106:107], s[52:53], v[208:209] op_sel_hi:[1,0,0]
	v_pk_fma_f32 v[120:121], v[104:105], s[52:53], v[208:209] op_sel_hi:[1,0,0]
	v_mfma_f32_32x32x16_bf16 v[32:47], v[84:87], v[64:67], v[32:47]
	v_exp_f32_e32 v84, v229
	v_exp_f32_e32 v85, v233
	v_exp_f32_e32 v86, v234
	v_exp_f32_e32 v87, v235
	v_mfma_f32_32x32x16_bf16 v[32:47], v[92:95], v[68:71], v[32:47]
	ds_read_b64_tr_b16 v[92:93], v209 offset:0x1600
	ds_read_b64_tr_b16 v[94:95], v209 offset:0x1e00
	ds_read_b64_tr_b16 v[96:97], v209 offset:0x2600
	ds_read_b64_tr_b16 v[98:99], v209 offset:0x2e00
	ds_read_b64_tr_b16 v[100:101], v209 offset:0x3600
	ds_read_b64_tr_b16 v[102:103], v209 offset:0x3e00
	s_waitcnt lgkmcnt(0)
	v_mfma_f32_32x32x16_bf16 v[16:31], v[76:79], v[88:91], v[16:31]
	v_exp_f32_e32 v88, v236
	v_exp_f32_e32 v89, v237
	v_exp_f32_e32 v90, v238
	v_exp_f32_e32 v91, v239
	v_cmp_gt_f32_e32 vcc, 1.0, v210
	v_mfma_f32_32x32x16_bf16 v[16:31], v[92:95], v[72:75], v[16:31]
	v_exp_f32_e32 v92, v240
	v_exp_f32_e32 v93, v241
	v_exp_f32_e32 v94, v242
	v_exp_f32_e32 v95, v243
	s_barrier
	v_mfma_f32_32x32x16_bf16 v[16:31], v[96:99], v[64:67], v[16:31]
	s_waitcnt vmcnt(4)
	ds_write_b128 v212, v[162:165]
	ds_write_b128 v213, v[166:169]
	ds_write_b128 v214, v[170:173] offset:32768
	ds_write_b128 v215, v[174:177] offset:32768
	v_mfma_f32_32x32x16_bf16 v[16:31], v[100:103], v[68:71], v[16:31]
	s_cbranch_vccz .Lgqa_slow_883
	v_pk_mul_f32 v[14:15], v[14:15], v[210:211] op_sel_hi:[1,0]
	v_pk_mul_f32 v[12:13], v[12:13], v[210:211] op_sel_hi:[1,0]
	v_pk_mul_f32 v[10:11], v[10:11], v[210:211] op_sel_hi:[1,0]
	v_pk_mul_f32 v[8:9], v[8:9], v[210:211] op_sel_hi:[1,0]
	v_pk_mul_f32 v[6:7], v[6:7], v[210:211] op_sel_hi:[1,0]
	v_pk_mul_f32 v[4:5], v[4:5], v[210:211] op_sel_hi:[1,0]
	v_pk_mul_f32 v[2:3], v[2:3], v[210:211] op_sel_hi:[1,0]
	v_pk_mul_f32 v[0:1], v[0:1], v[210:211] op_sel_hi:[1,0]
	v_pk_mul_f32 v[62:63], v[62:63], v[210:211] op_sel_hi:[1,0]
	v_pk_mul_f32 v[60:61], v[60:61], v[210:211] op_sel_hi:[1,0]
	v_pk_mul_f32 v[58:59], v[58:59], v[210:211] op_sel_hi:[1,0]
	v_pk_mul_f32 v[56:57], v[56:57], v[210:211] op_sel_hi:[1,0]
	v_pk_mul_f32 v[54:55], v[54:55], v[210:211] op_sel_hi:[1,0]
	v_pk_mul_f32 v[52:53], v[52:53], v[210:211] op_sel_hi:[1,0]
	v_pk_mul_f32 v[50:51], v[50:51], v[210:211] op_sel_hi:[1,0]
	v_pk_mul_f32 v[48:49], v[48:49], v[210:211] op_sel_hi:[1,0]
	v_pk_mul_f32 v[46:47], v[210:211], v[46:47] op_sel_hi:[0,1]
	v_pk_mul_f32 v[44:45], v[210:211], v[44:45] op_sel_hi:[0,1]
	v_pk_mul_f32 v[42:43], v[210:211], v[42:43] op_sel_hi:[0,1]
	v_pk_mul_f32 v[40:41], v[210:211], v[40:41] op_sel_hi:[0,1]
	v_pk_mul_f32 v[38:39], v[210:211], v[38:39] op_sel_hi:[0,1]
	v_pk_mul_f32 v[36:37], v[210:211], v[36:37] op_sel_hi:[0,1]
	v_pk_mul_f32 v[34:35], v[210:211], v[34:35] op_sel_hi:[0,1]
	v_pk_mul_f32 v[32:33], v[210:211], v[32:33] op_sel_hi:[0,1]
	v_pk_mul_f32 v[30:31], v[210:211], v[30:31] op_sel_hi:[0,1]
	v_pk_mul_f32 v[28:29], v[210:211], v[28:29] op_sel_hi:[0,1]
	v_pk_mul_f32 v[26:27], v[210:211], v[26:27] op_sel_hi:[0,1]
	v_pk_mul_f32 v[24:25], v[210:211], v[24:25] op_sel_hi:[0,1]
	v_pk_mul_f32 v[22:23], v[210:211], v[22:23] op_sel_hi:[0,1]
	v_pk_mul_f32 v[20:21], v[210:211], v[20:21] op_sel_hi:[0,1]
	v_pk_mul_f32 v[18:19], v[210:211], v[18:19] op_sel_hi:[0,1]
	v_pk_mul_f32 v[16:17], v[210:211], v[16:17] op_sel_hi:[0,1]
.Lgqa_slow_883:
	s_waitcnt lgkmcnt(0)
	s_barrier
	ds_read_b128 v[64:67], v216 offset:32768
	ds_read_b128 v[68:71], v216 offset:40960
	ds_read_b128 v[162:165], v218 offset:32768
	ds_read_b128 v[166:169], v218 offset:40960
	v_exp_f32_e32 v112, v112
	v_exp_f32_e32 v113, v113
	s_waitcnt lgkmcnt(3)
	v_mfma_f32_32x32x16_bf16 v[96:111], v[64:67], v[138:141], 0
	v_exp_f32_e32 v114, v114
	v_exp_f32_e32 v115, v115
	v_exp_f32_e32 v116, v116
	v_exp_f32_e32 v117, v117
	v_exp_f32_e32 v118, v118
	v_exp_f32_e32 v119, v119
	s_waitcnt lgkmcnt(2)
	v_mfma_f32_32x32x16_bf16 v[64:79], v[68:71], v[138:141], 0
	s_waitcnt lgkmcnt(1)
	v_mfma_f32_32x32x16_bf16 v[96:111], v[162:165], v[154:157], v[96:111]
	s_waitcnt lgkmcnt(0)
	v_mfma_f32_32x32x16_bf16 v[64:79], v[166:169], v[154:157], v[64:79]
	ds_read_b128 v[162:165], v219 offset:32768
	ds_read_b128 v[166:169], v219 offset:40960
	s_waitcnt lgkmcnt(1)
	v_mfma_f32_32x32x16_bf16 v[96:111], v[162:165], v[158:161], v[96:111]
	s_waitcnt lgkmcnt(0)
	v_mfma_f32_32x32x16_bf16 v[64:79], v[166:169], v[158:161], v[64:79]
	ds_read_b128 v[162:165], v220 offset:32768
	ds_read_b128 v[166:169], v220 offset:40960
	s_waitcnt lgkmcnt(1)
	v_mfma_f32_32x32x16_bf16 v[96:111], v[162:165], v[150:153], v[96:111]
	s_waitcnt lgkmcnt(0)
	v_mfma_f32_32x32x16_bf16 v[64:79], v[166:169], v[150:153], v[64:79]
	ds_read_b128 v[162:165], v221 offset:32768
	ds_read_b128 v[166:169], v221 offset:40960
	s_waitcnt lgkmcnt(1)
	v_mfma_f32_32x32x16_bf16 v[96:111], v[162:165], v[146:149], v[96:111]
	s_waitcnt lgkmcnt(0)
	v_mfma_f32_32x32x16_bf16 v[64:79], v[166:169], v[146:149], v[64:79]
	ds_read_b128 v[162:165], v222 offset:32768
	ds_read_b128 v[166:169], v222 offset:40960
	s_waitcnt lgkmcnt(1)
	v_mfma_f32_32x32x16_bf16 v[96:111], v[162:165], v[142:145], v[96:111]
	s_waitcnt lgkmcnt(0)
	v_mfma_f32_32x32x16_bf16 v[64:79], v[166:169], v[142:145], v[64:79]
	ds_read_b128 v[162:165], v224 offset:32768
	ds_read_b128 v[166:169], v224 offset:40960
	s_waitcnt lgkmcnt(1)
	v_mfma_f32_32x32x16_bf16 v[96:111], v[162:165], v[134:137], v[96:111]
	s_waitcnt lgkmcnt(0)
	v_mfma_f32_32x32x16_bf16 v[64:79], v[166:169], v[134:137], v[64:79]
	ds_read_b128 v[162:165], v223 offset:32768
	ds_read_b128 v[166:169], v223 offset:40960
	s_waitcnt lgkmcnt(1)
	v_mfma_f32_32x32x16_bf16 v[96:111], v[162:165], v[130:133], v[96:111]
	v_exp_f32_e32 v162, v120
	v_exp_f32_e32 v163, v121
	v_exp_f32_e32 v164, v122
	v_exp_f32_e32 v165, v123
	v_add_f32_e32 v120, v80, v81
	v_add_f32_e32 v121, v88, v89
	v_add_f32_e32 v122, v112, v113
	s_waitcnt lgkmcnt(0)
	v_mfma_f32_32x32x16_bf16 v[64:79], v[166:169], v[130:133], v[64:79]
	v_exp_f32_e32 v166, v124
	v_exp_f32_e32 v167, v125
	v_add_f32_e32 v123, v162, v163
	v_exp_f32_e32 v168, v126
	v_add_f32_e32 v120, v82, v120
	v_add_f32_e32 v121, v90, v121
	v_add_f32_e32 v122, v114, v122
	v_add_f32_e32 v123, v164, v123
	v_exp_f32_e32 v169, v127
	v_add_f32_e32 v120, v83, v120
	v_add_f32_e32 v121, v91, v121
	v_add_f32_e32 v122, v115, v122
	v_add_f32_e32 v123, v165, v123
	v_add_f32_e32 v120, v84, v120
	v_add_f32_e32 v121, v92, v121
	v_add_f32_e32 v122, v116, v122
	v_add_f32_e32 v123, v166, v123
	v_add_f32_e32 v120, v85, v120
	v_add_f32_e32 v121, v93, v121
	v_add_f32_e32 v122, v117, v122
	v_add_f32_e32 v123, v167, v123
	v_add_f32_e32 v120, v86, v120
	v_add_f32_e32 v121, v94, v121
	v_add_f32_e32 v122, v118, v122
	v_add_f32_e32 v123, v168, v123
	v_add_f32_e32 v120, v87, v120
	v_add_f32_e32 v121, v95, v121
	v_add_f32_e32 v122, v119, v122
	v_add_f32_e32 v123, v169, v123
	v_add_f32_e32 v120, v121, v120
	v_add_f32_e32 v121, v123, v122
	v_add_f32_e32 v229, v120, v121
	v_mov_b32_e32 v233, v229
	s_nop 1
	v_permlane32_swap_b32_e32 v229, v233
	v_cvt_pk_bf16_f32 v124, v80, v81
	v_cvt_pk_bf16_f32 v125, v82, v83
	v_cvt_pk_bf16_f32 v126, v84, v85
	v_cvt_pk_bf16_f32 v127, v86, v87
	v_cvt_pk_bf16_f32 v120, v88, v89
	v_cvt_pk_bf16_f32 v121, v90, v91
	v_cvt_pk_bf16_f32 v122, v92, v93
	v_cvt_pk_bf16_f32 v123, v94, v95
	v_cvt_pk_bf16_f32 v112, v112, v113
	v_cvt_pk_bf16_f32 v113, v114, v115
	v_cvt_pk_bf16_f32 v114, v116, v117
	v_cvt_pk_bf16_f32 v115, v118, v119
	v_cvt_pk_bf16_f32 v116, v162, v163
	v_cvt_pk_bf16_f32 v117, v164, v165
	v_cvt_pk_bf16_f32 v118, v166, v167
	v_cvt_pk_bf16_f32 v119, v168, v169
	s_min_i32 s2, s39, s14
	s_mul_i32 s2, s2, s62
	s_lshl_b32 s72, s2, 6
	s_lshl_b64 s[2:3], s[72:73], 1
	s_add_u32 s12, s10, s2
	s_addc_u32 s13, s11, s3
	s_add_u32 s2, s8, s2
	s_addc_u32 s3, s9, s3
	v_lshl_add_u64 v[80:81], s[12:13], 0, v[128:129]
	v_lshl_add_u64 v[82:83], s[12:13], 0, v[198:199]
	global_load_dwordx4 v[162:165], v[80:81], off
	global_load_dwordx4 v[166:169], v[82:83], off
	v_lshl_add_u64 v[80:81], s[2:3], 0, v[128:129]
	v_lshl_add_u64 v[82:83], s[2:3], 0, v[198:199]
	global_load_dwordx4 v[170:173], v[80:81], off
	global_load_dwordx4 v[174:177], v[82:83], off
	ds_read_b64_tr_b16 v[80:81], v211 offset:0
	ds_read_b64_tr_b16 v[82:83], v211 offset:0x800
	ds_read_b64_tr_b16 v[84:85], v211 offset:0x1000
	ds_read_b64_tr_b16 v[86:87], v211 offset:0x1800
	ds_read_b64_tr_b16 v[88:89], v211 offset:0x2000
	ds_read_b64_tr_b16 v[90:91], v211 offset:0x2800
	ds_read_b64_tr_b16 v[92:93], v211 offset:0x3000
	ds_read_b64_tr_b16 v[94:95], v211 offset:0x3800
	s_waitcnt lgkmcnt(0)
	s_nop 0
	v_mfma_f32_32x32x16_bf16 v[0:15], v[80:83], v[124:127], v[0:15]
	v_max_f32_e32 v80, v65, v65
	v_max_f32_e32 v81, v64, v64
	v_max_f32_e32 v80, v81, v80
	v_max3_f32 v81, v96, v97, v98
	v_max3_f32 v80, v80, v66, v67
	v_max3_f32 v81, v81, v99, v100
	v_max3_f32 v80, v80, v68, v69
	v_mfma_f32_32x32x16_bf16 v[0:15], v[84:87], v[120:123], v[0:15]
	v_max3_f32 v81, v81, v101, v102
	v_max3_f32 v80, v80, v70, v71
	v_max3_f32 v81, v81, v103, v104
	v_max3_f32 v80, v80, v72, v73
	v_max3_f32 v81, v81, v105, v106
	v_max3_f32 v80, v80, v74, v75
	v_max3_f32 v81, v81, v107, v108
	v_mfma_f32_32x32x16_bf16 v[0:15], v[88:91], v[112:115], v[0:15]
	v_max3_f32 v80, v80, v76, v77
	v_max3_f32 v81, v81, v109, v110
	v_max3_f32 v80, v80, v78, v79
	v_max3_f32 v194, v81, v111, v80
	ds_read_b64_tr_b16 v[80:81], v211 offset:0x200
	ds_read_b64_tr_b16 v[82:83], v211 offset:0xa00
	ds_read_b64_tr_b16 v[84:85], v211 offset:0x1200
	v_mfma_f32_32x32x16_bf16 v[0:15], v[92:95], v[116:119], v[0:15]
	ds_read_b64_tr_b16 v[86:87], v211 offset:0x1a00
	ds_read_b64_tr_b16 v[88:89], v211 offset:0x2200
	ds_read_b64_tr_b16 v[90:91], v211 offset:0x2a00
	ds_read_b64_tr_b16 v[92:93], v211 offset:0x3200
	ds_read_b64_tr_b16 v[94:95], v211 offset:0x3a00
	s_waitcnt lgkmcnt(0)
	v_mfma_f32_32x32x16_bf16 v[48:63], v[80:83], v[124:127], v[48:63]
	v_mov_b32_e32 v80, v194
	s_nop 1
	v_permlane32_swap_b32_e32 v194, v80
	v_max_f32_e32 v80, v80, v80
	v_max_f32_e32 v81, v194, v194
	v_max_f32_e32 v80, v81, v80
	v_sub_f32_e32 v81, v80, v226
	v_mfma_f32_32x32x16_bf16 v[48:63], v[84:87], v[120:123], v[48:63]
	v_cmp_ge_f32_e32 vcc, s31, v81
	v_max_f32_e32 v81, v226, v226
	v_max_f32_e32 v80, v81, v80
	v_sub_f32_e32 v81, v226, v80
	v_mul_f32_e32 v81, 0x3e0293ee, v81
	v_exp_f32_e32 v81, v81
	s_cmp_eq_u64 vcc, exec
	v_mfma_f32_32x32x16_bf16 v[48:63], v[88:91], v[112:115], v[48:63]
	s_cselect_b64 vcc, -1, 0
	v_cndmask_b32_e64 v208, v81, 1.0, vcc
	v_cndmask_b32_e32 v226, v80, v226, vcc
	ds_read_b64_tr_b16 v[80:81], v211 offset:0x400
	ds_read_b64_tr_b16 v[82:83], v211 offset:0xc00
	ds_read_b64_tr_b16 v[84:85], v211 offset:0x1400
	ds_read_b64_tr_b16 v[86:87], v211 offset:0x1c00
	v_mfma_f32_32x32x16_bf16 v[48:63], v[92:95], v[116:119], v[48:63]
	ds_read_b64_tr_b16 v[88:89], v211 offset:0x2400
	ds_read_b64_tr_b16 v[90:91], v211 offset:0x2c00
	ds_read_b64_tr_b16 v[92:93], v211 offset:0x3400
	ds_read_b64_tr_b16 v[94:95], v211 offset:0x3c00
	s_waitcnt lgkmcnt(0)
	v_mul_f32_e32 v234, 0xbe0293ee, v226
	v_fmamk_f32 v96, v96, 0x3e0293ee, v234
	v_fmamk_f32 v97, v97, 0x3e0293ee, v234
	v_fmamk_f32 v98, v98, 0x3e0293ee, v234
	v_fmamk_f32 v99, v99, 0x3e0293ee, v234
	v_fmamk_f32 v100, v100, 0x3e0293ee, v234
	v_fmamk_f32 v101, v101, 0x3e0293ee, v234
	v_fmamk_f32 v102, v102, 0x3e0293ee, v234
	v_fmamk_f32 v103, v103, 0x3e0293ee, v234
	v_fmamk_f32 v104, v104, 0x3e0293ee, v234
	v_fmamk_f32 v105, v105, 0x3e0293ee, v234
	v_fmamk_f32 v106, v106, 0x3e0293ee, v234
	v_fmamk_f32 v107, v107, 0x3e0293ee, v234
	v_fmamk_f32 v108, v108, 0x3e0293ee, v234
	v_fmamk_f32 v109, v109, 0x3e0293ee, v234
	v_fmamk_f32 v110, v110, 0x3e0293ee, v234
	v_fmamk_f32 v111, v111, 0x3e0293ee, v234
	v_mfma_f32_32x32x16_bf16 v[32:47], v[80:83], v[124:127], v[32:47]
	v_fma_f32 v80, v64, s52, v234
	v_fma_f32 v81, v65, s52, v234
	v_exp_f32_e32 v64, v96
	v_exp_f32_e32 v65, v97
	v_pk_fma_f32 v[82:83], v[66:67], s[52:53], v[234:235] op_sel_hi:[1,0,0]
	v_exp_f32_e32 v66, v98
	v_exp_f32_e32 v67, v99
	v_mfma_f32_32x32x16_bf16 v[32:47], v[84:87], v[120:123], v[32:47]
	v_fma_f32 v84, v68, s52, v234
	v_fma_f32 v85, v69, s52, v234
	v_exp_f32_e32 v68, v100
	v_exp_f32_e32 v69, v101
	v_pk_fma_f32 v[86:87], v[70:71], s[52:53], v[234:235] op_sel_hi:[1,0,0]
	v_exp_f32_e32 v70, v102
	v_exp_f32_e32 v71, v103
	v_mfma_f32_32x32x16_bf16 v[32:47], v[88:91], v[112:115], v[32:47]
	v_fma_f32 v88, v72, s52, v234
	v_fma_f32 v89, v73, s52, v234
	ds_read_b64_tr_b16 v[72:73], v211 offset:0x600
	v_fma_f32 v90, v74, s52, v234
	v_fma_f32 v91, v75, s52, v234
	ds_read_b64_tr_b16 v[74:75], v211 offset:0xe00
	v_mfma_f32_32x32x16_bf16 v[32:47], v[92:95], v[116:119], v[32:47]
	v_fma_f32 v92, v76, s52, v234
	v_fma_f32 v93, v77, s52, v234
	ds_read_b64_tr_b16 v[76:77], v211 offset:0x1600
	v_fma_f32 v94, v78, s52, v234
	v_fma_f32 v95, v79, s52, v234
	ds_read_b64_tr_b16 v[78:79], v211 offset:0x1e00
	ds_read_b64_tr_b16 v[96:97], v211 offset:0x2600
	ds_read_b64_tr_b16 v[98:99], v211 offset:0x2e00
	ds_read_b64_tr_b16 v[100:101], v211 offset:0x3600
	ds_read_b64_tr_b16 v[102:103], v211 offset:0x3e00
	s_waitcnt lgkmcnt(0)
	v_mfma_f32_32x32x16_bf16 v[16:31], v[72:75], v[124:127], v[16:31]
	v_exp_f32_e32 v72, v104
	v_exp_f32_e32 v73, v105
	v_exp_f32_e32 v74, v106
	v_exp_f32_e32 v75, v107
	v_cmp_gt_f32_e32 vcc, 1.0, v208
	v_mfma_f32_32x32x16_bf16 v[16:31], v[76:79], v[120:123], v[16:31]
	v_exp_f32_e32 v76, v108
	v_exp_f32_e32 v77, v109
	v_exp_f32_e32 v78, v110
	v_exp_f32_e32 v79, v111
	s_barrier
	v_mfma_f32_32x32x16_bf16 v[16:31], v[96:99], v[112:115], v[16:31]
	s_waitcnt vmcnt(4)
	ds_write_b128 v212, v[178:181] offset:16384
	ds_write_b128 v213, v[182:185] offset:16384
	ds_write_b128 v214, v[186:189] offset:49152
	ds_write_b128 v215, v[190:193] offset:49152
	v_mfma_f32_32x32x16_bf16 v[16:31], v[100:103], v[116:119], v[16:31]
	s_cbranch_vccz .Lgqa_slow_885
	v_pk_mul_f32 v[14:15], v[14:15], v[208:209] op_sel_hi:[1,0]
	v_pk_mul_f32 v[12:13], v[12:13], v[208:209] op_sel_hi:[1,0]
	v_pk_mul_f32 v[10:11], v[10:11], v[208:209] op_sel_hi:[1,0]
	v_pk_mul_f32 v[8:9], v[8:9], v[208:209] op_sel_hi:[1,0]
	v_pk_mul_f32 v[6:7], v[6:7], v[208:209] op_sel_hi:[1,0]
	v_pk_mul_f32 v[4:5], v[4:5], v[208:209] op_sel_hi:[1,0]
	v_pk_mul_f32 v[2:3], v[2:3], v[208:209] op_sel_hi:[1,0]
	v_pk_mul_f32 v[0:1], v[0:1], v[208:209] op_sel_hi:[1,0]
	v_pk_mul_f32 v[62:63], v[62:63], v[208:209] op_sel_hi:[1,0]
	v_pk_mul_f32 v[60:61], v[60:61], v[208:209] op_sel_hi:[1,0]
	v_pk_mul_f32 v[58:59], v[58:59], v[208:209] op_sel_hi:[1,0]
	v_pk_mul_f32 v[56:57], v[56:57], v[208:209] op_sel_hi:[1,0]
	v_pk_mul_f32 v[54:55], v[54:55], v[208:209] op_sel_hi:[1,0]
	v_pk_mul_f32 v[52:53], v[52:53], v[208:209] op_sel_hi:[1,0]
	v_pk_mul_f32 v[50:51], v[50:51], v[208:209] op_sel_hi:[1,0]
	v_pk_mul_f32 v[48:49], v[48:49], v[208:209] op_sel_hi:[1,0]
	v_pk_mul_f32 v[46:47], v[208:209], v[46:47] op_sel_hi:[0,1]
	v_pk_mul_f32 v[44:45], v[208:209], v[44:45] op_sel_hi:[0,1]
	v_pk_mul_f32 v[42:43], v[208:209], v[42:43] op_sel_hi:[0,1]
	v_pk_mul_f32 v[40:41], v[208:209], v[40:41] op_sel_hi:[0,1]
	v_pk_mul_f32 v[38:39], v[208:209], v[38:39] op_sel_hi:[0,1]
	v_pk_mul_f32 v[36:37], v[208:209], v[36:37] op_sel_hi:[0,1]
	v_pk_mul_f32 v[34:35], v[208:209], v[34:35] op_sel_hi:[0,1]
	v_pk_mul_f32 v[32:33], v[208:209], v[32:33] op_sel_hi:[0,1]
	v_pk_mul_f32 v[30:31], v[208:209], v[30:31] op_sel_hi:[0,1]
	v_pk_mul_f32 v[28:29], v[208:209], v[28:29] op_sel_hi:[0,1]
	v_pk_mul_f32 v[26:27], v[208:209], v[26:27] op_sel_hi:[0,1]
	v_pk_mul_f32 v[24:25], v[208:209], v[24:25] op_sel_hi:[0,1]
	v_pk_mul_f32 v[22:23], v[208:209], v[22:23] op_sel_hi:[0,1]
	v_pk_mul_f32 v[20:21], v[208:209], v[20:21] op_sel_hi:[0,1]
	v_pk_mul_f32 v[18:19], v[208:209], v[18:19] op_sel_hi:[0,1]
	v_pk_mul_f32 v[16:17], v[208:209], v[16:17] op_sel_hi:[0,1]
